# baseline (speedup 1.0000x reference)
.LBB6_32:
	s_or_b64 exec, exec, s[2:3]
	s_add_i32 s0, 0, 0x18000
	v_add_u32_e32 v48, s0, v39
	s_mov_b64 s[0:1], 0x80
	v_readfirstlane_b32 s22, v48
	v_add_u32_e32 v49, 0x2000, v48
	v_lshl_add_u64 v[2:3], v[30:31], 0, s[0:1]
	s_mov_b32 m0, s22
	v_readfirstlane_b32 s21, v49
	v_add_u32_e32 v46, 0x8000, v35
	s_waitcnt vmcnt(4)
	s_barrier
	global_load_lds_dwordx4 v[2:3], off
	v_lshl_add_u64 v[2:3], v[32:33], 0, s[0:1]
	s_mov_b32 m0, s21
	v_readfirstlane_b32 s19, v46
	v_add_u32_e32 v47, 0xa000, v35
	s_add_i32 s2, 0, 0x1c000
	global_load_lds_dwordx4 v[2:3], off
	v_lshl_add_u64 v[2:3], v[26:27], 0, s[0:1]
	s_mov_b32 m0, s19
	v_readfirstlane_b32 s17, v47
	v_add_u32_e32 v38, s2, v39
	global_load_lds_dwordx4 v[2:3], off
	v_lshl_add_u64 v[2:3], v[28:29], 0, s[0:1]
	s_mov_b32 m0, s17
	v_readfirstlane_b32 s4, v38
	v_add_u32_e32 v40, 0x2000, v38
	global_load_lds_dwordx4 v[2:3], off
	v_lshl_add_u64 v[2:3], v[22:23], 0, s[0:1]
	s_mov_b32 m0, s4
	v_readfirstlane_b32 s3, v40
	global_load_lds_dwordx4 v[2:3], off
	v_lshl_add_u64 v[2:3], v[24:25], 0, s[0:1]
	s_mov_b32 m0, s3
	v_and_b32_e32 v4, 48, v0
	global_load_lds_dwordx4 v[2:3], off
	v_lshlrev_b32_e32 v2, 6, v0
	v_and_b32_e32 v3, 0x3c0, v2
	v_and_b32_e32 v5, 32, v103
	v_bitop3_b32 v6, v3, v5, v4 bitop3:0x36
	v_and_b32_e32 v2, 0x3000, v2
	v_add3_u32 v234, 0, v2, v6
	v_add_u32_e32 v2, 0x10000, v234
	v_add_u32_e32 v4, 0x10800, v234
	s_waitcnt vmcnt(6)
	s_barrier
	v_add_u32_e32 v3, 0x10400, v234
	ds_read_b128 v[10:13], v2
	ds_read_b128 v[14:17], v3
	v_add_u32_e32 v5, 0x10c00, v234
	ds_read_b128 v[50:53], v4
	ds_read_b128 v[54:57], v5
	v_and_b32_e32 v1, 0x2000, v1
	v_add3_u32 v1, 0, v1, v6
	v_add_u32_e32 v37, 0xc000, v35
	v_add_u32_e32 v39, 0xe000, v35
	v_readfirstlane_b32 s7, v37
	v_lshl_add_u64 v[6:7], v[18:19], 0, s[0:1]
	s_mov_b32 m0, s7
	v_readfirstlane_b32 s2, v39
	global_load_lds_dwordx4 v[6:7], off
	v_lshl_add_u64 v[6:7], v[20:21], 0, s[0:1]
	s_mov_b32 m0, s2
	s_nop 0
	global_load_lds_dwordx4 v[6:7], off
	ds_read_b128 v[42:45], v1
	ds_read_b128 v[58:61], v1 offset:1024
	ds_read_b128 v[62:65], v1 offset:2048
	ds_read_b128 v[66:69], v1 offset:3072
	ds_read_b128 v[70:73], v1 offset:4096
	ds_read_b128 v[74:77], v1 offset:5120
	ds_read_b128 v[78:81], v1 offset:6144
	ds_read_b128 v[82:85], v1 offset:7168
	s_waitcnt lgkmcnt(8)
	s_barrier
	s_waitcnt lgkmcnt(0)
	s_setprio 1
	s_waitcnt lgkmcnt(0)
	v_mfma_f32_16x16x32_f16 v[6:9], v[10:13], v[42:45], 0
	v_mfma_f32_16x16x32_f16 v[86:89], v[14:17], v[58:61], v[6:9]
	v_mfma_f32_16x16x32_f16 v[6:9], v[50:53], v[42:45], 0
	v_mfma_f32_16x16x32_f16 v[90:93], v[54:57], v[58:61], v[6:9]
	v_mfma_f32_16x16x32_f16 v[6:9], v[10:13], v[62:65], 0
	v_mfma_f32_16x16x32_f16 v[94:97], v[14:17], v[66:69], v[6:9]
	v_mfma_f32_16x16x32_f16 v[6:9], v[50:53], v[62:65], 0
	v_mfma_f32_16x16x32_f16 v[98:101], v[54:57], v[66:69], v[6:9]
	v_mfma_f32_16x16x32_f16 v[6:9], v[10:13], v[70:73], 0
	v_mfma_f32_16x16x32_f16 v[102:105], v[14:17], v[74:77], v[6:9]
	v_mfma_f32_16x16x32_f16 v[6:9], v[50:53], v[70:73], 0
	v_mfma_f32_16x16x32_f16 v[106:109], v[54:57], v[74:77], v[6:9]
	v_mfma_f32_16x16x32_f16 v[6:9], v[10:13], v[78:81], 0
	v_mfma_f32_16x16x32_f16 v[110:113], v[14:17], v[82:85], v[6:9]
	v_mfma_f32_16x16x32_f16 v[6:9], v[50:53], v[78:81], 0
	v_mfma_f32_16x16x32_f16 v[114:117], v[54:57], v[82:85], v[6:9]
	s_setprio 0
	s_barrier
	s_mov_b64 s[0:1], 0x100
	v_readfirstlane_b32 s15, v36
	v_add_u32_e32 v41, 0x2000, v36
	s_nop 1
	v_add_u32_e32 v6, 0x14000, v234
	v_add_u32_e32 v8, 0x14800, v234
	v_lshl_add_u64 v[134:135], v[30:31], 0, s[0:1]
	s_mov_b32 m0, s15
	v_readfirstlane_b32 s5, v41
	v_add_u32_e32 v7, 0x14400, v234
	ds_read_b128 v[118:121], v6
	ds_read_b128 v[122:125], v7
	v_add_u32_e32 v9, 0x14c00, v234
	ds_read_b128 v[126:129], v8
	ds_read_b128 v[130:133], v9
	global_load_lds_dwordx4 v[134:135], off
	v_lshl_add_u64 v[134:135], v[32:33], 0, s[0:1]
	s_mov_b32 m0, s5
	s_nop 0
	global_load_lds_dwordx4 v[134:135], off
	s_barrier
	s_waitcnt lgkmcnt(0)
	s_setprio 1
	s_waitcnt lgkmcnt(0)
	v_mfma_f32_16x16x32_f16 v[134:137], v[118:121], v[42:45], 0
	v_mfma_f32_16x16x32_f16 v[42:45], v[126:129], v[42:45], 0
	v_mfma_f32_16x16x32_f16 v[134:137], v[122:125], v[58:61], v[134:137]
	v_mfma_f32_16x16x32_f16 v[58:61], v[130:133], v[58:61], v[42:45]
	v_mfma_f32_16x16x32_f16 v[42:45], v[118:121], v[62:65], 0
	v_mfma_f32_16x16x32_f16 v[138:141], v[122:125], v[66:69], v[42:45]
	v_mfma_f32_16x16x32_f16 v[42:45], v[126:129], v[62:65], 0
	v_mfma_f32_16x16x32_f16 v[62:65], v[130:133], v[66:69], v[42:45]
	v_mfma_f32_16x16x32_f16 v[42:45], v[118:121], v[70:73], 0
	v_mfma_f32_16x16x32_f16 v[66:69], v[122:125], v[74:77], v[42:45]
	v_mfma_f32_16x16x32_f16 v[42:45], v[126:129], v[70:73], 0
	v_mfma_f32_16x16x32_f16 v[70:73], v[130:133], v[74:77], v[42:45]
	v_mfma_f32_16x16x32_f16 v[42:45], v[118:121], v[78:81], 0
	v_mfma_f32_16x16x32_f16 v[74:77], v[122:125], v[82:85], v[42:45]
	v_mfma_f32_16x16x32_f16 v[42:45], v[126:129], v[78:81], 0
	v_mfma_f32_16x16x32_f16 v[78:81], v[130:133], v[82:85], v[42:45]
	s_setprio 0
	v_readfirstlane_b32 s16, v35
	s_nop 4
	v_lshl_add_u64 v[42:43], v[26:27], 0, s[0:1]
	s_mov_b32 m0, s16
	s_barrier
	ds_read_b128 v[82:85], v1 offset:16384
	ds_read_b128 v[142:145], v1 offset:17408
	ds_read_b128 v[146:149], v1 offset:18432
	ds_read_b128 v[150:153], v1 offset:19456
	ds_read_b128 v[154:157], v1 offset:20480
	ds_read_b128 v[158:161], v1 offset:21504
	ds_read_b128 v[162:165], v1 offset:22528
	ds_read_b128 v[166:169], v1 offset:23552
	global_load_lds_dwordx4 v[42:43], off
	v_add_u32_e32 v42, 0x2000, v35
	v_lshl_add_u64 v[44:45], v[28:29], 0, s[0:1]
	v_readfirstlane_b32 s10, v42
	s_mov_b32 m0, s10
	s_nop 0
	global_load_lds_dwordx4 v[44:45], off
	s_barrier
	s_waitcnt lgkmcnt(0)
	s_setprio 1
	s_waitcnt lgkmcnt(0)
	v_mfma_f32_16x16x32_f16 v[170:173], v[10:13], v[82:85], 0
	v_mfma_f32_16x16x32_f16 v[178:181], v[10:13], v[146:149], 0
	v_mfma_f32_16x16x32_f16 v[186:189], v[10:13], v[154:157], 0
	v_mfma_f32_16x16x32_f16 v[10:13], v[10:13], v[162:165], 0
	v_mfma_f32_16x16x32_f16 v[174:177], v[50:53], v[82:85], 0
	v_mfma_f32_16x16x32_f16 v[182:185], v[50:53], v[146:149], 0
	v_mfma_f32_16x16x32_f16 v[190:193], v[50:53], v[154:157], 0
	v_mfma_f32_16x16x32_f16 v[194:197], v[14:17], v[166:169], v[10:13]
	v_mfma_f32_16x16x32_f16 v[10:13], v[50:53], v[162:165], 0
	v_mfma_f32_16x16x32_f16 v[170:173], v[14:17], v[142:145], v[170:173]
	v_mfma_f32_16x16x32_f16 v[174:177], v[54:57], v[142:145], v[174:177]
	v_mfma_f32_16x16x32_f16 v[178:181], v[14:17], v[150:153], v[178:181]
	v_mfma_f32_16x16x32_f16 v[182:185], v[54:57], v[150:153], v[182:185]
	v_mfma_f32_16x16x32_f16 v[186:189], v[14:17], v[158:161], v[186:189]
	v_mfma_f32_16x16x32_f16 v[190:193], v[54:57], v[158:161], v[190:193]
	v_mfma_f32_16x16x32_f16 v[50:53], v[54:57], v[166:169], v[10:13]
	s_setprio 0
	s_barrier
	v_readfirstlane_b32 s14, v34
	v_add_u32_e32 v43, 0x2000, v34
	v_lshl_add_u64 v[10:11], v[22:23], 0, s[0:1]
	s_mov_b32 m0, s14
	v_readfirstlane_b32 s11, v43
	global_load_lds_dwordx4 v[10:11], off
	v_lshl_add_u64 v[10:11], v[24:25], 0, s[0:1]
	s_mov_b32 m0, s11
	s_nop 0
	global_load_lds_dwordx4 v[10:11], off
	s_waitcnt vmcnt(6)
	s_barrier
	s_setprio 1
	v_mfma_f32_16x16x32_f16 v[10:13], v[118:121], v[82:85], 0
	v_mfma_f32_16x16x32_f16 v[54:57], v[122:125], v[142:145], v[10:13]
	v_mfma_f32_16x16x32_f16 v[10:13], v[126:129], v[82:85], 0
	v_mfma_f32_16x16x32_f16 v[82:85], v[130:133], v[142:145], v[10:13]
	v_mfma_f32_16x16x32_f16 v[10:13], v[118:121], v[146:149], 0
	v_mfma_f32_16x16x32_f16 v[142:145], v[122:125], v[150:153], v[10:13]
	v_mfma_f32_16x16x32_f16 v[10:13], v[126:129], v[146:149], 0
	v_mfma_f32_16x16x32_f16 v[146:149], v[130:133], v[150:153], v[10:13]
	v_mfma_f32_16x16x32_f16 v[10:13], v[118:121], v[154:157], 0
	v_mfma_f32_16x16x32_f16 v[150:153], v[122:125], v[158:161], v[10:13]
	v_mfma_f32_16x16x32_f16 v[10:13], v[126:129], v[154:157], 0
	v_mfma_f32_16x16x32_f16 v[154:157], v[130:133], v[158:161], v[10:13]
	v_mfma_f32_16x16x32_f16 v[10:13], v[118:121], v[162:165], 0
	v_mfma_f32_16x16x32_f16 v[118:121], v[122:125], v[166:169], v[10:13]
	v_mfma_f32_16x16x32_f16 v[10:13], v[126:129], v[162:165], 0
	v_mfma_f32_16x16x32_f16 v[122:125], v[130:133], v[166:169], v[10:13]
	s_setprio 0
	s_nop 5
	v_add_u32_e32 v10, 0x18000, v234
	v_add_u32_e32 v12, 0x18800, v234
	s_barrier
	v_add_u32_e32 v11, 0x18400, v234
	ds_read_b128 v[126:129], v10
	ds_read_b128 v[130:133], v11
	v_add_u32_e32 v13, 0x18c00, v234
	ds_read_b128 v[158:161], v12
	ds_read_b128 v[162:165], v13
	v_add_u32_e32 v44, 0x4000, v35
	v_add_u32_e32 v45, 0x6000, v35
	v_readfirstlane_b32 s20, v44
	v_lshl_add_u64 v[14:15], v[18:19], 0, s[0:1]
	s_mov_b32 m0, s20
	v_readfirstlane_b32 s18, v45
	ds_read_b128 v[166:169], v1 offset:32768
	ds_read_b128 v[198:201], v1 offset:33792
	ds_read_b128 v[202:205], v1 offset:34816
	ds_read_b128 v[206:209], v1 offset:35840
	ds_read_b128 v[210:213], v1 offset:36864
	ds_read_b128 v[214:217], v1 offset:37888
	ds_read_b128 v[218:221], v1 offset:38912
	ds_read_b128 v[222:225], v1 offset:39936
	global_load_lds_dwordx4 v[14:15], off
	v_lshl_add_u64 v[14:15], v[20:21], 0, s[0:1]
	s_mov_b32 m0, s18
	s_nop 0
	global_load_lds_dwordx4 v[14:15], off
	s_waitcnt lgkmcnt(8)
	s_barrier
	s_waitcnt lgkmcnt(0)
	s_setprio 1
	s_waitcnt lgkmcnt(0)
	v_mfma_f32_16x16x32_f16 v[14:17], v[126:129], v[166:169], v[86:89]
	v_mfma_f32_16x16x32_f16 v[86:89], v[130:133], v[198:201], v[14:17]
	v_mfma_f32_16x16x32_f16 v[14:17], v[158:161], v[166:169], v[90:93]
	v_mfma_f32_16x16x32_f16 v[90:93], v[162:165], v[198:201], v[14:17]
	v_mfma_f32_16x16x32_f16 v[14:17], v[126:129], v[202:205], v[94:97]
	v_mfma_f32_16x16x32_f16 v[94:97], v[130:133], v[206:209], v[14:17]
	v_mfma_f32_16x16x32_f16 v[14:17], v[158:161], v[202:205], v[98:101]
	v_mfma_f32_16x16x32_f16 v[98:101], v[162:165], v[206:209], v[14:17]
	v_mfma_f32_16x16x32_f16 v[14:17], v[126:129], v[210:213], v[102:105]
	v_mfma_f32_16x16x32_f16 v[102:105], v[130:133], v[214:217], v[14:17]
	v_mfma_f32_16x16x32_f16 v[14:17], v[158:161], v[210:213], v[106:109]
	v_mfma_f32_16x16x32_f16 v[106:109], v[162:165], v[214:217], v[14:17]
	v_mfma_f32_16x16x32_f16 v[14:17], v[126:129], v[218:221], v[110:113]
	v_mfma_f32_16x16x32_f16 v[110:113], v[130:133], v[222:225], v[14:17]
	v_mfma_f32_16x16x32_f16 v[14:17], v[158:161], v[218:221], v[114:117]
	v_mfma_f32_16x16x32_f16 v[114:117], v[162:165], v[222:225], v[14:17]
	s_setprio 0
	s_barrier
	s_mov_b64 s[0:1], 0x180
	s_mov_b32 m0, s22
	s_nop 2
	v_add_u32_e32 v14, 0x1c000, v234
	v_add_u32_e32 v16, 0x1c800, v234
	v_lshl_add_u64 v[242:243], v[30:31], 0, s[0:1]
	v_add_u32_e32 v15, 0x1c400, v234
	ds_read_b128 v[226:229], v14
	ds_read_b128 v[230:233], v15
	v_add_u32_e32 v17, 0x1cc00, v234
	ds_read_b128 v[234:237], v16
	ds_read_b128 v[238:241], v17
	global_load_lds_dwordx4 v[242:243], off
	v_lshl_add_u64 v[242:243], v[32:33], 0, s[0:1]
	s_mov_b32 m0, s21
	s_nop 0
	global_load_lds_dwordx4 v[242:243], off
	s_barrier
	s_waitcnt lgkmcnt(0)
	s_setprio 1
	s_waitcnt lgkmcnt(0)
	v_mfma_f32_16x16x32_f16 v[134:137], v[226:229], v[166:169], v[134:137]
	v_mfma_f32_16x16x32_f16 v[138:141], v[226:229], v[202:205], v[138:141]
	v_mfma_f32_16x16x32_f16 v[66:69], v[226:229], v[210:213], v[66:69]
	v_mfma_f32_16x16x32_f16 v[70:73], v[234:237], v[210:213], v[70:73]
	v_mfma_f32_16x16x32_f16 v[74:77], v[226:229], v[218:221], v[74:77]
	v_mfma_f32_16x16x32_f16 v[78:81], v[234:237], v[218:221], v[78:81]
	v_mfma_f32_16x16x32_f16 v[134:137], v[230:233], v[198:201], v[134:137]
	v_mfma_f32_16x16x32_f16 v[58:61], v[234:237], v[166:169], v[58:61]
	v_mfma_f32_16x16x32_f16 v[138:141], v[230:233], v[206:209], v[138:141]
	v_mfma_f32_16x16x32_f16 v[62:65], v[234:237], v[202:205], v[62:65]
	v_mfma_f32_16x16x32_f16 v[66:69], v[230:233], v[214:217], v[66:69]
	v_mfma_f32_16x16x32_f16 v[70:73], v[238:241], v[214:217], v[70:73]
	v_mfma_f32_16x16x32_f16 v[74:77], v[230:233], v[222:225], v[74:77]
	v_mfma_f32_16x16x32_f16 v[78:81], v[238:241], v[222:225], v[78:81]
	v_mfma_f32_16x16x32_f16 v[58:61], v[238:241], v[198:201], v[58:61]
	v_mfma_f32_16x16x32_f16 v[62:65], v[238:241], v[206:209], v[62:65]
	s_setprio 0
	s_mov_b32 m0, s19
	v_lshl_add_u64 v[242:243], v[26:27], 0, s[0:1]
	s_barrier
	ds_read_b128 v[166:169], v1 offset:49152
	ds_read_b128 v[198:201], v1 offset:50176
	ds_read_b128 v[202:205], v1 offset:51200
	ds_read_b128 v[206:209], v1 offset:52224
	ds_read_b128 v[210:213], v1 offset:53248
	ds_read_b128 v[214:217], v1 offset:54272
	ds_read_b128 v[218:221], v1 offset:55296
	ds_read_b128 v[222:225], v1 offset:56320
	global_load_lds_dwordx4 v[242:243], off
	v_lshl_add_u64 v[242:243], v[28:29], 0, s[0:1]
	s_mov_b32 m0, s17
	s_nop 0
	global_load_lds_dwordx4 v[242:243], off
	s_barrier
	s_waitcnt lgkmcnt(0)
	s_setprio 1
	s_waitcnt lgkmcnt(0)
	v_mfma_f32_16x16x32_f16 v[170:173], v[126:129], v[166:169], v[170:173]
	v_mfma_f32_16x16x32_f16 v[178:181], v[126:129], v[202:205], v[178:181]
	v_mfma_f32_16x16x32_f16 v[186:189], v[126:129], v[210:213], v[186:189]
	v_mfma_f32_16x16x32_f16 v[126:129], v[126:129], v[218:221], v[194:197]
	v_mfma_f32_16x16x32_f16 v[174:177], v[158:161], v[166:169], v[174:177]
	v_mfma_f32_16x16x32_f16 v[182:185], v[158:161], v[202:205], v[182:185]
	v_mfma_f32_16x16x32_f16 v[190:193], v[158:161], v[210:213], v[190:193]
	v_mfma_f32_16x16x32_f16 v[126:129], v[130:133], v[222:225], v[126:129]
	v_mfma_f32_16x16x32_f16 v[50:53], v[158:161], v[218:221], v[50:53]
	v_mfma_f32_16x16x32_f16 v[170:173], v[130:133], v[198:201], v[170:173]
	v_mfma_f32_16x16x32_f16 v[174:177], v[162:165], v[198:201], v[174:177]
	v_mfma_f32_16x16x32_f16 v[178:181], v[130:133], v[206:209], v[178:181]
	v_mfma_f32_16x16x32_f16 v[182:185], v[162:165], v[206:209], v[182:185]
	v_mfma_f32_16x16x32_f16 v[186:189], v[130:133], v[214:217], v[186:189]
	v_mfma_f32_16x16x32_f16 v[190:193], v[162:165], v[214:217], v[190:193]
	v_mfma_f32_16x16x32_f16 v[50:53], v[162:165], v[222:225], v[50:53]
	s_setprio 0
	s_barrier
	s_mov_b32 m0, s4
	v_lshl_add_u64 v[130:131], v[22:23], 0, s[0:1]
	global_load_lds_dwordx4 v[130:131], off
	v_lshl_add_u64 v[130:131], v[24:25], 0, s[0:1]
	s_mov_b32 m0, s3
	s_nop 0
	global_load_lds_dwordx4 v[130:131], off
	s_waitcnt vmcnt(6)
	s_barrier
	s_setprio 1
	v_mfma_f32_16x16x32_f16 v[82:85], v[234:237], v[166:169], v[82:85]
	v_mfma_f32_16x16x32_f16 v[130:133], v[226:229], v[202:205], v[142:145]
	v_mfma_f32_16x16x32_f16 v[142:145], v[234:237], v[202:205], v[146:149]
	v_mfma_f32_16x16x32_f16 v[146:149], v[226:229], v[210:213], v[150:153]
	v_mfma_f32_16x16x32_f16 v[150:153], v[234:237], v[210:213], v[154:157]
	v_mfma_f32_16x16x32_f16 v[118:121], v[226:229], v[218:221], v[118:121]
	v_mfma_f32_16x16x32_f16 v[122:125], v[234:237], v[218:221], v[122:125]
	v_mfma_f32_16x16x32_f16 v[54:57], v[226:229], v[166:169], v[54:57]
	v_mfma_f32_16x16x32_f16 v[82:85], v[238:241], v[198:201], v[82:85]
	v_mfma_f32_16x16x32_f16 v[130:133], v[230:233], v[206:209], v[130:133]
	v_mfma_f32_16x16x32_f16 v[142:145], v[238:241], v[206:209], v[142:145]
	v_mfma_f32_16x16x32_f16 v[150:153], v[238:241], v[214:217], v[150:153]
	v_mfma_f32_16x16x32_f16 v[118:121], v[230:233], v[222:225], v[118:121]
	v_mfma_f32_16x16x32_f16 v[122:125], v[238:241], v[222:225], v[122:125]
	v_mfma_f32_16x16x32_f16 v[54:57], v[230:233], v[198:201], v[54:57]
	v_mfma_f32_16x16x32_f16 v[146:149], v[230:233], v[214:217], v[146:149]
	s_setprio 0
	s_barrier
	ds_read_b128 v[154:157], v2
	ds_read_b128 v[158:161], v3
	ds_read_b128 v[162:165], v4
	ds_read_b128 v[166:169], v5
	s_mov_b32 m0, s7
	v_lshl_add_u64 v[194:195], v[18:19], 0, s[0:1]
	global_load_lds_dwordx4 v[194:195], off
	v_lshl_add_u64 v[194:195], v[20:21], 0, s[0:1]
	s_mov_b32 m0, s2
	s_nop 0
	global_load_lds_dwordx4 v[194:195], off
	ds_read_b128 v[194:197], v1
	ds_read_b128 v[198:201], v1 offset:1024
	ds_read_b128 v[202:205], v1 offset:2048
	ds_read_b128 v[206:209], v1 offset:3072
	ds_read_b128 v[210:213], v1 offset:4096
	ds_read_b128 v[214:217], v1 offset:5120
	ds_read_b128 v[218:221], v1 offset:6144
	ds_read_b128 v[222:225], v1 offset:7168
	s_waitcnt lgkmcnt(8)
	s_barrier
	s_waitcnt lgkmcnt(0)
	s_setprio 1
	s_waitcnt lgkmcnt(0)
	v_mfma_f32_16x16x32_f16 v[86:89], v[154:157], v[194:197], v[86:89]
	v_mfma_f32_16x16x32_f16 v[90:93], v[162:165], v[194:197], v[90:93]
	v_mfma_f32_16x16x32_f16 v[94:97], v[154:157], v[202:205], v[94:97]
	v_mfma_f32_16x16x32_f16 v[98:101], v[162:165], v[202:205], v[98:101]
	v_mfma_f32_16x16x32_f16 v[102:105], v[154:157], v[210:213], v[102:105]
	v_mfma_f32_16x16x32_f16 v[106:109], v[162:165], v[210:213], v[106:109]
	v_mfma_f32_16x16x32_f16 v[110:113], v[154:157], v[218:221], v[110:113]
	v_mfma_f32_16x16x32_f16 v[114:117], v[162:165], v[218:221], v[114:117]
	v_mfma_f32_16x16x32_f16 v[86:89], v[158:161], v[198:201], v[86:89]
	v_mfma_f32_16x16x32_f16 v[90:93], v[166:169], v[198:201], v[90:93]
	v_mfma_f32_16x16x32_f16 v[94:97], v[158:161], v[206:209], v[94:97]
	v_mfma_f32_16x16x32_f16 v[98:101], v[166:169], v[206:209], v[98:101]
	v_mfma_f32_16x16x32_f16 v[102:105], v[158:161], v[214:217], v[102:105]
	v_mfma_f32_16x16x32_f16 v[106:109], v[166:169], v[214:217], v[106:109]
	v_mfma_f32_16x16x32_f16 v[110:113], v[158:161], v[222:225], v[110:113]
	v_mfma_f32_16x16x32_f16 v[114:117], v[166:169], v[222:225], v[114:117]
	s_setprio 0
	s_barrier
	s_mov_b64 s[0:1], 0x200
	s_mov_b32 m0, s15
	v_lshl_add_u64 v[242:243], v[30:31], 0, s[0:1]
	ds_read_b128 v[226:229], v6
	ds_read_b128 v[230:233], v7
	ds_read_b128 v[234:237], v8
	ds_read_b128 v[238:241], v9
	global_load_lds_dwordx4 v[242:243], off
	v_lshl_add_u64 v[242:243], v[32:33], 0, s[0:1]
	s_mov_b32 m0, s5
	s_nop 0
	global_load_lds_dwordx4 v[242:243], off
	s_barrier
	s_waitcnt lgkmcnt(0)
	s_setprio 1
	s_waitcnt lgkmcnt(0)
	v_mfma_f32_16x16x32_f16 v[134:137], v[226:229], v[194:197], v[134:137]
	v_mfma_f32_16x16x32_f16 v[138:141], v[226:229], v[202:205], v[138:141]
	v_mfma_f32_16x16x32_f16 v[66:69], v[226:229], v[210:213], v[66:69]
	v_mfma_f32_16x16x32_f16 v[70:73], v[234:237], v[210:213], v[70:73]
	v_mfma_f32_16x16x32_f16 v[74:77], v[226:229], v[218:221], v[74:77]
	v_mfma_f32_16x16x32_f16 v[78:81], v[234:237], v[218:221], v[78:81]
	v_mfma_f32_16x16x32_f16 v[134:137], v[230:233], v[198:201], v[134:137]
	v_mfma_f32_16x16x32_f16 v[58:61], v[234:237], v[194:197], v[58:61]
	v_mfma_f32_16x16x32_f16 v[138:141], v[230:233], v[206:209], v[138:141]
	v_mfma_f32_16x16x32_f16 v[62:65], v[234:237], v[202:205], v[62:65]
	v_mfma_f32_16x16x32_f16 v[66:69], v[230:233], v[214:217], v[66:69]
	v_mfma_f32_16x16x32_f16 v[70:73], v[238:241], v[214:217], v[70:73]
	v_mfma_f32_16x16x32_f16 v[74:77], v[230:233], v[222:225], v[74:77]
	v_mfma_f32_16x16x32_f16 v[78:81], v[238:241], v[222:225], v[78:81]
	v_mfma_f32_16x16x32_f16 v[58:61], v[238:241], v[198:201], v[58:61]
	v_mfma_f32_16x16x32_f16 v[62:65], v[238:241], v[206:209], v[62:65]
	s_setprio 0
	s_mov_b32 m0, s16
	v_lshl_add_u64 v[242:243], v[26:27], 0, s[0:1]
	s_barrier
	ds_read_b128 v[194:197], v1 offset:16384
	ds_read_b128 v[198:201], v1 offset:17408
	ds_read_b128 v[202:205], v1 offset:18432
	ds_read_b128 v[206:209], v1 offset:19456
	ds_read_b128 v[210:213], v1 offset:20480
	ds_read_b128 v[214:217], v1 offset:21504
	ds_read_b128 v[218:221], v1 offset:22528
	ds_read_b128 v[222:225], v1 offset:23552
	global_load_lds_dwordx4 v[242:243], off
	v_lshl_add_u64 v[242:243], v[28:29], 0, s[0:1]
	s_mov_b32 m0, s10
	s_nop 0
	global_load_lds_dwordx4 v[242:243], off
	s_barrier
	s_waitcnt lgkmcnt(0)
	s_setprio 1
	s_waitcnt lgkmcnt(0)
	v_mfma_f32_16x16x32_f16 v[126:129], v[154:157], v[218:221], v[126:129]
	v_mfma_f32_16x16x32_f16 v[170:173], v[154:157], v[194:197], v[170:173]
	v_mfma_f32_16x16x32_f16 v[174:177], v[162:165], v[194:197], v[174:177]
	v_mfma_f32_16x16x32_f16 v[178:181], v[154:157], v[202:205], v[178:181]
	v_mfma_f32_16x16x32_f16 v[182:185], v[162:165], v[202:205], v[182:185]
	v_mfma_f32_16x16x32_f16 v[186:189], v[154:157], v[210:213], v[186:189]
	v_mfma_f32_16x16x32_f16 v[190:193], v[162:165], v[210:213], v[190:193]
	v_mfma_f32_16x16x32_f16 v[126:129], v[158:161], v[222:225], v[126:129]
	v_mfma_f32_16x16x32_f16 v[50:53], v[162:165], v[218:221], v[50:53]
	v_mfma_f32_16x16x32_f16 v[170:173], v[158:161], v[198:201], v[170:173]
	v_mfma_f32_16x16x32_f16 v[174:177], v[166:169], v[198:201], v[174:177]
	v_mfma_f32_16x16x32_f16 v[178:181], v[158:161], v[206:209], v[178:181]
	v_mfma_f32_16x16x32_f16 v[182:185], v[166:169], v[206:209], v[182:185]
	v_mfma_f32_16x16x32_f16 v[186:189], v[158:161], v[214:217], v[186:189]
	v_mfma_f32_16x16x32_f16 v[190:193], v[166:169], v[214:217], v[190:193]
	v_mfma_f32_16x16x32_f16 v[50:53], v[166:169], v[222:225], v[50:53]
	s_setprio 0
	s_barrier
	s_mov_b32 m0, s14
	v_lshl_add_u64 v[154:155], v[22:23], 0, s[0:1]
	global_load_lds_dwordx4 v[154:155], off
	v_lshl_add_u64 v[154:155], v[24:25], 0, s[0:1]
	s_mov_b32 m0, s11
	s_nop 0
	global_load_lds_dwordx4 v[154:155], off
	s_waitcnt vmcnt(6)
	s_barrier
	s_setprio 1
	v_mfma_f32_16x16x32_f16 v[82:85], v[234:237], v[194:197], v[82:85]
	v_mfma_f32_16x16x32_f16 v[130:133], v[226:229], v[202:205], v[130:133]
	v_mfma_f32_16x16x32_f16 v[142:145], v[234:237], v[202:205], v[142:145]
	v_mfma_f32_16x16x32_f16 v[150:153], v[234:237], v[210:213], v[150:153]
	v_mfma_f32_16x16x32_f16 v[118:121], v[226:229], v[218:221], v[118:121]
	v_mfma_f32_16x16x32_f16 v[122:125], v[234:237], v[218:221], v[122:125]
	v_mfma_f32_16x16x32_f16 v[54:57], v[226:229], v[194:197], v[54:57]
	v_mfma_f32_16x16x32_f16 v[82:85], v[238:241], v[198:201], v[82:85]
	v_mfma_f32_16x16x32_f16 v[130:133], v[230:233], v[206:209], v[130:133]
	v_mfma_f32_16x16x32_f16 v[142:145], v[238:241], v[206:209], v[142:145]
	v_mfma_f32_16x16x32_f16 v[146:149], v[226:229], v[210:213], v[146:149]
	v_mfma_f32_16x16x32_f16 v[150:153], v[238:241], v[214:217], v[150:153]
	v_mfma_f32_16x16x32_f16 v[118:121], v[230:233], v[222:225], v[118:121]
	v_mfma_f32_16x16x32_f16 v[122:125], v[238:241], v[222:225], v[122:125]
	v_mfma_f32_16x16x32_f16 v[54:57], v[230:233], v[198:201], v[54:57]
	v_mfma_f32_16x16x32_f16 v[146:149], v[230:233], v[214:217], v[146:149]
	s_setprio 0
	s_barrier
	ds_read_b128 v[154:157], v10
	ds_read_b128 v[158:161], v11
	ds_read_b128 v[162:165], v12
	ds_read_b128 v[166:169], v13
	s_mov_b32 m0, s20
	v_lshl_add_u64 v[226:227], v[18:19], 0, s[0:1]
	ds_read_b128 v[194:197], v1 offset:32768
	ds_read_b128 v[198:201], v1 offset:33792
	ds_read_b128 v[202:205], v1 offset:34816
	ds_read_b128 v[206:209], v1 offset:35840
	ds_read_b128 v[210:213], v1 offset:36864
	ds_read_b128 v[214:217], v1 offset:37888
	ds_read_b128 v[218:221], v1 offset:38912
	ds_read_b128 v[222:225], v1 offset:39936
	global_load_lds_dwordx4 v[226:227], off
	v_lshl_add_u64 v[226:227], v[20:21], 0, s[0:1]
	s_mov_b32 m0, s18
	s_nop 0
	global_load_lds_dwordx4 v[226:227], off
	s_waitcnt lgkmcnt(8)
	s_barrier
	s_waitcnt lgkmcnt(0)
	s_setprio 1
	s_waitcnt lgkmcnt(0)
	v_mfma_f32_16x16x32_f16 v[86:89], v[154:157], v[194:197], v[86:89]
	v_mfma_f32_16x16x32_f16 v[90:93], v[162:165], v[194:197], v[90:93]
	v_mfma_f32_16x16x32_f16 v[94:97], v[154:157], v[202:205], v[94:97]
	v_mfma_f32_16x16x32_f16 v[98:101], v[162:165], v[202:205], v[98:101]
	v_mfma_f32_16x16x32_f16 v[102:105], v[154:157], v[210:213], v[102:105]
	v_mfma_f32_16x16x32_f16 v[106:109], v[162:165], v[210:213], v[106:109]
	v_mfma_f32_16x16x32_f16 v[110:113], v[154:157], v[218:221], v[110:113]
	v_mfma_f32_16x16x32_f16 v[114:117], v[162:165], v[218:221], v[114:117]
	v_mfma_f32_16x16x32_f16 v[86:89], v[158:161], v[198:201], v[86:89]
	v_mfma_f32_16x16x32_f16 v[90:93], v[166:169], v[198:201], v[90:93]
	v_mfma_f32_16x16x32_f16 v[94:97], v[158:161], v[206:209], v[94:97]
	v_mfma_f32_16x16x32_f16 v[98:101], v[166:169], v[206:209], v[98:101]
	v_mfma_f32_16x16x32_f16 v[102:105], v[158:161], v[214:217], v[102:105]
	v_mfma_f32_16x16x32_f16 v[106:109], v[166:169], v[214:217], v[106:109]
	v_mfma_f32_16x16x32_f16 v[110:113], v[158:161], v[222:225], v[110:113]
	v_mfma_f32_16x16x32_f16 v[114:117], v[166:169], v[222:225], v[114:117]
	s_setprio 0
	s_barrier
	s_mov_b64 s[0:1], 0x280
	v_readfirstlane_b32 s10, v48
	v_lshl_add_u64 v[242:243], v[30:31], 0, s[0:1]
	s_mov_b32 m0, s10
	v_readfirstlane_b32 s2, v49
	ds_read_b128 v[226:229], v14
	ds_read_b128 v[230:233], v15
	ds_read_b128 v[234:237], v16
	ds_read_b128 v[238:241], v17
	global_load_lds_dwordx4 v[242:243], off
	v_lshl_add_u64 v[242:243], v[32:33], 0, s[0:1]
	s_mov_b32 m0, s2
	s_nop 0
	global_load_lds_dwordx4 v[242:243], off
	s_barrier
	s_waitcnt lgkmcnt(0)
	s_setprio 1
	s_waitcnt lgkmcnt(0)
	v_mfma_f32_16x16x32_f16 v[134:137], v[226:229], v[194:197], v[134:137]
	v_mfma_f32_16x16x32_f16 v[138:141], v[226:229], v[202:205], v[138:141]
	v_mfma_f32_16x16x32_f16 v[66:69], v[226:229], v[210:213], v[66:69]
	v_mfma_f32_16x16x32_f16 v[70:73], v[234:237], v[210:213], v[70:73]
	v_mfma_f32_16x16x32_f16 v[74:77], v[226:229], v[218:221], v[74:77]
	v_mfma_f32_16x16x32_f16 v[78:81], v[234:237], v[218:221], v[78:81]
	v_mfma_f32_16x16x32_f16 v[134:137], v[230:233], v[198:201], v[134:137]
	v_mfma_f32_16x16x32_f16 v[58:61], v[234:237], v[194:197], v[58:61]
	v_mfma_f32_16x16x32_f16 v[138:141], v[230:233], v[206:209], v[138:141]
	v_mfma_f32_16x16x32_f16 v[62:65], v[234:237], v[202:205], v[62:65]
	v_mfma_f32_16x16x32_f16 v[66:69], v[230:233], v[214:217], v[66:69]
	v_mfma_f32_16x16x32_f16 v[70:73], v[238:241], v[214:217], v[70:73]
	v_mfma_f32_16x16x32_f16 v[74:77], v[230:233], v[222:225], v[74:77]
	v_mfma_f32_16x16x32_f16 v[78:81], v[238:241], v[222:225], v[78:81]
	v_mfma_f32_16x16x32_f16 v[58:61], v[238:241], v[198:201], v[58:61]
	v_mfma_f32_16x16x32_f16 v[62:65], v[238:241], v[206:209], v[62:65]
	s_setprio 0
	v_readfirstlane_b32 s11, v46
	v_lshl_add_u64 v[48:49], v[26:27], 0, s[0:1]
	s_mov_b32 m0, s11
	v_readfirstlane_b32 s3, v47
	s_barrier
	ds_read_b128 v[194:197], v1 offset:49152
	ds_read_b128 v[198:201], v1 offset:50176
	ds_read_b128 v[202:205], v1 offset:51200
	ds_read_b128 v[206:209], v1 offset:52224
	ds_read_b128 v[210:213], v1 offset:53248
	ds_read_b128 v[214:217], v1 offset:54272
	ds_read_b128 v[218:221], v1 offset:55296
	ds_read_b128 v[222:225], v1 offset:56320
	global_load_lds_dwordx4 v[48:49], off
	v_lshl_add_u64 v[48:49], v[28:29], 0, s[0:1]
	s_mov_b32 m0, s3
	s_nop 0
	global_load_lds_dwordx4 v[48:49], off
	s_barrier
	s_waitcnt lgkmcnt(0)
	s_setprio 1
	s_waitcnt lgkmcnt(0)
	v_mfma_f32_16x16x32_f16 v[126:129], v[154:157], v[218:221], v[126:129]
	v_mfma_f32_16x16x32_f16 v[46:49], v[154:157], v[194:197], v[170:173]
	v_mfma_f32_16x16x32_f16 v[170:173], v[162:165], v[194:197], v[174:177]
	v_mfma_f32_16x16x32_f16 v[174:177], v[154:157], v[202:205], v[178:181]
	v_mfma_f32_16x16x32_f16 v[178:181], v[162:165], v[202:205], v[182:185]
	v_mfma_f32_16x16x32_f16 v[182:185], v[154:157], v[210:213], v[186:189]
	v_mfma_f32_16x16x32_f16 v[186:189], v[162:165], v[210:213], v[190:193]
	v_mfma_f32_16x16x32_f16 v[126:129], v[158:161], v[222:225], v[126:129]
	v_mfma_f32_16x16x32_f16 v[50:53], v[162:165], v[218:221], v[50:53]
	v_mfma_f32_16x16x32_f16 v[46:49], v[158:161], v[198:201], v[46:49]
	v_mfma_f32_16x16x32_f16 v[170:173], v[166:169], v[198:201], v[170:173]
	v_mfma_f32_16x16x32_f16 v[174:177], v[158:161], v[206:209], v[174:177]
	v_mfma_f32_16x16x32_f16 v[178:181], v[166:169], v[206:209], v[178:181]
	v_mfma_f32_16x16x32_f16 v[182:185], v[158:161], v[214:217], v[182:185]
	v_mfma_f32_16x16x32_f16 v[186:189], v[166:169], v[214:217], v[186:189]
	v_mfma_f32_16x16x32_f16 v[50:53], v[166:169], v[222:225], v[50:53]
	s_setprio 0
	s_barrier
	v_readfirstlane_b32 s5, v38
	v_lshl_add_u64 v[154:155], v[22:23], 0, s[0:1]
	s_mov_b32 m0, s5
	v_readfirstlane_b32 s4, v40
	global_load_lds_dwordx4 v[154:155], off
	v_lshl_add_u64 v[154:155], v[24:25], 0, s[0:1]
	s_mov_b32 m0, s4
	s_nop 0
	global_load_lds_dwordx4 v[154:155], off
	s_waitcnt vmcnt(6)
	s_barrier
	s_setprio 1
	v_mfma_f32_16x16x32_f16 v[82:85], v[234:237], v[194:197], v[82:85]
	v_mfma_f32_16x16x32_f16 v[130:133], v[226:229], v[202:205], v[130:133]
	v_mfma_f32_16x16x32_f16 v[142:145], v[234:237], v[202:205], v[142:145]
	v_mfma_f32_16x16x32_f16 v[150:153], v[234:237], v[210:213], v[150:153]
	v_mfma_f32_16x16x32_f16 v[118:121], v[226:229], v[218:221], v[118:121]
	v_mfma_f32_16x16x32_f16 v[122:125], v[234:237], v[218:221], v[122:125]
	v_mfma_f32_16x16x32_f16 v[54:57], v[226:229], v[194:197], v[54:57]
	v_mfma_f32_16x16x32_f16 v[82:85], v[238:241], v[198:201], v[82:85]
	v_mfma_f32_16x16x32_f16 v[130:133], v[230:233], v[206:209], v[130:133]
	v_mfma_f32_16x16x32_f16 v[142:145], v[238:241], v[206:209], v[142:145]
	v_mfma_f32_16x16x32_f16 v[146:149], v[226:229], v[210:213], v[146:149]
	v_mfma_f32_16x16x32_f16 v[150:153], v[238:241], v[214:217], v[150:153]
	v_mfma_f32_16x16x32_f16 v[118:121], v[230:233], v[222:225], v[118:121]
	v_mfma_f32_16x16x32_f16 v[122:125], v[238:241], v[222:225], v[122:125]
	v_mfma_f32_16x16x32_f16 v[54:57], v[230:233], v[198:201], v[54:57]
	v_mfma_f32_16x16x32_f16 v[146:149], v[230:233], v[214:217], v[146:149]
	s_setprio 0
	s_barrier
	ds_read_b128 v[154:157], v2
	ds_read_b128 v[158:161], v3
	ds_read_b128 v[162:165], v4
	ds_read_b128 v[166:169], v5
	v_readfirstlane_b32 s14, v37
	v_lshl_add_u64 v[190:191], v[18:19], 0, s[0:1]
	s_mov_b32 m0, s14
	v_readfirstlane_b32 s7, v39
	global_load_lds_dwordx4 v[190:191], off
	v_lshl_add_u64 v[190:191], v[20:21], 0, s[0:1]
	s_mov_b32 m0, s7
	s_nop 0
	global_load_lds_dwordx4 v[190:191], off
	ds_read_b128 v[190:193], v1
	ds_read_b128 v[194:197], v1 offset:1024
	ds_read_b128 v[198:201], v1 offset:2048
	ds_read_b128 v[202:205], v1 offset:3072
	ds_read_b128 v[206:209], v1 offset:4096
	ds_read_b128 v[210:213], v1 offset:5120
	ds_read_b128 v[214:217], v1 offset:6144
	ds_read_b128 v[218:221], v1 offset:7168
	s_waitcnt lgkmcnt(8)
	s_barrier
	s_waitcnt lgkmcnt(0)
	s_setprio 1
	s_waitcnt lgkmcnt(0)
	v_mfma_f32_16x16x32_f16 v[86:89], v[154:157], v[190:193], v[86:89]
	v_mfma_f32_16x16x32_f16 v[90:93], v[162:165], v[190:193], v[90:93]
	v_mfma_f32_16x16x32_f16 v[94:97], v[154:157], v[198:201], v[94:97]
	v_mfma_f32_16x16x32_f16 v[98:101], v[162:165], v[198:201], v[98:101]
	v_mfma_f32_16x16x32_f16 v[102:105], v[154:157], v[206:209], v[102:105]
	v_mfma_f32_16x16x32_f16 v[106:109], v[162:165], v[206:209], v[106:109]
	v_mfma_f32_16x16x32_f16 v[110:113], v[154:157], v[214:217], v[110:113]
	v_mfma_f32_16x16x32_f16 v[114:117], v[162:165], v[214:217], v[114:117]
	v_mfma_f32_16x16x32_f16 v[86:89], v[158:161], v[194:197], v[86:89]
	v_mfma_f32_16x16x32_f16 v[90:93], v[166:169], v[194:197], v[90:93]
	v_mfma_f32_16x16x32_f16 v[94:97], v[158:161], v[202:205], v[94:97]
	v_mfma_f32_16x16x32_f16 v[98:101], v[166:169], v[202:205], v[98:101]
	v_mfma_f32_16x16x32_f16 v[102:105], v[158:161], v[210:213], v[102:105]
	v_mfma_f32_16x16x32_f16 v[106:109], v[166:169], v[210:213], v[106:109]
	v_mfma_f32_16x16x32_f16 v[110:113], v[158:161], v[218:221], v[110:113]
	v_mfma_f32_16x16x32_f16 v[114:117], v[166:169], v[218:221], v[114:117]
	s_setprio 0
	s_barrier
	s_mov_b64 s[0:1], 0x300
	v_readfirstlane_b32 s15, v36
	v_lshl_add_u64 v[38:39], v[30:31], 0, s[0:1]
	s_mov_b32 m0, s15
	v_readfirstlane_b32 s15, v41
	ds_read_b128 v[222:225], v6
	ds_read_b128 v[226:229], v7
	ds_read_b128 v[230:233], v8
	ds_read_b128 v[234:237], v9
	global_load_lds_dwordx4 v[38:39], off
	v_lshl_add_u64 v[36:37], v[32:33], 0, s[0:1]
	s_mov_b32 m0, s15
	s_nop 0
	global_load_lds_dwordx4 v[36:37], off
	s_barrier
	s_waitcnt lgkmcnt(0)
	s_setprio 1
	s_waitcnt lgkmcnt(0)
	v_mfma_f32_16x16x32_f16 v[36:39], v[222:225], v[190:193], v[134:137]
	v_mfma_f32_16x16x32_f16 v[134:137], v[222:225], v[198:201], v[138:141]
	v_mfma_f32_16x16x32_f16 v[66:69], v[222:225], v[206:209], v[66:69]
	v_mfma_f32_16x16x32_f16 v[70:73], v[230:233], v[206:209], v[70:73]
	v_mfma_f32_16x16x32_f16 v[74:77], v[222:225], v[214:217], v[74:77]
	v_mfma_f32_16x16x32_f16 v[78:81], v[230:233], v[214:217], v[78:81]
	v_mfma_f32_16x16x32_f16 v[58:61], v[230:233], v[190:193], v[58:61]
	v_mfma_f32_16x16x32_f16 v[134:137], v[226:229], v[202:205], v[134:137]
	v_mfma_f32_16x16x32_f16 v[62:65], v[230:233], v[198:201], v[62:65]
	v_mfma_f32_16x16x32_f16 v[66:69], v[226:229], v[210:213], v[66:69]
	v_mfma_f32_16x16x32_f16 v[70:73], v[234:237], v[210:213], v[70:73]
	v_mfma_f32_16x16x32_f16 v[74:77], v[226:229], v[218:221], v[74:77]
	v_mfma_f32_16x16x32_f16 v[78:81], v[234:237], v[218:221], v[78:81]
	v_mfma_f32_16x16x32_f16 v[36:39], v[226:229], v[194:197], v[36:39]
	v_mfma_f32_16x16x32_f16 v[58:61], v[234:237], v[194:197], v[58:61]
	v_mfma_f32_16x16x32_f16 v[62:65], v[234:237], v[202:205], v[62:65]
	s_setprio 0
	v_readfirstlane_b32 s15, v35
	v_lshl_add_u64 v[40:41], v[26:27], 0, s[0:1]
	s_mov_b32 m0, s15
	v_readfirstlane_b32 s15, v42
	s_barrier
	ds_read_b128 v[138:141], v1 offset:16384
	ds_read_b128 v[190:193], v1 offset:17408
	ds_read_b128 v[194:197], v1 offset:18432
	ds_read_b128 v[198:201], v1 offset:19456
	ds_read_b128 v[202:205], v1 offset:20480
	ds_read_b128 v[206:209], v1 offset:21504
	ds_read_b128 v[210:213], v1 offset:22528
	ds_read_b128 v[214:217], v1 offset:23552
	global_load_lds_dwordx4 v[40:41], off
	v_lshl_add_u64 v[40:41], v[28:29], 0, s[0:1]
	s_mov_b32 m0, s15
	s_nop 0
	global_load_lds_dwordx4 v[40:41], off
	s_barrier
	s_waitcnt lgkmcnt(0)
	s_setprio 1
	s_waitcnt lgkmcnt(0)
	v_mfma_f32_16x16x32_f16 v[126:129], v[154:157], v[210:213], v[126:129]
	v_mfma_f32_16x16x32_f16 v[46:49], v[154:157], v[138:141], v[46:49]
	v_mfma_f32_16x16x32_f16 v[170:173], v[162:165], v[138:141], v[170:173]
	v_mfma_f32_16x16x32_f16 v[174:177], v[154:157], v[194:197], v[174:177]
	v_mfma_f32_16x16x32_f16 v[178:181], v[162:165], v[194:197], v[178:181]
	v_mfma_f32_16x16x32_f16 v[182:185], v[154:157], v[202:205], v[182:185]
	v_mfma_f32_16x16x32_f16 v[186:189], v[162:165], v[202:205], v[186:189]
	v_mfma_f32_16x16x32_f16 v[126:129], v[158:161], v[214:217], v[126:129]
	v_mfma_f32_16x16x32_f16 v[50:53], v[162:165], v[210:213], v[50:53]
	v_mfma_f32_16x16x32_f16 v[46:49], v[158:161], v[190:193], v[46:49]
	v_mfma_f32_16x16x32_f16 v[170:173], v[166:169], v[190:193], v[170:173]
	v_mfma_f32_16x16x32_f16 v[174:177], v[158:161], v[198:201], v[174:177]
	v_mfma_f32_16x16x32_f16 v[178:181], v[166:169], v[198:201], v[178:181]
	v_mfma_f32_16x16x32_f16 v[182:185], v[158:161], v[206:209], v[182:185]
	v_mfma_f32_16x16x32_f16 v[186:189], v[166:169], v[206:209], v[186:189]
	v_mfma_f32_16x16x32_f16 v[50:53], v[166:169], v[214:217], v[50:53]
	s_setprio 0
	s_barrier
	v_readfirstlane_b32 s15, v34
	v_lshl_add_u64 v[40:41], v[22:23], 0, s[0:1]
	s_mov_b32 m0, s15
	v_readfirstlane_b32 s15, v43
	global_load_lds_dwordx4 v[40:41], off
	v_lshl_add_u64 v[34:35], v[24:25], 0, s[0:1]
	s_mov_b32 m0, s15
	s_nop 0
	global_load_lds_dwordx4 v[34:35], off
	s_waitcnt vmcnt(6)
	s_barrier
	s_setprio 1
	v_mfma_f32_16x16x32_f16 v[40:43], v[222:225], v[138:141], v[54:57]
	v_mfma_f32_16x16x32_f16 v[54:57], v[230:233], v[138:141], v[82:85]
	v_mfma_f32_16x16x32_f16 v[82:85], v[222:225], v[194:197], v[130:133]
	v_mfma_f32_16x16x32_f16 v[130:133], v[230:233], v[194:197], v[142:145]
	v_mfma_f32_16x16x32_f16 v[138:141], v[222:225], v[202:205], v[146:149]
	v_mfma_f32_16x16x32_f16 v[142:145], v[230:233], v[202:205], v[150:153]
	v_mfma_f32_16x16x32_f16 v[118:121], v[222:225], v[210:213], v[118:121]
	v_mfma_f32_16x16x32_f16 v[122:125], v[230:233], v[210:213], v[122:125]
	v_mfma_f32_16x16x32_f16 v[82:85], v[226:229], v[198:201], v[82:85]
	v_mfma_f32_16x16x32_f16 v[130:133], v[234:237], v[198:201], v[130:133]
	v_mfma_f32_16x16x32_f16 v[138:141], v[226:229], v[206:209], v[138:141]
	v_mfma_f32_16x16x32_f16 v[142:145], v[234:237], v[206:209], v[142:145]
	v_mfma_f32_16x16x32_f16 v[118:121], v[226:229], v[214:217], v[118:121]
	v_mfma_f32_16x16x32_f16 v[122:125], v[234:237], v[214:217], v[122:125]
	v_mfma_f32_16x16x32_f16 v[40:43], v[226:229], v[190:193], v[40:43]
	v_mfma_f32_16x16x32_f16 v[54:57], v[234:237], v[190:193], v[54:57]
	s_setprio 0
	s_barrier
	ds_read_b128 v[146:149], v10
	ds_read_b128 v[150:153], v11
	ds_read_b128 v[154:157], v12
	ds_read_b128 v[158:161], v13
	v_readfirstlane_b32 s15, v44
	v_lshl_add_u64 v[34:35], v[18:19], 0, s[0:1]
	s_mov_b32 m0, s15
	ds_read_b128 v[162:165], v1 offset:32768
	ds_read_b128 v[166:169], v1 offset:33792
	ds_read_b128 v[190:193], v1 offset:34816
	ds_read_b128 v[194:197], v1 offset:35840
	ds_read_b128 v[198:201], v1 offset:36864
	ds_read_b128 v[202:205], v1 offset:37888
	ds_read_b128 v[206:209], v1 offset:38912
	ds_read_b128 v[210:213], v1 offset:39936
	global_load_lds_dwordx4 v[34:35], off
	v_lshl_add_u64 v[34:35], v[20:21], 0, s[0:1]
	v_readfirstlane_b32 s0, v45
	s_mov_b32 m0, s0
	s_nop 0
	global_load_lds_dwordx4 v[34:35], off
	s_waitcnt lgkmcnt(8)
	s_barrier
	s_waitcnt lgkmcnt(0)
	s_setprio 1
	s_waitcnt lgkmcnt(0)
	v_mfma_f32_16x16x32_f16 v[86:89], v[146:149], v[162:165], v[86:89]
	v_mfma_f32_16x16x32_f16 v[90:93], v[154:157], v[162:165], v[90:93]
	v_mfma_f32_16x16x32_f16 v[94:97], v[146:149], v[190:193], v[94:97]
	v_mfma_f32_16x16x32_f16 v[98:101], v[154:157], v[190:193], v[98:101]
	v_mfma_f32_16x16x32_f16 v[102:105], v[146:149], v[198:201], v[102:105]
	v_mfma_f32_16x16x32_f16 v[106:109], v[154:157], v[198:201], v[106:109]
	v_mfma_f32_16x16x32_f16 v[110:113], v[146:149], v[206:209], v[110:113]
	v_mfma_f32_16x16x32_f16 v[114:117], v[154:157], v[206:209], v[114:117]
	v_mfma_f32_16x16x32_f16 v[86:89], v[150:153], v[166:169], v[86:89]
	v_mfma_f32_16x16x32_f16 v[90:93], v[158:161], v[166:169], v[90:93]
	v_mfma_f32_16x16x32_f16 v[94:97], v[150:153], v[194:197], v[94:97]
	v_mfma_f32_16x16x32_f16 v[98:101], v[158:161], v[194:197], v[98:101]
	v_mfma_f32_16x16x32_f16 v[102:105], v[150:153], v[202:205], v[102:105]
	v_mfma_f32_16x16x32_f16 v[106:109], v[158:161], v[202:205], v[106:109]
	v_mfma_f32_16x16x32_f16 v[110:113], v[150:153], v[210:213], v[110:113]
	v_mfma_f32_16x16x32_f16 v[114:117], v[158:161], v[210:213], v[114:117]
	s_setprio 0
	s_barrier
	s_mov_b64 s[0:1], 0x380
	s_mov_b32 m0, s10
	v_lshl_add_u64 v[30:31], v[30:31], 0, s[0:1]
	ds_read_b128 v[214:217], v14
	ds_read_b128 v[218:221], v15
	ds_read_b128 v[222:225], v16
	ds_read_b128 v[226:229], v17
	global_load_lds_dwordx4 v[30:31], off
	v_lshl_add_u64 v[30:31], v[32:33], 0, s[0:1]
	s_mov_b32 m0, s2
	s_nop 0
	global_load_lds_dwordx4 v[30:31], off
	s_barrier
	s_waitcnt lgkmcnt(0)
	s_setprio 1
	s_waitcnt lgkmcnt(0)
	v_mfma_f32_16x16x32_f16 v[30:33], v[214:217], v[162:165], v[36:39]
	v_mfma_f32_16x16x32_f16 v[66:69], v[214:217], v[198:201], v[66:69]
	v_mfma_f32_16x16x32_f16 v[70:73], v[222:225], v[198:201], v[70:73]
	v_mfma_f32_16x16x32_f16 v[74:77], v[214:217], v[206:209], v[74:77]
	v_mfma_f32_16x16x32_f16 v[78:81], v[222:225], v[206:209], v[78:81]
	v_mfma_f32_16x16x32_f16 v[30:33], v[218:221], v[166:169], v[30:33]
	v_mfma_f32_16x16x32_f16 v[34:37], v[222:225], v[162:165], v[58:61]
	v_mfma_f32_16x16x32_f16 v[58:61], v[214:217], v[190:193], v[134:137]
	v_mfma_f32_16x16x32_f16 v[62:65], v[222:225], v[190:193], v[62:65]
	v_mfma_f32_16x16x32_f16 v[66:69], v[218:221], v[202:205], v[66:69]
	v_mfma_f32_16x16x32_f16 v[70:73], v[226:229], v[202:205], v[70:73]
	v_mfma_f32_16x16x32_f16 v[74:77], v[218:221], v[210:213], v[74:77]
	v_mfma_f32_16x16x32_f16 v[78:81], v[226:229], v[210:213], v[78:81]
	v_mfma_f32_16x16x32_f16 v[34:37], v[226:229], v[166:169], v[34:37]
	v_mfma_f32_16x16x32_f16 v[58:61], v[218:221], v[194:197], v[58:61]
	v_mfma_f32_16x16x32_f16 v[62:65], v[226:229], v[194:197], v[62:65]
	s_setprio 0
	s_mov_b32 m0, s11
	v_lshl_add_u64 v[26:27], v[26:27], 0, s[0:1]
	s_barrier
	ds_read_b128 v[134:137], v1 offset:49152
	ds_read_b128 v[162:165], v1 offset:50176
	ds_read_b128 v[166:169], v1 offset:51200
	ds_read_b128 v[190:193], v1 offset:52224
	ds_read_b128 v[194:197], v1 offset:53248
	ds_read_b128 v[198:201], v1 offset:54272
	ds_read_b128 v[202:205], v1 offset:55296
	ds_read_b128 v[206:209], v1 offset:56320
	global_load_lds_dwordx4 v[26:27], off
	v_lshl_add_u64 v[26:27], v[28:29], 0, s[0:1]
	s_mov_b32 m0, s3
	s_nop 0
	global_load_lds_dwordx4 v[26:27], off
	s_barrier
	s_waitcnt lgkmcnt(0)
	s_setprio 1
	s_waitcnt lgkmcnt(0)
	v_mfma_f32_16x16x32_f16 v[26:29], v[146:149], v[134:137], v[46:49]
	v_mfma_f32_16x16x32_f16 v[126:129], v[146:149], v[202:205], v[126:129]
	v_mfma_f32_16x16x32_f16 v[26:29], v[150:153], v[162:165], v[26:29]
	v_mfma_f32_16x16x32_f16 v[44:47], v[154:157], v[134:137], v[170:173]
	v_mfma_f32_16x16x32_f16 v[170:173], v[146:149], v[166:169], v[174:177]
	v_mfma_f32_16x16x32_f16 v[174:177], v[154:157], v[166:169], v[178:181]
	v_mfma_f32_16x16x32_f16 v[178:181], v[146:149], v[194:197], v[182:185]
	v_mfma_f32_16x16x32_f16 v[182:185], v[154:157], v[194:197], v[186:189]
	v_mfma_f32_16x16x32_f16 v[126:129], v[150:153], v[206:209], v[126:129]
	v_mfma_f32_16x16x32_f16 v[48:51], v[154:157], v[202:205], v[50:53]
	v_mfma_f32_16x16x32_f16 v[44:47], v[158:161], v[162:165], v[44:47]
	v_mfma_f32_16x16x32_f16 v[170:173], v[150:153], v[190:193], v[170:173]
	v_mfma_f32_16x16x32_f16 v[174:177], v[158:161], v[190:193], v[174:177]
	v_mfma_f32_16x16x32_f16 v[178:181], v[150:153], v[198:201], v[178:181]
	v_mfma_f32_16x16x32_f16 v[182:185], v[158:161], v[198:201], v[182:185]
	v_mfma_f32_16x16x32_f16 v[48:51], v[158:161], v[206:209], v[48:51]
	s_setprio 0
	s_barrier
	s_mov_b32 m0, s5
	v_lshl_add_u64 v[22:23], v[22:23], 0, s[0:1]
	global_load_lds_dwordx4 v[22:23], off
	v_lshl_add_u64 v[22:23], v[24:25], 0, s[0:1]
	s_mov_b32 m0, s4
	s_nop 0
	global_load_lds_dwordx4 v[22:23], off
	s_waitcnt vmcnt(6)
	s_barrier
	s_setprio 1
	v_mfma_f32_16x16x32_f16 v[22:25], v[214:217], v[134:137], v[40:43]
	v_mfma_f32_16x16x32_f16 v[38:41], v[222:225], v[134:137], v[54:57]
	v_mfma_f32_16x16x32_f16 v[52:55], v[214:217], v[166:169], v[82:85]
	v_mfma_f32_16x16x32_f16 v[82:85], v[222:225], v[166:169], v[130:133]
	v_mfma_f32_16x16x32_f16 v[130:133], v[214:217], v[194:197], v[138:141]
	v_mfma_f32_16x16x32_f16 v[134:137], v[222:225], v[194:197], v[142:145]
	v_mfma_f32_16x16x32_f16 v[118:121], v[214:217], v[202:205], v[118:121]
	v_mfma_f32_16x16x32_f16 v[122:125], v[222:225], v[202:205], v[122:125]
	v_mfma_f32_16x16x32_f16 v[22:25], v[218:221], v[162:165], v[22:25]
	v_mfma_f32_16x16x32_f16 v[82:85], v[226:229], v[190:193], v[82:85]
	v_mfma_f32_16x16x32_f16 v[130:133], v[218:221], v[198:201], v[130:133]
	v_mfma_f32_16x16x32_f16 v[134:137], v[226:229], v[198:201], v[134:137]
	v_mfma_f32_16x16x32_f16 v[118:121], v[218:221], v[206:209], v[118:121]
	v_mfma_f32_16x16x32_f16 v[122:125], v[226:229], v[206:209], v[122:125]
	v_mfma_f32_16x16x32_f16 v[38:41], v[226:229], v[162:165], v[38:41]
	v_mfma_f32_16x16x32_f16 v[52:55], v[218:221], v[190:193], v[52:55]
	s_setprio 0
	s_mov_b32 m0, s14
	v_lshl_add_u64 v[18:19], v[18:19], 0, s[0:1]
	s_barrier
	ds_read_b128 v[138:141], v2
	ds_read_b128 v[142:145], v3
	ds_read_b128 v[146:149], v4
	ds_read_b128 v[2:5], v5
	global_load_lds_dwordx4 v[18:19], off
	v_lshl_add_u64 v[18:19], v[20:21], 0, s[0:1]
	s_mov_b32 m0, s7
	s_nop 0
	global_load_lds_dwordx4 v[18:19], off
	ds_read_b128 v[18:21], v1
	ds_read_b128 v[150:153], v1 offset:1024
	ds_read_b128 v[154:157], v1 offset:2048
	ds_read_b128 v[158:161], v1 offset:3072
	ds_read_b128 v[162:165], v1 offset:4096
	ds_read_b128 v[166:169], v1 offset:5120
	ds_read_b128 v[186:189], v1 offset:6144
	ds_read_b128 v[190:193], v1 offset:7168
	s_barrier
	s_waitcnt lgkmcnt(0)
	s_setprio 1
	s_waitcnt lgkmcnt(0)
	v_mfma_f32_16x16x32_f16 v[86:89], v[138:141], v[18:21], v[86:89]
	v_mfma_f32_16x16x32_f16 v[90:93], v[146:149], v[18:21], v[90:93]
	v_mfma_f32_16x16x32_f16 v[94:97], v[138:141], v[154:157], v[94:97]
	v_mfma_f32_16x16x32_f16 v[98:101], v[146:149], v[154:157], v[98:101]
	v_mfma_f32_16x16x32_f16 v[102:105], v[138:141], v[162:165], v[102:105]
	v_mfma_f32_16x16x32_f16 v[106:109], v[146:149], v[162:165], v[106:109]
	v_mfma_f32_16x16x32_f16 v[110:113], v[138:141], v[186:189], v[110:113]
	v_mfma_f32_16x16x32_f16 v[86:89], v[142:145], v[150:153], v[86:89]
	v_mfma_f32_16x16x32_f16 v[90:93], v[2:5], v[150:153], v[90:93]
	v_mfma_f32_16x16x32_f16 v[94:97], v[142:145], v[158:161], v[94:97]
	v_mfma_f32_16x16x32_f16 v[98:101], v[2:5], v[158:161], v[98:101]
	v_mfma_f32_16x16x32_f16 v[102:105], v[142:145], v[166:169], v[102:105]
	v_mfma_f32_16x16x32_f16 v[106:109], v[2:5], v[166:169], v[106:109]
	v_mfma_f32_16x16x32_f16 v[110:113], v[142:145], v[190:193], v[110:113]
	v_mfma_f32_16x16x32_f16 v[114:117], v[146:149], v[186:189], v[114:117]
	v_mfma_f32_16x16x32_f16 v[194:197], v[2:5], v[190:193], v[114:117]
	s_setprio 0
	s_barrier
	s_nop 4
	ds_read_b128 v[114:117], v6
	ds_read_b128 v[198:201], v7
	ds_read_b128 v[202:205], v8
	ds_read_b128 v[6:9], v9
	s_barrier
	s_waitcnt lgkmcnt(0)
	s_setprio 1
	s_waitcnt lgkmcnt(0)
	v_mfma_f32_16x16x32_f16 v[30:33], v[114:117], v[18:21], v[30:33]
	v_mfma_f32_16x16x32_f16 v[18:21], v[202:205], v[18:21], v[34:37]
	v_mfma_f32_16x16x32_f16 v[34:37], v[114:117], v[154:157], v[58:61]
	v_mfma_f32_16x16x32_f16 v[56:59], v[202:205], v[154:157], v[62:65]
	v_mfma_f32_16x16x32_f16 v[60:63], v[114:117], v[162:165], v[66:69]
	v_mfma_f32_16x16x32_f16 v[64:67], v[202:205], v[162:165], v[70:73]
	v_mfma_f32_16x16x32_f16 v[68:71], v[114:117], v[186:189], v[74:77]
	v_mfma_f32_16x16x32_f16 v[72:75], v[202:205], v[186:189], v[78:81]
	v_mfma_f32_16x16x32_f16 v[30:33], v[198:201], v[150:153], v[30:33]
	v_mfma_f32_16x16x32_f16 v[18:21], v[6:9], v[150:153], v[18:21]
	v_mfma_f32_16x16x32_f16 v[64:67], v[6:9], v[166:169], v[64:67]
	v_mfma_f32_16x16x32_f16 v[68:71], v[198:201], v[190:193], v[68:71]
	v_mfma_f32_16x16x32_f16 v[72:75], v[6:9], v[190:193], v[72:75]
	v_mfma_f32_16x16x32_f16 v[34:37], v[198:201], v[158:161], v[34:37]
	v_mfma_f32_16x16x32_f16 v[56:59], v[6:9], v[158:161], v[56:59]
	v_mfma_f32_16x16x32_f16 v[60:63], v[198:201], v[166:169], v[60:63]
	s_setprio 0
	s_barrier
	ds_read_b128 v[76:79], v1 offset:16384
	ds_read_b128 v[150:153], v1 offset:17408
	ds_read_b128 v[154:157], v1 offset:18432
	ds_read_b128 v[158:161], v1 offset:19456
	ds_read_b128 v[162:165], v1 offset:20480
	ds_read_b128 v[166:169], v1 offset:21504
	ds_read_b128 v[186:189], v1 offset:22528
	ds_read_b128 v[190:193], v1 offset:23552
	s_waitcnt vmcnt(4)
	s_barrier
	s_waitcnt lgkmcnt(0)
	s_setprio 1
	s_waitcnt lgkmcnt(0)
	v_mfma_f32_16x16x32_f16 v[26:29], v[138:141], v[76:79], v[26:29]
	v_mfma_f32_16x16x32_f16 v[42:45], v[146:149], v[76:79], v[44:47]
	v_mfma_f32_16x16x32_f16 v[174:177], v[146:149], v[154:157], v[174:177]
	v_mfma_f32_16x16x32_f16 v[182:185], v[146:149], v[162:165], v[182:185]
	v_mfma_f32_16x16x32_f16 v[46:49], v[146:149], v[186:189], v[48:51]
	v_mfma_f32_16x16x32_f16 v[26:29], v[142:145], v[150:153], v[26:29]
	v_mfma_f32_16x16x32_f16 v[42:45], v[2:5], v[150:153], v[42:45]
	v_mfma_f32_16x16x32_f16 v[170:173], v[138:141], v[154:157], v[170:173]
	v_mfma_f32_16x16x32_f16 v[174:177], v[2:5], v[158:161], v[174:177]
	v_mfma_f32_16x16x32_f16 v[178:181], v[138:141], v[162:165], v[178:181]
	v_mfma_f32_16x16x32_f16 v[182:185], v[2:5], v[166:169], v[182:185]
	v_mfma_f32_16x16x32_f16 v[126:129], v[138:141], v[186:189], v[126:129]
	v_mfma_f32_16x16x32_f16 v[2:5], v[2:5], v[190:193], v[46:49]
	v_mfma_f32_16x16x32_f16 v[170:173], v[142:145], v[158:161], v[170:173]
	v_mfma_f32_16x16x32_f16 v[178:181], v[142:145], v[166:169], v[178:181]
	v_mfma_f32_16x16x32_f16 v[206:209], v[142:145], v[190:193], v[126:129]
	s_setprio 0
	s_setprio 1
	v_mfma_f32_16x16x32_f16 v[22:25], v[114:117], v[76:79], v[22:25]
	v_mfma_f32_16x16x32_f16 v[46:49], v[198:201], v[150:153], v[22:25]
	v_mfma_f32_16x16x32_f16 v[22:25], v[202:205], v[76:79], v[38:41]
	v_mfma_f32_16x16x32_f16 v[38:41], v[6:9], v[150:153], v[22:25]
	v_mfma_f32_16x16x32_f16 v[22:25], v[114:117], v[154:157], v[52:55]
	v_mfma_f32_16x16x32_f16 v[50:53], v[198:201], v[158:161], v[22:25]
	v_mfma_f32_16x16x32_f16 v[22:25], v[202:205], v[154:157], v[82:85]
	v_mfma_f32_16x16x32_f16 v[146:149], v[6:9], v[158:161], v[22:25]
	v_mfma_f32_16x16x32_f16 v[22:25], v[114:117], v[162:165], v[130:133]
	v_mfma_f32_16x16x32_f16 v[210:213], v[198:201], v[166:169], v[22:25]
	v_mfma_f32_16x16x32_f16 v[22:25], v[202:205], v[162:165], v[134:137]
	v_mfma_f32_16x16x32_f16 v[166:169], v[6:9], v[166:169], v[22:25]
	v_mfma_f32_16x16x32_f16 v[22:25], v[114:117], v[186:189], v[118:121]
	v_mfma_f32_16x16x32_f16 v[198:201], v[198:201], v[190:193], v[22:25]
	v_mfma_f32_16x16x32_f16 v[22:25], v[202:205], v[186:189], v[122:125]
	v_mfma_f32_16x16x32_f16 v[186:189], v[6:9], v[190:193], v[22:25]
	s_setprio 0
	s_barrier
	ds_read_b128 v[6:9], v10
	ds_read_b128 v[76:79], v11
	ds_read_b128 v[190:193], v12
	ds_read_b128 v[10:13], v13
	s_nop 0
	ds_read_b128 v[22:25], v1 offset:32768
	ds_read_b128 v[122:125], v1 offset:33792
	ds_read_b128 v[126:129], v1 offset:34816
	ds_read_b128 v[138:141], v1 offset:35840
	ds_read_b128 v[202:205], v1 offset:36864
	ds_read_b128 v[214:217], v1 offset:37888
	ds_read_b128 v[218:221], v1 offset:38912
	ds_read_b128 v[222:225], v1 offset:39936
	s_waitcnt vmcnt(2)
	s_barrier
	s_waitcnt lgkmcnt(0)
	s_setprio 1
	s_waitcnt lgkmcnt(0)
	v_mfma_f32_16x16x32_f16 v[80:83], v[6:9], v[22:25], v[86:89]
	v_mfma_f32_16x16x32_f16 v[162:165], v[76:79], v[122:125], v[80:83]
	v_mfma_f32_16x16x32_f16 v[80:83], v[190:193], v[22:25], v[90:93]
	v_mfma_f32_16x16x32_f16 v[154:157], v[10:13], v[122:125], v[80:83]
	v_mfma_f32_16x16x32_f16 v[80:83], v[6:9], v[126:129], v[94:97]
	v_mfma_f32_16x16x32_f16 v[134:137], v[76:79], v[138:141], v[80:83]
	v_mfma_f32_16x16x32_f16 v[80:83], v[190:193], v[126:129], v[98:101]
	v_mfma_f32_16x16x32_f16 v[130:133], v[10:13], v[138:141], v[80:83]
	v_mfma_f32_16x16x32_f16 v[80:83], v[6:9], v[202:205], v[102:105]
	v_mfma_f32_16x16x32_f16 v[118:121], v[76:79], v[214:217], v[80:83]
	v_mfma_f32_16x16x32_f16 v[80:83], v[190:193], v[202:205], v[106:109]
	v_mfma_f32_16x16x32_f16 v[114:117], v[10:13], v[214:217], v[80:83]
	v_mfma_f32_16x16x32_f16 v[80:83], v[6:9], v[218:221], v[110:113]
	v_mfma_f32_16x16x32_f16 v[86:89], v[76:79], v[222:225], v[80:83]
	v_mfma_f32_16x16x32_f16 v[80:83], v[190:193], v[218:221], v[194:197]
	v_mfma_f32_16x16x32_f16 v[82:85], v[10:13], v[222:225], v[80:83]
	s_setprio 0
	s_barrier
	ds_read_b128 v[194:197], v14
	ds_read_b128 v[226:229], v15
	ds_read_b128 v[230:233], v16
	ds_read_b128 v[234:237], v17
	s_waitcnt vmcnt(0)
	s_barrier
	s_waitcnt lgkmcnt(0)
	s_setprio 1
	s_waitcnt lgkmcnt(0)
	v_mfma_f32_16x16x32_f16 v[14:17], v[194:197], v[22:25], v[30:33]
	v_mfma_f32_16x16x32_f16 v[158:161], v[226:229], v[122:125], v[14:17]
	v_mfma_f32_16x16x32_f16 v[14:17], v[230:233], v[22:25], v[18:21]
	v_mfma_f32_16x16x32_f16 v[150:153], v[234:237], v[122:125], v[14:17]
	v_mfma_f32_16x16x32_f16 v[14:17], v[194:197], v[126:129], v[34:37]
	v_mfma_f32_16x16x32_f16 v[142:145], v[226:229], v[138:141], v[14:17]
	v_mfma_f32_16x16x32_f16 v[14:17], v[230:233], v[126:129], v[56:59]
	v_mfma_f32_16x16x32_f16 v[138:141], v[234:237], v[138:141], v[14:17]
	v_mfma_f32_16x16x32_f16 v[14:17], v[194:197], v[202:205], v[60:63]
	v_mfma_f32_16x16x32_f16 v[126:129], v[226:229], v[214:217], v[14:17]
	v_mfma_f32_16x16x32_f16 v[14:17], v[230:233], v[202:205], v[64:67]
	v_mfma_f32_16x16x32_f16 v[122:125], v[234:237], v[214:217], v[14:17]
	v_mfma_f32_16x16x32_f16 v[14:17], v[194:197], v[218:221], v[68:71]
	v_mfma_f32_16x16x32_f16 v[98:101], v[226:229], v[222:225], v[14:17]
	v_mfma_f32_16x16x32_f16 v[14:17], v[230:233], v[218:221], v[72:75]
	v_mfma_f32_16x16x32_f16 v[90:93], v[234:237], v[222:225], v[14:17]
	s_setprio 0
	s_barrier
	ds_read_b128 v[30:33], v1 offset:49152
	ds_read_b128 v[34:37], v1 offset:50176
	ds_read_b128 v[54:57], v1 offset:51200
	ds_read_b128 v[58:61], v1 offset:52224
	ds_read_b128 v[62:65], v1 offset:53248
	ds_read_b128 v[202:205], v1 offset:54272
	ds_read_b128 v[214:217], v1 offset:55296
	ds_read_b128 v[218:221], v1 offset:56320
	s_barrier
	s_waitcnt lgkmcnt(0)
	s_setprio 1
	s_waitcnt lgkmcnt(0)
	v_mfma_f32_16x16x32_f16 v[14:17], v[6:9], v[30:33], v[26:29]
	v_mfma_f32_16x16x32_f16 v[102:105], v[76:79], v[34:37], v[14:17]
	v_mfma_f32_16x16x32_f16 v[14:17], v[190:193], v[30:33], v[42:45]
	v_mfma_f32_16x16x32_f16 v[94:97], v[10:13], v[34:37], v[14:17]
	v_mfma_f32_16x16x32_f16 v[14:17], v[6:9], v[54:57], v[170:173]
	v_mfma_f32_16x16x32_f16 v[70:73], v[76:79], v[58:61], v[14:17]
	v_mfma_f32_16x16x32_f16 v[14:17], v[190:193], v[54:57], v[174:177]
	v_mfma_f32_16x16x32_f16 v[66:69], v[10:13], v[58:61], v[14:17]
	v_mfma_f32_16x16x32_f16 v[14:17], v[6:9], v[62:65], v[178:181]
	v_mfma_f32_16x16x32_f16 v[22:25], v[76:79], v[202:205], v[14:17]
	v_mfma_f32_16x16x32_f16 v[14:17], v[190:193], v[62:65], v[182:185]
	v_mfma_f32_16x16x32_f16 v[6:9], v[6:9], v[214:217], v[206:209]
	v_mfma_f32_16x16x32_f16 v[2:5], v[190:193], v[214:217], v[2:5]
	v_mfma_f32_16x16x32_f16 v[18:21], v[10:13], v[202:205], v[14:17]
	v_mfma_f32_16x16x32_f16 v[14:17], v[76:79], v[218:221], v[6:9]
	v_mfma_f32_16x16x32_f16 v[6:9], v[10:13], v[218:221], v[2:5]
	s_setprio 0
	s_setprio 1
	v_mfma_f32_16x16x32_f16 v[2:5], v[194:197], v[30:33], v[46:49]
	v_mfma_f32_16x16x32_f16 v[110:113], v[226:229], v[34:37], v[2:5]
	v_mfma_f32_16x16x32_f16 v[2:5], v[230:233], v[30:33], v[38:41]
	v_mfma_f32_16x16x32_f16 v[106:109], v[234:237], v[34:37], v[2:5]
	v_mfma_f32_16x16x32_f16 v[2:5], v[194:197], v[54:57], v[50:53]
	v_mfma_f32_16x16x32_f16 v[78:81], v[226:229], v[58:61], v[2:5]
	v_mfma_f32_16x16x32_f16 v[2:5], v[230:233], v[54:57], v[146:149]
	v_mfma_f32_16x16x32_f16 v[74:77], v[234:237], v[58:61], v[2:5]
	v_mfma_f32_16x16x32_f16 v[2:5], v[194:197], v[62:65], v[210:213]
	v_mfma_f32_16x16x32_f16 v[30:33], v[226:229], v[202:205], v[2:5]
	v_mfma_f32_16x16x32_f16 v[2:5], v[230:233], v[62:65], v[166:169]
	v_mfma_f32_16x16x32_f16 v[26:29], v[234:237], v[202:205], v[2:5]
	v_mfma_f32_16x16x32_f16 v[2:5], v[194:197], v[214:217], v[198:201]
	v_mfma_f32_16x16x32_f16 v[10:13], v[226:229], v[218:221], v[2:5]
	v_mfma_f32_16x16x32_f16 v[2:5], v[230:233], v[214:217], v[186:189]
	v_mfma_f32_16x16x32_f16 v[2:5], v[234:237], v[218:221], v[2:5]
	s_setprio 0
	s_barrier
	s_add_i32 s0, 0, 0x20800
	v_bfe_u32 v166, v0, 4, 2
	v_bfe_u32 v1, v0, 6, 2
	v_lshlrev_b32_e32 v34, 5, v166
	v_lshl_or_b32 v34, v1, 7, v34
	v_add_u32_e32 v35, s0, v34
	s_add_i32 s1, 0, 0x20c00
	v_add_u32_e32 v36, s1, v34
	ds_read_b128 v[58:61], v35
	ds_read_b128 v[62:65], v36
	v_or_b32_e32 v35, 16, v34
	v_add_u32_e32 v36, s0, v35
	v_add_u32_e32 v35, s1, v35
	ds_read_b128 v[50:53], v36
	ds_read_b128 v[54:57], v35
	v_or_b32_e32 v35, 0x200, v34
	v_add_u32_e32 v36, s0, v35
	v_add_u32_e32 v35, s1, v35
	v_or_b32_e32 v34, 0x210, v34
	ds_read_b128 v[42:45], v36
	ds_read_b128 v[46:49], v35
	v_add_u32_e32 v35, s0, v34
	v_and_b32_e32 v146, 15, v0
	v_ashrrev_i32_e32 v0, 2, v0
	s_movk_i32 s0, 0xffc0
	v_and_or_b32 v168, v0, s0, v146
	s_add_i32 s0, 0, 0x20000
	v_add_u32_e32 v38, s1, v34
	v_lshl_add_u32 v169, v168, 3, s0
	ds_read_b128 v[34:37], v35
	ds_read_b128 v[38:41], v38
	s_waitcnt vmcnt(0)
	ds_read2st64_b64 v[146:149], v169 offset1:2
	v_lshlrev_b32_e32 v0, 5, v1
	v_lshlrev_b32_e32 v1, 3, v166
	v_or3_b32 v166, v0, v1, s13
	v_add_u32_e32 v167, s12, v168
	s_waitcnt lgkmcnt(0)
	v_pk_fma_f32 v[0:1], v[146:147], v[58:59], v[162:163] op_sel_hi:[0,1,1] neg_lo:[1,0,0] neg_hi:[1,0,0]
	v_pk_fma_f32 v[0:1], v[146:147], v[0:1], v[62:63] op_sel:[1,0,0]
	v_mul_lo_u32 v170, v167, s6
	v_cvt_pk_f16_f32 v162, v0, v1
	v_pk_fma_f32 v[0:1], v[146:147], v[60:61], v[164:165] op_sel_hi:[0,1,1] neg_lo:[1,0,0] neg_hi:[1,0,0]
	v_pk_fma_f32 v[0:1], v[146:147], v[0:1], v[64:65] op_sel:[1,0,0]
	s_and_b32 s9, s9, 0xffff
	v_cvt_pk_f16_f32 v163, v0, v1
	v_pk_fma_f32 v[0:1], v[146:147], v[50:51], v[154:155] op_sel_hi:[0,1,1] neg_lo:[1,0,0] neg_hi:[1,0,0]
	v_pk_fma_f32 v[0:1], v[146:147], v[0:1], v[54:55] op_sel:[1,0,0]
	s_mov_b32 s11, 0x20000
	v_cvt_pk_f16_f32 v164, v0, v1
	v_pk_fma_f32 v[0:1], v[146:147], v[52:53], v[156:157] op_sel_hi:[0,1,1] neg_lo:[1,0,0] neg_hi:[1,0,0]
	v_pk_fma_f32 v[0:1], v[146:147], v[0:1], v[56:57] op_sel:[1,0,0]
	s_mov_b32 s10, 0x7ffffff0
	v_cvt_pk_f16_f32 v165, v0, v1
	v_pk_fma_f32 v[0:1], v[146:147], v[42:43], v[158:159] op_sel_hi:[0,1,1] neg_lo:[1,0,0] neg_hi:[1,0,0]
	v_pk_fma_f32 v[0:1], v[146:147], v[0:1], v[46:47] op_sel:[1,0,0]
	v_add_lshl_u32 v170, v166, v170, 1
	v_cvt_pk_f16_f32 v154, v0, v1
	v_pk_fma_f32 v[0:1], v[146:147], v[44:45], v[160:161] op_sel_hi:[0,1,1] neg_lo:[1,0,0] neg_hi:[1,0,0]
	v_pk_fma_f32 v[0:1], v[146:147], v[0:1], v[48:49] op_sel:[1,0,0]
	buffer_store_dwordx4 v[162:165], v170, s[8:11], 0 offen sc1
	v_cvt_pk_f16_f32 v155, v0, v1
	v_pk_fma_f32 v[0:1], v[146:147], v[34:35], v[150:151] op_sel_hi:[0,1,1] neg_lo:[1,0,0] neg_hi:[1,0,0]
	v_pk_fma_f32 v[0:1], v[146:147], v[0:1], v[38:39] op_sel:[1,0,0]
	s_nop 0
	v_cvt_pk_f16_f32 v156, v0, v1
	v_pk_fma_f32 v[0:1], v[146:147], v[36:37], v[152:153] op_sel_hi:[0,1,1] neg_lo:[1,0,0] neg_hi:[1,0,0]
	v_pk_fma_f32 v[0:1], v[146:147], v[0:1], v[40:41] op_sel:[1,0,0]
	s_nop 0
	v_cvt_pk_f16_f32 v157, v0, v1
	v_or_b32_e32 v0, 16, v168
	v_add_u32_e32 v146, s12, v0
	v_lshl_add_u32 v0, v0, 3, s0
	ds_read_b64 v[0:1], v0
	buffer_store_dwordx4 v[154:157], v170, s[8:11], 0 offen offset:256 sc1
	s_waitcnt lgkmcnt(0)
	v_pk_fma_f32 v[134:135], v[0:1], v[58:59], v[134:135] op_sel_hi:[0,1,1] neg_lo:[1,0,0] neg_hi:[1,0,0]
	v_pk_fma_f32 v[136:137], v[0:1], v[60:61], v[136:137] op_sel_hi:[0,1,1] neg_lo:[1,0,0] neg_hi:[1,0,0]
	v_pk_fma_f32 v[130:131], v[0:1], v[50:51], v[130:131] op_sel_hi:[0,1,1] neg_lo:[1,0,0] neg_hi:[1,0,0]
	v_pk_fma_f32 v[134:135], v[0:1], v[134:135], v[62:63] op_sel:[1,0,0]
	v_pk_fma_f32 v[136:137], v[0:1], v[136:137], v[64:65] op_sel:[1,0,0]
	v_pk_fma_f32 v[130:131], v[0:1], v[130:131], v[54:55] op_sel:[1,0,0]
	v_cvt_pk_f16_f32 v134, v134, v135
	v_cvt_pk_f16_f32 v135, v136, v137
	v_cvt_pk_f16_f32 v136, v130, v131
	v_pk_fma_f32 v[130:131], v[0:1], v[52:53], v[132:133] op_sel_hi:[0,1,1] neg_lo:[1,0,0] neg_hi:[1,0,0]
	v_pk_fma_f32 v[130:131], v[0:1], v[130:131], v[56:57] op_sel:[1,0,0]
	v_mul_lo_u32 v154, v146, s6
	v_or_b32_e32 v155, 32, v168
	v_or_b32_e32 v156, 48, v168
	v_cvt_pk_f16_f32 v137, v130, v131
	v_pk_fma_f32 v[130:131], v[0:1], v[42:43], v[142:143] op_sel_hi:[0,1,1] neg_lo:[1,0,0] neg_hi:[1,0,0]
	v_pk_fma_f32 v[132:133], v[0:1], v[44:45], v[144:145] op_sel_hi:[0,1,1] neg_lo:[1,0,0] neg_hi:[1,0,0]
	v_lshl_add_u32 v146, v155, 3, s0
	v_lshl_add_u32 v147, v156, 3, s0
	v_add_lshl_u32 v154, v166, v154, 1
	v_pk_fma_f32 v[130:131], v[0:1], v[130:131], v[46:47] op_sel:[1,0,0]
	v_pk_fma_f32 v[132:133], v[0:1], v[132:133], v[48:49] op_sel:[1,0,0]
	ds_read_b64 v[150:151], v146
	ds_read_b64 v[146:147], v147
	ds_read_b64 v[152:153], v169 offset:1408
	buffer_store_dwordx4 v[134:137], v154, s[8:11], 0 offen sc1
	v_cvt_pk_f16_f32 v130, v130, v131
	v_cvt_pk_f16_f32 v131, v132, v133
	v_pk_fma_f32 v[132:133], v[0:1], v[34:35], v[138:139] op_sel_hi:[0,1,1] neg_lo:[1,0,0] neg_hi:[1,0,0]
	v_pk_fma_f32 v[134:135], v[0:1], v[36:37], v[140:141] op_sel_hi:[0,1,1] neg_lo:[1,0,0] neg_hi:[1,0,0]
	v_pk_fma_f32 v[132:133], v[0:1], v[132:133], v[38:39] op_sel:[1,0,0]
	v_pk_fma_f32 v[0:1], v[0:1], v[134:135], v[40:41] op_sel:[1,0,0]
	v_cvt_pk_f16_f32 v132, v132, v133
	v_cvt_pk_f16_f32 v133, v0, v1
	v_add_u32_e32 v0, s12, v155
	buffer_store_dwordx4 v[130:133], v154, s[8:11], 0 offen offset:256 sc1
	s_waitcnt lgkmcnt(0)
	v_pk_fma_f32 v[2:3], v[152:153], v[34:35], v[2:3] op_sel_hi:[0,1,1] neg_lo:[1,0,0] neg_hi:[1,0,0]
	v_pk_fma_f32 v[4:5], v[152:153], v[36:37], v[4:5] op_sel_hi:[0,1,1] neg_lo:[1,0,0] neg_hi:[1,0,0]
	v_mul_lo_u32 v130, v0, s6
	v_pk_fma_f32 v[0:1], v[150:151], v[58:59], v[118:119] op_sel_hi:[0,1,1] neg_lo:[1,0,0] neg_hi:[1,0,0]
	v_pk_fma_f32 v[0:1], v[150:151], v[0:1], v[62:63] op_sel:[1,0,0]
	v_add_lshl_u32 v130, v166, v130, 1
	v_cvt_pk_f16_f32 v118, v0, v1
	v_pk_fma_f32 v[0:1], v[150:151], v[60:61], v[120:121] op_sel_hi:[0,1,1] neg_lo:[1,0,0] neg_hi:[1,0,0]
	v_pk_fma_f32 v[0:1], v[150:151], v[0:1], v[64:65] op_sel:[1,0,0]
	v_pk_fma_f32 v[2:3], v[152:153], v[2:3], v[38:39] op_sel:[1,0,0]
	v_cvt_pk_f16_f32 v119, v0, v1
	v_pk_fma_f32 v[0:1], v[150:151], v[50:51], v[114:115] op_sel_hi:[0,1,1] neg_lo:[1,0,0] neg_hi:[1,0,0]
	v_pk_fma_f32 v[0:1], v[150:151], v[0:1], v[54:55] op_sel:[1,0,0]
	v_pk_fma_f32 v[4:5], v[152:153], v[4:5], v[40:41] op_sel:[1,0,0]
	v_cvt_pk_f16_f32 v120, v0, v1
	v_pk_fma_f32 v[0:1], v[150:151], v[52:53], v[116:117] op_sel_hi:[0,1,1] neg_lo:[1,0,0] neg_hi:[1,0,0]
	v_pk_fma_f32 v[0:1], v[150:151], v[0:1], v[56:57] op_sel:[1,0,0]
	v_cvt_pk_f16_f32 v2, v2, v3
	v_cvt_pk_f16_f32 v121, v0, v1
	v_pk_fma_f32 v[0:1], v[150:151], v[42:43], v[126:127] op_sel_hi:[0,1,1] neg_lo:[1,0,0] neg_hi:[1,0,0]
	v_pk_fma_f32 v[0:1], v[150:151], v[0:1], v[46:47] op_sel:[1,0,0]
	buffer_store_dwordx4 v[118:121], v130, s[8:11], 0 offen sc1
	v_cvt_pk_f16_f32 v114, v0, v1
	v_pk_fma_f32 v[0:1], v[150:151], v[44:45], v[128:129] op_sel_hi:[0,1,1] neg_lo:[1,0,0] neg_hi:[1,0,0]
	v_pk_fma_f32 v[0:1], v[150:151], v[0:1], v[48:49] op_sel:[1,0,0]
	v_cvt_pk_f16_f32 v3, v4, v5
	v_cvt_pk_f16_f32 v115, v0, v1
	v_pk_fma_f32 v[0:1], v[150:151], v[34:35], v[122:123] op_sel_hi:[0,1,1] neg_lo:[1,0,0] neg_hi:[1,0,0]
	v_pk_fma_f32 v[0:1], v[150:151], v[0:1], v[38:39] op_sel:[1,0,0]
	s_nop 0
	v_cvt_pk_f16_f32 v116, v0, v1
	v_pk_fma_f32 v[0:1], v[150:151], v[36:37], v[124:125] op_sel_hi:[0,1,1] neg_lo:[1,0,0] neg_hi:[1,0,0]
	v_pk_fma_f32 v[0:1], v[150:151], v[0:1], v[40:41] op_sel:[1,0,0]
	s_nop 0
	v_cvt_pk_f16_f32 v117, v0, v1
	v_add_u32_e32 v0, s12, v156
	buffer_store_dwordx4 v[114:117], v130, s[8:11], 0 offen offset:256 sc1
	s_and_saveexec_b64 s[44:45], vcc
	s_cbranch_execz .LBB6_34
	s_barrier
.LBB6_34:
	s_or_b64 exec, exec, s[44:45]
	s_nop 1
	v_mul_lo_u32 v114, v0, s6
	v_pk_fma_f32 v[0:1], v[146:147], v[58:59], v[86:87] op_sel_hi:[0,1,1] neg_lo:[1,0,0] neg_hi:[1,0,0]
	v_pk_fma_f32 v[0:1], v[146:147], v[0:1], v[62:63] op_sel:[1,0,0]
	v_add_lshl_u32 v114, v166, v114, 1
	v_cvt_pk_f16_f32 v86, v0, v1
	v_pk_fma_f32 v[0:1], v[146:147], v[60:61], v[88:89] op_sel_hi:[0,1,1] neg_lo:[1,0,0] neg_hi:[1,0,0]
	v_pk_fma_f32 v[0:1], v[146:147], v[0:1], v[64:65] op_sel:[1,0,0]
	s_nop 0
	v_cvt_pk_f16_f32 v87, v0, v1
	v_pk_fma_f32 v[0:1], v[146:147], v[50:51], v[82:83] op_sel_hi:[0,1,1] neg_lo:[1,0,0] neg_hi:[1,0,0]
	v_pk_fma_f32 v[0:1], v[146:147], v[0:1], v[54:55] op_sel:[1,0,0]
	s_nop 0
	v_cvt_pk_f16_f32 v88, v0, v1
	v_pk_fma_f32 v[0:1], v[146:147], v[52:53], v[84:85] op_sel_hi:[0,1,1] neg_lo:[1,0,0] neg_hi:[1,0,0]
	v_pk_fma_f32 v[0:1], v[146:147], v[0:1], v[56:57] op_sel:[1,0,0]
	s_nop 0
	v_cvt_pk_f16_f32 v89, v0, v1
	v_pk_fma_f32 v[0:1], v[146:147], v[42:43], v[98:99] op_sel_hi:[0,1,1] neg_lo:[1,0,0] neg_hi:[1,0,0]
	v_pk_fma_f32 v[0:1], v[146:147], v[0:1], v[46:47] op_sel:[1,0,0]
	buffer_store_dwordx4 v[86:89], v114, s[8:11], 0 offen sc1
	v_cvt_pk_f16_f32 v82, v0, v1
	v_pk_fma_f32 v[0:1], v[146:147], v[44:45], v[100:101] op_sel_hi:[0,1,1] neg_lo:[1,0,0] neg_hi:[1,0,0]
	v_pk_fma_f32 v[0:1], v[146:147], v[0:1], v[48:49] op_sel:[1,0,0]
	s_nop 0
	v_cvt_pk_f16_f32 v83, v0, v1
	v_pk_fma_f32 v[0:1], v[146:147], v[34:35], v[90:91] op_sel_hi:[0,1,1] neg_lo:[1,0,0] neg_hi:[1,0,0]
	v_pk_fma_f32 v[0:1], v[146:147], v[0:1], v[38:39] op_sel:[1,0,0]
	s_nop 0
	v_cvt_pk_f16_f32 v84, v0, v1
	v_pk_fma_f32 v[0:1], v[146:147], v[36:37], v[92:93] op_sel_hi:[0,1,1] neg_lo:[1,0,0] neg_hi:[1,0,0]
	v_pk_fma_f32 v[0:1], v[146:147], v[0:1], v[40:41] op_sel:[1,0,0]
	s_nop 0
	v_cvt_pk_f16_f32 v85, v0, v1
	v_add_u32_e32 v0, 0x80, v167
	v_mul_lo_u32 v86, v0, s6
	v_pk_fma_f32 v[0:1], v[148:149], v[58:59], v[102:103] op_sel_hi:[0,1,1] neg_lo:[1,0,0] neg_hi:[1,0,0]
	v_pk_fma_f32 v[0:1], v[148:149], v[0:1], v[62:63] op_sel:[1,0,0]
	buffer_store_dwordx4 v[82:85], v114, s[8:11], 0 offen offset:256 sc1
	v_add_lshl_u32 v90, v166, v86, 1
	ds_read2_b64 v[86:89], v169 offset0:144 offset1:160
	v_cvt_pk_f16_f32 v82, v0, v1
	v_pk_fma_f32 v[0:1], v[148:149], v[60:61], v[104:105] op_sel_hi:[0,1,1] neg_lo:[1,0,0] neg_hi:[1,0,0]
	v_pk_fma_f32 v[0:1], v[148:149], v[0:1], v[64:65] op_sel:[1,0,0]
	s_nop 0
	v_cvt_pk_f16_f32 v83, v0, v1
	v_pk_fma_f32 v[0:1], v[148:149], v[50:51], v[94:95] op_sel_hi:[0,1,1] neg_lo:[1,0,0] neg_hi:[1,0,0]
	v_pk_fma_f32 v[0:1], v[148:149], v[0:1], v[54:55] op_sel:[1,0,0]
	s_nop 0
	v_cvt_pk_f16_f32 v84, v0, v1
	v_pk_fma_f32 v[0:1], v[148:149], v[52:53], v[96:97] op_sel_hi:[0,1,1] neg_lo:[1,0,0] neg_hi:[1,0,0]
	v_pk_fma_f32 v[0:1], v[148:149], v[0:1], v[56:57] op_sel:[1,0,0]
	s_nop 0
	v_cvt_pk_f16_f32 v85, v0, v1
	v_pk_fma_f32 v[0:1], v[148:149], v[42:43], v[110:111] op_sel_hi:[0,1,1] neg_lo:[1,0,0] neg_hi:[1,0,0]
	v_pk_fma_f32 v[0:1], v[148:149], v[0:1], v[46:47] op_sel:[1,0,0]
	buffer_store_dwordx4 v[82:85], v90, s[8:11], 0 offen sc1
	s_nop 1
	v_cvt_pk_f16_f32 v82, v0, v1
	v_pk_fma_f32 v[0:1], v[148:149], v[44:45], v[112:113] op_sel_hi:[0,1,1] neg_lo:[1,0,0] neg_hi:[1,0,0]
	v_pk_fma_f32 v[0:1], v[148:149], v[0:1], v[48:49] op_sel:[1,0,0]
	s_nop 0
	v_cvt_pk_f16_f32 v83, v0, v1
	v_pk_fma_f32 v[0:1], v[148:149], v[34:35], v[106:107] op_sel_hi:[0,1,1] neg_lo:[1,0,0] neg_hi:[1,0,0]
	v_pk_fma_f32 v[0:1], v[148:149], v[0:1], v[38:39] op_sel:[1,0,0]
	s_nop 0
	v_cvt_pk_f16_f32 v84, v0, v1
	v_pk_fma_f32 v[0:1], v[148:149], v[36:37], v[108:109] op_sel_hi:[0,1,1] neg_lo:[1,0,0] neg_hi:[1,0,0]
	v_pk_fma_f32 v[0:1], v[148:149], v[0:1], v[40:41] op_sel:[1,0,0]
	s_nop 0
	v_cvt_pk_f16_f32 v85, v0, v1
	v_add_u32_e32 v0, 0x90, v167
	buffer_store_dwordx4 v[82:85], v90, s[8:11], 0 offen offset:256 sc1
	s_nop 1
	v_mul_lo_u32 v82, v0, s6
	s_waitcnt lgkmcnt(0)
	v_pk_fma_f32 v[0:1], v[86:87], v[58:59], v[70:71] op_sel_hi:[0,1,1] neg_lo:[1,0,0] neg_hi:[1,0,0]
	v_pk_fma_f32 v[0:1], v[86:87], v[0:1], v[62:63] op_sel:[1,0,0]
	v_add_lshl_u32 v82, v166, v82, 1
	v_cvt_pk_f16_f32 v70, v0, v1
	v_pk_fma_f32 v[0:1], v[86:87], v[60:61], v[72:73] op_sel_hi:[0,1,1] neg_lo:[1,0,0] neg_hi:[1,0,0]
	v_pk_fma_f32 v[0:1], v[86:87], v[0:1], v[64:65] op_sel:[1,0,0]
	s_nop 0
	v_cvt_pk_f16_f32 v71, v0, v1
	v_pk_fma_f32 v[0:1], v[86:87], v[50:51], v[66:67] op_sel_hi:[0,1,1] neg_lo:[1,0,0] neg_hi:[1,0,0]
	v_pk_fma_f32 v[0:1], v[86:87], v[0:1], v[54:55] op_sel:[1,0,0]
	s_nop 0
	v_cvt_pk_f16_f32 v72, v0, v1
	v_pk_fma_f32 v[0:1], v[86:87], v[52:53], v[68:69] op_sel_hi:[0,1,1] neg_lo:[1,0,0] neg_hi:[1,0,0]
	v_pk_fma_f32 v[0:1], v[86:87], v[0:1], v[56:57] op_sel:[1,0,0]
	s_nop 0
	v_cvt_pk_f16_f32 v73, v0, v1
	v_pk_fma_f32 v[0:1], v[86:87], v[42:43], v[78:79] op_sel_hi:[0,1,1] neg_lo:[1,0,0] neg_hi:[1,0,0]
	v_pk_fma_f32 v[0:1], v[86:87], v[0:1], v[46:47] op_sel:[1,0,0]
	buffer_store_dwordx4 v[70:73], v82, s[8:11], 0 offen sc1
	v_cvt_pk_f16_f32 v66, v0, v1
	v_pk_fma_f32 v[0:1], v[86:87], v[44:45], v[80:81] op_sel_hi:[0,1,1] neg_lo:[1,0,0] neg_hi:[1,0,0]
	v_pk_fma_f32 v[0:1], v[86:87], v[0:1], v[48:49] op_sel:[1,0,0]
	s_nop 0
	v_cvt_pk_f16_f32 v67, v0, v1
	v_pk_fma_f32 v[0:1], v[86:87], v[34:35], v[74:75] op_sel_hi:[0,1,1] neg_lo:[1,0,0] neg_hi:[1,0,0]
	v_pk_fma_f32 v[0:1], v[86:87], v[0:1], v[38:39] op_sel:[1,0,0]
	s_nop 0
	v_cvt_pk_f16_f32 v68, v0, v1
	v_pk_fma_f32 v[0:1], v[86:87], v[36:37], v[76:77] op_sel_hi:[0,1,1] neg_lo:[1,0,0] neg_hi:[1,0,0]
	v_pk_fma_f32 v[0:1], v[86:87], v[0:1], v[40:41] op_sel:[1,0,0]
	s_nop 0
	v_cvt_pk_f16_f32 v69, v0, v1
	v_add_u32_e32 v0, 0xa0, v167
	buffer_store_dwordx4 v[66:69], v82, s[8:11], 0 offen offset:256 sc1
	s_nop 1
	v_mul_lo_u32 v66, v0, s6
	v_pk_fma_f32 v[0:1], v[88:89], v[58:59], v[22:23] op_sel_hi:[0,1,1] neg_lo:[1,0,0] neg_hi:[1,0,0]
	v_pk_fma_f32 v[0:1], v[88:89], v[0:1], v[62:63] op_sel:[1,0,0]
	v_add_lshl_u32 v66, v166, v66, 1
	v_cvt_pk_f16_f32 v22, v0, v1
	v_pk_fma_f32 v[0:1], v[88:89], v[60:61], v[24:25] op_sel_hi:[0,1,1] neg_lo:[1,0,0] neg_hi:[1,0,0]
	v_pk_fma_f32 v[0:1], v[88:89], v[0:1], v[64:65] op_sel:[1,0,0]
	s_nop 0
	v_cvt_pk_f16_f32 v23, v0, v1
	v_pk_fma_f32 v[0:1], v[88:89], v[50:51], v[18:19] op_sel_hi:[0,1,1] neg_lo:[1,0,0] neg_hi:[1,0,0]
	v_pk_fma_f32 v[0:1], v[88:89], v[0:1], v[54:55] op_sel:[1,0,0]
	s_nop 0
	v_cvt_pk_f16_f32 v24, v0, v1
	v_pk_fma_f32 v[0:1], v[88:89], v[52:53], v[20:21] op_sel_hi:[0,1,1] neg_lo:[1,0,0] neg_hi:[1,0,0]
	v_pk_fma_f32 v[0:1], v[88:89], v[0:1], v[56:57] op_sel:[1,0,0]
	s_nop 0
	v_cvt_pk_f16_f32 v25, v0, v1
	v_pk_fma_f32 v[0:1], v[88:89], v[42:43], v[30:31] op_sel_hi:[0,1,1] neg_lo:[1,0,0] neg_hi:[1,0,0]
	v_pk_fma_f32 v[0:1], v[88:89], v[0:1], v[46:47] op_sel:[1,0,0]
	buffer_store_dwordx4 v[22:25], v66, s[8:11], 0 offen sc1
	v_cvt_pk_f16_f32 v18, v0, v1
	v_pk_fma_f32 v[0:1], v[88:89], v[44:45], v[32:33] op_sel_hi:[0,1,1] neg_lo:[1,0,0] neg_hi:[1,0,0]
	v_pk_fma_f32 v[0:1], v[88:89], v[0:1], v[48:49] op_sel:[1,0,0]
	s_nop 0
	v_cvt_pk_f16_f32 v19, v0, v1
	v_pk_fma_f32 v[0:1], v[88:89], v[34:35], v[26:27] op_sel_hi:[0,1,1] neg_lo:[1,0,0] neg_hi:[1,0,0]
	v_pk_fma_f32 v[0:1], v[88:89], v[0:1], v[38:39] op_sel:[1,0,0]
	s_nop 0
	v_cvt_pk_f16_f32 v20, v0, v1
	v_pk_fma_f32 v[0:1], v[88:89], v[36:37], v[28:29] op_sel_hi:[0,1,1] neg_lo:[1,0,0] neg_hi:[1,0,0]
	v_pk_fma_f32 v[0:1], v[88:89], v[0:1], v[40:41] op_sel:[1,0,0]
	s_nop 0
	v_cvt_pk_f16_f32 v21, v0, v1
	v_add_u32_e32 v0, 0xb0, v167
	buffer_store_dwordx4 v[18:21], v66, s[8:11], 0 offen offset:256 sc1
	s_nop 1
	v_mul_lo_u32 v18, v0, s6
	v_pk_fma_f32 v[0:1], v[152:153], v[58:59], v[14:15] op_sel_hi:[0,1,1] neg_lo:[1,0,0] neg_hi:[1,0,0]
	v_pk_fma_f32 v[0:1], v[152:153], v[0:1], v[62:63] op_sel:[1,0,0]
	s_nop 0
	v_cvt_pk_f16_f32 v14, v0, v1
	v_pk_fma_f32 v[0:1], v[152:153], v[60:61], v[16:17] op_sel_hi:[0,1,1] neg_lo:[1,0,0] neg_hi:[1,0,0]
	v_pk_fma_f32 v[0:1], v[152:153], v[0:1], v[64:65] op_sel:[1,0,0]
	s_nop 0
	v_cvt_pk_f16_f32 v15, v0, v1
	v_pk_fma_f32 v[0:1], v[152:153], v[50:51], v[6:7] op_sel_hi:[0,1,1] neg_lo:[1,0,0] neg_hi:[1,0,0]
	v_pk_fma_f32 v[0:1], v[152:153], v[0:1], v[54:55] op_sel:[1,0,0]
	v_pk_fma_f32 v[6:7], v[152:153], v[44:45], v[12:13] op_sel_hi:[0,1,1] neg_lo:[1,0,0] neg_hi:[1,0,0]
	v_cvt_pk_f16_f32 v16, v0, v1
	v_pk_fma_f32 v[0:1], v[152:153], v[52:53], v[8:9] op_sel_hi:[0,1,1] neg_lo:[1,0,0] neg_hi:[1,0,0]
	v_pk_fma_f32 v[0:1], v[152:153], v[0:1], v[56:57] op_sel:[1,0,0]
	v_pk_fma_f32 v[6:7], v[152:153], v[6:7], v[48:49] op_sel:[1,0,0]
	v_cvt_pk_f16_f32 v17, v0, v1
	v_pk_fma_f32 v[0:1], v[152:153], v[42:43], v[10:11] op_sel_hi:[0,1,1] neg_lo:[1,0,0] neg_hi:[1,0,0]
	v_pk_fma_f32 v[0:1], v[152:153], v[0:1], v[46:47] op_sel:[1,0,0]
	v_add_lshl_u32 v8, v166, v18, 1
	v_cvt_pk_f16_f32 v0, v0, v1
	v_cvt_pk_f16_f32 v1, v6, v7
	buffer_store_dwordx4 v[14:17], v8, s[8:11], 0 offen sc1
	buffer_store_dwordx4 v[0:3], v8, s[8:11], 0 offen offset:256 sc1
	s_endpgm

.LBB8_6:
	s_or_b64 exec, exec, s[2:3]
	s_add_i32 s0, 0, 0x18000
	v_add_u32_e32 v48, s0, v38
	s_mov_b64 s[0:1], 0x80
	v_readfirstlane_b32 s22, v48
	v_add_u32_e32 v49, 0x2000, v48
	v_lshl_add_u64 v[2:3], v[30:31], 0, s[0:1]
	s_mov_b32 m0, s22
	v_readfirstlane_b32 s21, v49
	v_add_u32_e32 v46, 0x8000, v35
	s_waitcnt vmcnt(4)
	s_barrier
	global_load_lds_dwordx4 v[2:3], off
	v_lshl_add_u64 v[2:3], v[32:33], 0, s[0:1]
	s_mov_b32 m0, s21
	v_readfirstlane_b32 s19, v46
	v_add_u32_e32 v47, 0xa000, v35
	s_add_i32 s2, 0, 0x1c000
	global_load_lds_dwordx4 v[2:3], off
	v_lshl_add_u64 v[2:3], v[26:27], 0, s[0:1]
	s_mov_b32 m0, s19
	v_readfirstlane_b32 s16, v47
	v_add_u32_e32 v37, s2, v38
	global_load_lds_dwordx4 v[2:3], off
	v_lshl_add_u64 v[2:3], v[28:29], 0, s[0:1]
	s_mov_b32 m0, s16
	v_readfirstlane_b32 s3, v37
	v_add_u32_e32 v39, 0x2000, v37
	global_load_lds_dwordx4 v[2:3], off
	v_lshl_add_u64 v[2:3], v[22:23], 0, s[0:1]
	s_mov_b32 m0, s3
	v_readfirstlane_b32 s2, v39
	global_load_lds_dwordx4 v[2:3], off
	v_lshl_add_u64 v[2:3], v[24:25], 0, s[0:1]
	s_mov_b32 m0, s2
	v_lshlrev_b32_e32 v1, 6, v0
	global_load_lds_dwordx4 v[2:3], off
	v_lshlrev_b32_e32 v4, 2, v0
	v_and_b32_e32 v2, 0x3c0, v1
	v_and_b32_e32 v3, 48, v0
	v_and_b32_e32 v4, 32, v4
	v_bitop3_b32 v6, v2, v4, v3 bitop3:0x36
	v_and_b32_e32 v1, 0x3000, v1
	v_add3_u32 v234, 0, v1, v6
	v_add_u32_e32 v2, 0x10000, v234
	v_add_u32_e32 v4, 0x10800, v234
	s_waitcnt vmcnt(6)
	s_barrier
	v_add_u32_e32 v3, 0x10400, v234
	ds_read_b128 v[10:13], v2
	ds_read_b128 v[14:17], v3
	v_add_u32_e32 v5, 0x10c00, v234
	ds_read_b128 v[50:53], v4
	ds_read_b128 v[54:57], v5
	v_lshlrev_b32_e32 v1, 5, v0
	v_and_b32_e32 v1, 0x2000, v1
	v_add3_u32 v1, 0, v1, v6
	v_add_u32_e32 v38, 0xc000, v35
	v_add_u32_e32 v40, 0xe000, v35
	v_readfirstlane_b32 s7, v38
	v_lshl_add_u64 v[6:7], v[18:19], 0, s[0:1]
	s_mov_b32 m0, s7
	v_readfirstlane_b32 s4, v40
	global_load_lds_dwordx4 v[6:7], off
	v_lshl_add_u64 v[6:7], v[20:21], 0, s[0:1]
	s_mov_b32 m0, s4
	s_nop 0
	global_load_lds_dwordx4 v[6:7], off
	ds_read_b128 v[42:45], v1
	ds_read_b128 v[58:61], v1 offset:1024
	ds_read_b128 v[62:65], v1 offset:2048
	ds_read_b128 v[66:69], v1 offset:3072
	ds_read_b128 v[70:73], v1 offset:4096
	ds_read_b128 v[74:77], v1 offset:5120
	ds_read_b128 v[78:81], v1 offset:6144
	ds_read_b128 v[82:85], v1 offset:7168
	s_waitcnt lgkmcnt(8)
	s_barrier
	s_waitcnt lgkmcnt(0)
	s_setprio 1
	s_waitcnt lgkmcnt(0)
	v_mfma_f32_16x16x32_f16 v[6:9], v[10:13], v[42:45], 0
	v_mfma_f32_16x16x32_f16 v[86:89], v[14:17], v[58:61], v[6:9]
	v_mfma_f32_16x16x32_f16 v[6:9], v[50:53], v[42:45], 0
	v_mfma_f32_16x16x32_f16 v[90:93], v[54:57], v[58:61], v[6:9]
	v_mfma_f32_16x16x32_f16 v[6:9], v[10:13], v[62:65], 0
	v_mfma_f32_16x16x32_f16 v[94:97], v[14:17], v[66:69], v[6:9]
	v_mfma_f32_16x16x32_f16 v[6:9], v[50:53], v[62:65], 0
	v_mfma_f32_16x16x32_f16 v[98:101], v[54:57], v[66:69], v[6:9]
	v_mfma_f32_16x16x32_f16 v[6:9], v[10:13], v[70:73], 0
	v_mfma_f32_16x16x32_f16 v[102:105], v[14:17], v[74:77], v[6:9]
	v_mfma_f32_16x16x32_f16 v[6:9], v[50:53], v[70:73], 0
	v_mfma_f32_16x16x32_f16 v[106:109], v[54:57], v[74:77], v[6:9]
	v_mfma_f32_16x16x32_f16 v[6:9], v[10:13], v[78:81], 0
	v_mfma_f32_16x16x32_f16 v[110:113], v[14:17], v[82:85], v[6:9]
	v_mfma_f32_16x16x32_f16 v[6:9], v[50:53], v[78:81], 0
	v_mfma_f32_16x16x32_f16 v[114:117], v[54:57], v[82:85], v[6:9]
	s_setprio 0
	s_barrier
	s_mov_b64 s[0:1], 0x100
	v_readfirstlane_b32 s15, v36
	v_add_u32_e32 v41, 0x2000, v36
	s_nop 1
	v_add_u32_e32 v6, 0x14000, v234
	v_add_u32_e32 v8, 0x14800, v234
	v_lshl_add_u64 v[134:135], v[30:31], 0, s[0:1]
	s_mov_b32 m0, s15
	v_readfirstlane_b32 s5, v41
	v_add_u32_e32 v7, 0x14400, v234
	ds_read_b128 v[118:121], v6
	ds_read_b128 v[122:125], v7
	v_add_u32_e32 v9, 0x14c00, v234
	ds_read_b128 v[126:129], v8
	ds_read_b128 v[130:133], v9
	global_load_lds_dwordx4 v[134:135], off
	v_lshl_add_u64 v[134:135], v[32:33], 0, s[0:1]
	s_mov_b32 m0, s5
	s_nop 0
	global_load_lds_dwordx4 v[134:135], off
	s_barrier
	s_waitcnt lgkmcnt(0)
	s_setprio 1
	s_waitcnt lgkmcnt(0)
	v_mfma_f32_16x16x32_f16 v[134:137], v[118:121], v[42:45], 0
	v_mfma_f32_16x16x32_f16 v[42:45], v[126:129], v[42:45], 0
	v_mfma_f32_16x16x32_f16 v[134:137], v[122:125], v[58:61], v[134:137]
	v_mfma_f32_16x16x32_f16 v[58:61], v[130:133], v[58:61], v[42:45]
	v_mfma_f32_16x16x32_f16 v[42:45], v[118:121], v[62:65], 0
	v_mfma_f32_16x16x32_f16 v[138:141], v[122:125], v[66:69], v[42:45]
	v_mfma_f32_16x16x32_f16 v[42:45], v[126:129], v[62:65], 0
	v_mfma_f32_16x16x32_f16 v[62:65], v[130:133], v[66:69], v[42:45]
	v_mfma_f32_16x16x32_f16 v[42:45], v[118:121], v[70:73], 0
	v_mfma_f32_16x16x32_f16 v[66:69], v[122:125], v[74:77], v[42:45]
	v_mfma_f32_16x16x32_f16 v[42:45], v[126:129], v[70:73], 0
	v_mfma_f32_16x16x32_f16 v[70:73], v[130:133], v[74:77], v[42:45]
	v_mfma_f32_16x16x32_f16 v[42:45], v[118:121], v[78:81], 0
	v_mfma_f32_16x16x32_f16 v[74:77], v[122:125], v[82:85], v[42:45]
	v_mfma_f32_16x16x32_f16 v[42:45], v[126:129], v[78:81], 0
	v_mfma_f32_16x16x32_f16 v[78:81], v[130:133], v[82:85], v[42:45]
	s_setprio 0
	v_readfirstlane_b32 s17, v35
	s_nop 4
	v_lshl_add_u64 v[42:43], v[26:27], 0, s[0:1]
	s_mov_b32 m0, s17
	s_barrier
	ds_read_b128 v[82:85], v1 offset:16384
	ds_read_b128 v[142:145], v1 offset:17408
	ds_read_b128 v[146:149], v1 offset:18432
	ds_read_b128 v[150:153], v1 offset:19456
	ds_read_b128 v[154:157], v1 offset:20480
	ds_read_b128 v[158:161], v1 offset:21504
	ds_read_b128 v[162:165], v1 offset:22528
	ds_read_b128 v[166:169], v1 offset:23552
	global_load_lds_dwordx4 v[42:43], off
	v_add_u32_e32 v42, 0x2000, v35
	v_lshl_add_u64 v[44:45], v[28:29], 0, s[0:1]
	v_readfirstlane_b32 s10, v42
	s_mov_b32 m0, s10
	s_nop 0
	global_load_lds_dwordx4 v[44:45], off
	s_barrier
	s_waitcnt lgkmcnt(0)
	s_setprio 1
	s_waitcnt lgkmcnt(0)
	v_mfma_f32_16x16x32_f16 v[170:173], v[10:13], v[82:85], 0
	v_mfma_f32_16x16x32_f16 v[178:181], v[10:13], v[146:149], 0
	v_mfma_f32_16x16x32_f16 v[186:189], v[10:13], v[154:157], 0
	v_mfma_f32_16x16x32_f16 v[10:13], v[10:13], v[162:165], 0
	v_mfma_f32_16x16x32_f16 v[194:197], v[14:17], v[166:169], v[10:13]
	v_mfma_f32_16x16x32_f16 v[10:13], v[50:53], v[162:165], 0
	v_mfma_f32_16x16x32_f16 v[174:177], v[50:53], v[82:85], 0
	v_mfma_f32_16x16x32_f16 v[182:185], v[50:53], v[146:149], 0
	v_mfma_f32_16x16x32_f16 v[190:193], v[50:53], v[154:157], 0
	v_mfma_f32_16x16x32_f16 v[50:53], v[54:57], v[166:169], v[10:13]
	v_mfma_f32_16x16x32_f16 v[170:173], v[14:17], v[142:145], v[170:173]
	v_mfma_f32_16x16x32_f16 v[174:177], v[54:57], v[142:145], v[174:177]
	v_mfma_f32_16x16x32_f16 v[178:181], v[14:17], v[150:153], v[178:181]
	v_mfma_f32_16x16x32_f16 v[182:185], v[54:57], v[150:153], v[182:185]
	v_mfma_f32_16x16x32_f16 v[186:189], v[14:17], v[158:161], v[186:189]
	v_mfma_f32_16x16x32_f16 v[190:193], v[54:57], v[158:161], v[190:193]
	s_setprio 0
	s_barrier
	v_readfirstlane_b32 s14, v34
	v_add_u32_e32 v43, 0x2000, v34
	v_lshl_add_u64 v[10:11], v[22:23], 0, s[0:1]
	s_mov_b32 m0, s14
	v_readfirstlane_b32 s11, v43
	global_load_lds_dwordx4 v[10:11], off
	v_lshl_add_u64 v[10:11], v[24:25], 0, s[0:1]
	s_mov_b32 m0, s11
	s_nop 0
	global_load_lds_dwordx4 v[10:11], off
	s_waitcnt vmcnt(6)
	s_barrier
	s_setprio 1
	v_mfma_f32_16x16x32_f16 v[10:13], v[118:121], v[82:85], 0
	v_mfma_f32_16x16x32_f16 v[54:57], v[122:125], v[142:145], v[10:13]
	v_mfma_f32_16x16x32_f16 v[10:13], v[126:129], v[82:85], 0
	v_mfma_f32_16x16x32_f16 v[82:85], v[130:133], v[142:145], v[10:13]
	v_mfma_f32_16x16x32_f16 v[10:13], v[118:121], v[146:149], 0
	v_mfma_f32_16x16x32_f16 v[142:145], v[122:125], v[150:153], v[10:13]
	v_mfma_f32_16x16x32_f16 v[10:13], v[126:129], v[146:149], 0
	v_mfma_f32_16x16x32_f16 v[146:149], v[130:133], v[150:153], v[10:13]
	v_mfma_f32_16x16x32_f16 v[10:13], v[118:121], v[154:157], 0
	v_mfma_f32_16x16x32_f16 v[150:153], v[122:125], v[158:161], v[10:13]
	v_mfma_f32_16x16x32_f16 v[10:13], v[126:129], v[154:157], 0
	v_mfma_f32_16x16x32_f16 v[154:157], v[130:133], v[158:161], v[10:13]
	v_mfma_f32_16x16x32_f16 v[10:13], v[118:121], v[162:165], 0
	v_mfma_f32_16x16x32_f16 v[118:121], v[122:125], v[166:169], v[10:13]
	v_mfma_f32_16x16x32_f16 v[10:13], v[126:129], v[162:165], 0
	v_mfma_f32_16x16x32_f16 v[122:125], v[130:133], v[166:169], v[10:13]
	s_setprio 0
	s_nop 5
	v_add_u32_e32 v10, 0x18000, v234
	v_add_u32_e32 v12, 0x18800, v234
	s_barrier
	v_add_u32_e32 v11, 0x18400, v234
	ds_read_b128 v[126:129], v10
	ds_read_b128 v[130:133], v11
	v_add_u32_e32 v13, 0x18c00, v234
	ds_read_b128 v[158:161], v12
	ds_read_b128 v[162:165], v13
	v_add_u32_e32 v44, 0x4000, v35
	v_add_u32_e32 v45, 0x6000, v35
	v_readfirstlane_b32 s20, v44
	v_lshl_add_u64 v[14:15], v[18:19], 0, s[0:1]
	s_mov_b32 m0, s20
	v_readfirstlane_b32 s18, v45
	ds_read_b128 v[166:169], v1 offset:32768
	ds_read_b128 v[198:201], v1 offset:33792
	ds_read_b128 v[202:205], v1 offset:34816
	ds_read_b128 v[206:209], v1 offset:35840
	ds_read_b128 v[210:213], v1 offset:36864
	ds_read_b128 v[214:217], v1 offset:37888
	ds_read_b128 v[218:221], v1 offset:38912
	ds_read_b128 v[222:225], v1 offset:39936
	global_load_lds_dwordx4 v[14:15], off
	v_lshl_add_u64 v[14:15], v[20:21], 0, s[0:1]
	s_mov_b32 m0, s18
	s_nop 0
	global_load_lds_dwordx4 v[14:15], off
	s_waitcnt lgkmcnt(8)
	s_barrier
	s_waitcnt lgkmcnt(0)
	s_setprio 1
	s_waitcnt lgkmcnt(0)
	v_mfma_f32_16x16x32_f16 v[14:17], v[126:129], v[166:169], v[86:89]
	v_mfma_f32_16x16x32_f16 v[86:89], v[130:133], v[198:201], v[14:17]
	v_mfma_f32_16x16x32_f16 v[14:17], v[158:161], v[166:169], v[90:93]
	v_mfma_f32_16x16x32_f16 v[90:93], v[162:165], v[198:201], v[14:17]
	v_mfma_f32_16x16x32_f16 v[14:17], v[126:129], v[202:205], v[94:97]
	v_mfma_f32_16x16x32_f16 v[94:97], v[130:133], v[206:209], v[14:17]
	v_mfma_f32_16x16x32_f16 v[14:17], v[158:161], v[202:205], v[98:101]
	v_mfma_f32_16x16x32_f16 v[98:101], v[162:165], v[206:209], v[14:17]
	v_mfma_f32_16x16x32_f16 v[14:17], v[126:129], v[210:213], v[102:105]
	v_mfma_f32_16x16x32_f16 v[102:105], v[130:133], v[214:217], v[14:17]
	v_mfma_f32_16x16x32_f16 v[14:17], v[158:161], v[210:213], v[106:109]
	v_mfma_f32_16x16x32_f16 v[106:109], v[162:165], v[214:217], v[14:17]
	v_mfma_f32_16x16x32_f16 v[14:17], v[126:129], v[218:221], v[110:113]
	v_mfma_f32_16x16x32_f16 v[110:113], v[130:133], v[222:225], v[14:17]
	v_mfma_f32_16x16x32_f16 v[14:17], v[158:161], v[218:221], v[114:117]
	v_mfma_f32_16x16x32_f16 v[114:117], v[162:165], v[222:225], v[14:17]
	s_setprio 0
	s_barrier
	s_mov_b64 s[0:1], 0x180
	s_mov_b32 m0, s22
	s_nop 2
	v_add_u32_e32 v14, 0x1c000, v234
	v_add_u32_e32 v16, 0x1c800, v234
	v_lshl_add_u64 v[242:243], v[30:31], 0, s[0:1]
	v_add_u32_e32 v15, 0x1c400, v234
	ds_read_b128 v[226:229], v14
	ds_read_b128 v[230:233], v15
	v_add_u32_e32 v17, 0x1cc00, v234
	ds_read_b128 v[234:237], v16
	ds_read_b128 v[238:241], v17
	global_load_lds_dwordx4 v[242:243], off
	v_lshl_add_u64 v[242:243], v[32:33], 0, s[0:1]
	s_mov_b32 m0, s21
	s_nop 0
	global_load_lds_dwordx4 v[242:243], off
	s_barrier
	s_waitcnt lgkmcnt(0)
	s_setprio 1
	s_waitcnt lgkmcnt(0)
	v_mfma_f32_16x16x32_f16 v[134:137], v[226:229], v[166:169], v[134:137]
	v_mfma_f32_16x16x32_f16 v[58:61], v[234:237], v[166:169], v[58:61]
	v_mfma_f32_16x16x32_f16 v[138:141], v[226:229], v[202:205], v[138:141]
	v_mfma_f32_16x16x32_f16 v[62:65], v[234:237], v[202:205], v[62:65]
	v_mfma_f32_16x16x32_f16 v[66:69], v[226:229], v[210:213], v[66:69]
	v_mfma_f32_16x16x32_f16 v[70:73], v[234:237], v[210:213], v[70:73]
	v_mfma_f32_16x16x32_f16 v[74:77], v[226:229], v[218:221], v[74:77]
	v_mfma_f32_16x16x32_f16 v[78:81], v[234:237], v[218:221], v[78:81]
	v_mfma_f32_16x16x32_f16 v[134:137], v[230:233], v[198:201], v[134:137]
	v_mfma_f32_16x16x32_f16 v[58:61], v[238:241], v[198:201], v[58:61]
	v_mfma_f32_16x16x32_f16 v[138:141], v[230:233], v[206:209], v[138:141]
	v_mfma_f32_16x16x32_f16 v[62:65], v[238:241], v[206:209], v[62:65]
	v_mfma_f32_16x16x32_f16 v[66:69], v[230:233], v[214:217], v[66:69]
	v_mfma_f32_16x16x32_f16 v[70:73], v[238:241], v[214:217], v[70:73]
	v_mfma_f32_16x16x32_f16 v[74:77], v[230:233], v[222:225], v[74:77]
	v_mfma_f32_16x16x32_f16 v[78:81], v[238:241], v[222:225], v[78:81]
	s_setprio 0
	s_mov_b32 m0, s19
	v_lshl_add_u64 v[242:243], v[26:27], 0, s[0:1]
	s_barrier
	ds_read_b128 v[166:169], v1 offset:49152
	ds_read_b128 v[198:201], v1 offset:50176
	ds_read_b128 v[202:205], v1 offset:51200
	ds_read_b128 v[206:209], v1 offset:52224
	ds_read_b128 v[210:213], v1 offset:53248
	ds_read_b128 v[214:217], v1 offset:54272
	ds_read_b128 v[218:221], v1 offset:55296
	ds_read_b128 v[222:225], v1 offset:56320
	global_load_lds_dwordx4 v[242:243], off
	v_lshl_add_u64 v[242:243], v[28:29], 0, s[0:1]
	s_mov_b32 m0, s16
	s_nop 0
	global_load_lds_dwordx4 v[242:243], off
	s_barrier
	s_waitcnt lgkmcnt(0)
	s_setprio 1
	s_waitcnt lgkmcnt(0)
	v_mfma_f32_16x16x32_f16 v[170:173], v[126:129], v[166:169], v[170:173]
	v_mfma_f32_16x16x32_f16 v[178:181], v[126:129], v[202:205], v[178:181]
	v_mfma_f32_16x16x32_f16 v[186:189], v[126:129], v[210:213], v[186:189]
	v_mfma_f32_16x16x32_f16 v[126:129], v[126:129], v[218:221], v[194:197]
	v_mfma_f32_16x16x32_f16 v[50:53], v[158:161], v[218:221], v[50:53]
	v_mfma_f32_16x16x32_f16 v[174:177], v[158:161], v[166:169], v[174:177]
	v_mfma_f32_16x16x32_f16 v[182:185], v[158:161], v[202:205], v[182:185]
	v_mfma_f32_16x16x32_f16 v[190:193], v[158:161], v[210:213], v[190:193]
	v_mfma_f32_16x16x32_f16 v[126:129], v[130:133], v[222:225], v[126:129]
	v_mfma_f32_16x16x32_f16 v[50:53], v[162:165], v[222:225], v[50:53]
	v_mfma_f32_16x16x32_f16 v[170:173], v[130:133], v[198:201], v[170:173]
	v_mfma_f32_16x16x32_f16 v[174:177], v[162:165], v[198:201], v[174:177]
	v_mfma_f32_16x16x32_f16 v[178:181], v[130:133], v[206:209], v[178:181]
	v_mfma_f32_16x16x32_f16 v[182:185], v[162:165], v[206:209], v[182:185]
	v_mfma_f32_16x16x32_f16 v[186:189], v[130:133], v[214:217], v[186:189]
	v_mfma_f32_16x16x32_f16 v[190:193], v[162:165], v[214:217], v[190:193]
	s_setprio 0
	s_barrier
	s_mov_b32 m0, s3
	v_lshl_add_u64 v[130:131], v[22:23], 0, s[0:1]
	global_load_lds_dwordx4 v[130:131], off
	v_lshl_add_u64 v[130:131], v[24:25], 0, s[0:1]
	s_mov_b32 m0, s2
	s_nop 0
	global_load_lds_dwordx4 v[130:131], off
	s_waitcnt vmcnt(6)
	s_barrier
	s_setprio 1
	v_mfma_f32_16x16x32_f16 v[82:85], v[234:237], v[166:169], v[82:85]
	v_mfma_f32_16x16x32_f16 v[130:133], v[226:229], v[202:205], v[142:145]
	v_mfma_f32_16x16x32_f16 v[142:145], v[234:237], v[202:205], v[146:149]
	v_mfma_f32_16x16x32_f16 v[146:149], v[226:229], v[210:213], v[150:153]
	v_mfma_f32_16x16x32_f16 v[150:153], v[234:237], v[210:213], v[154:157]
	v_mfma_f32_16x16x32_f16 v[118:121], v[226:229], v[218:221], v[118:121]
	v_mfma_f32_16x16x32_f16 v[122:125], v[234:237], v[218:221], v[122:125]
	v_mfma_f32_16x16x32_f16 v[54:57], v[226:229], v[166:169], v[54:57]
	v_mfma_f32_16x16x32_f16 v[82:85], v[238:241], v[198:201], v[82:85]
	v_mfma_f32_16x16x32_f16 v[130:133], v[230:233], v[206:209], v[130:133]
	v_mfma_f32_16x16x32_f16 v[142:145], v[238:241], v[206:209], v[142:145]
	v_mfma_f32_16x16x32_f16 v[146:149], v[230:233], v[214:217], v[146:149]
	v_mfma_f32_16x16x32_f16 v[150:153], v[238:241], v[214:217], v[150:153]
	v_mfma_f32_16x16x32_f16 v[118:121], v[230:233], v[222:225], v[118:121]
	v_mfma_f32_16x16x32_f16 v[122:125], v[238:241], v[222:225], v[122:125]
	v_mfma_f32_16x16x32_f16 v[54:57], v[230:233], v[198:201], v[54:57]
	s_setprio 0
	s_barrier
	ds_read_b128 v[154:157], v2
	ds_read_b128 v[158:161], v3
	ds_read_b128 v[162:165], v4
	ds_read_b128 v[166:169], v5
	s_mov_b32 m0, s7
	v_lshl_add_u64 v[194:195], v[18:19], 0, s[0:1]
	global_load_lds_dwordx4 v[194:195], off
	v_lshl_add_u64 v[194:195], v[20:21], 0, s[0:1]
	s_mov_b32 m0, s4
	s_nop 0
	global_load_lds_dwordx4 v[194:195], off
	ds_read_b128 v[194:197], v1
	ds_read_b128 v[198:201], v1 offset:1024
	ds_read_b128 v[202:205], v1 offset:2048
	ds_read_b128 v[206:209], v1 offset:3072
	ds_read_b128 v[210:213], v1 offset:4096
	ds_read_b128 v[214:217], v1 offset:5120
	ds_read_b128 v[218:221], v1 offset:6144
	ds_read_b128 v[222:225], v1 offset:7168
	s_waitcnt lgkmcnt(8)
	s_barrier
	s_waitcnt lgkmcnt(0)
	s_setprio 1
	s_waitcnt lgkmcnt(0)
	v_mfma_f32_16x16x32_f16 v[86:89], v[154:157], v[194:197], v[86:89]
	v_mfma_f32_16x16x32_f16 v[90:93], v[162:165], v[194:197], v[90:93]
	v_mfma_f32_16x16x32_f16 v[94:97], v[154:157], v[202:205], v[94:97]
	v_mfma_f32_16x16x32_f16 v[98:101], v[162:165], v[202:205], v[98:101]
	v_mfma_f32_16x16x32_f16 v[102:105], v[154:157], v[210:213], v[102:105]
	v_mfma_f32_16x16x32_f16 v[106:109], v[162:165], v[210:213], v[106:109]
	v_mfma_f32_16x16x32_f16 v[110:113], v[154:157], v[218:221], v[110:113]
	v_mfma_f32_16x16x32_f16 v[86:89], v[158:161], v[198:201], v[86:89]
	v_mfma_f32_16x16x32_f16 v[90:93], v[166:169], v[198:201], v[90:93]
	v_mfma_f32_16x16x32_f16 v[94:97], v[158:161], v[206:209], v[94:97]
	v_mfma_f32_16x16x32_f16 v[98:101], v[166:169], v[206:209], v[98:101]
	v_mfma_f32_16x16x32_f16 v[102:105], v[158:161], v[214:217], v[102:105]
	v_mfma_f32_16x16x32_f16 v[106:109], v[166:169], v[214:217], v[106:109]
	v_mfma_f32_16x16x32_f16 v[110:113], v[158:161], v[222:225], v[110:113]
	v_mfma_f32_16x16x32_f16 v[114:117], v[162:165], v[218:221], v[114:117]
	v_mfma_f32_16x16x32_f16 v[114:117], v[166:169], v[222:225], v[114:117]
	s_setprio 0
	s_barrier
	s_mov_b64 s[0:1], 0x200
	s_mov_b32 m0, s15
	v_lshl_add_u64 v[242:243], v[30:31], 0, s[0:1]
	ds_read_b128 v[226:229], v6
	ds_read_b128 v[230:233], v7
	ds_read_b128 v[234:237], v8
	ds_read_b128 v[238:241], v9
	global_load_lds_dwordx4 v[242:243], off
	v_lshl_add_u64 v[242:243], v[32:33], 0, s[0:1]
	s_mov_b32 m0, s5
	s_nop 0
	global_load_lds_dwordx4 v[242:243], off
	s_barrier
	s_waitcnt lgkmcnt(0)
	s_setprio 1
	s_waitcnt lgkmcnt(0)
	v_mfma_f32_16x16x32_f16 v[134:137], v[226:229], v[194:197], v[134:137]
	v_mfma_f32_16x16x32_f16 v[58:61], v[234:237], v[194:197], v[58:61]
	v_mfma_f32_16x16x32_f16 v[138:141], v[226:229], v[202:205], v[138:141]
	v_mfma_f32_16x16x32_f16 v[62:65], v[234:237], v[202:205], v[62:65]
	v_mfma_f32_16x16x32_f16 v[66:69], v[226:229], v[210:213], v[66:69]
	v_mfma_f32_16x16x32_f16 v[70:73], v[234:237], v[210:213], v[70:73]
	v_mfma_f32_16x16x32_f16 v[74:77], v[226:229], v[218:221], v[74:77]
	v_mfma_f32_16x16x32_f16 v[78:81], v[234:237], v[218:221], v[78:81]
	v_mfma_f32_16x16x32_f16 v[134:137], v[230:233], v[198:201], v[134:137]
	v_mfma_f32_16x16x32_f16 v[58:61], v[238:241], v[198:201], v[58:61]
	v_mfma_f32_16x16x32_f16 v[138:141], v[230:233], v[206:209], v[138:141]
	v_mfma_f32_16x16x32_f16 v[62:65], v[238:241], v[206:209], v[62:65]
	v_mfma_f32_16x16x32_f16 v[66:69], v[230:233], v[214:217], v[66:69]
	v_mfma_f32_16x16x32_f16 v[70:73], v[238:241], v[214:217], v[70:73]
	v_mfma_f32_16x16x32_f16 v[74:77], v[230:233], v[222:225], v[74:77]
	v_mfma_f32_16x16x32_f16 v[78:81], v[238:241], v[222:225], v[78:81]
	s_setprio 0
	s_mov_b32 m0, s17
	v_lshl_add_u64 v[242:243], v[26:27], 0, s[0:1]
	s_barrier
	ds_read_b128 v[194:197], v1 offset:16384
	ds_read_b128 v[198:201], v1 offset:17408
	ds_read_b128 v[202:205], v1 offset:18432
	ds_read_b128 v[206:209], v1 offset:19456
	ds_read_b128 v[210:213], v1 offset:20480
	ds_read_b128 v[214:217], v1 offset:21504
	ds_read_b128 v[218:221], v1 offset:22528
	ds_read_b128 v[222:225], v1 offset:23552
	global_load_lds_dwordx4 v[242:243], off
	v_lshl_add_u64 v[242:243], v[28:29], 0, s[0:1]
	s_mov_b32 m0, s10
	s_nop 0
	global_load_lds_dwordx4 v[242:243], off
	s_barrier
	s_waitcnt lgkmcnt(0)
	s_setprio 1
	s_waitcnt lgkmcnt(0)
	v_mfma_f32_16x16x32_f16 v[126:129], v[154:157], v[218:221], v[126:129]
	v_mfma_f32_16x16x32_f16 v[50:53], v[162:165], v[218:221], v[50:53]
	v_mfma_f32_16x16x32_f16 v[170:173], v[154:157], v[194:197], v[170:173]
	v_mfma_f32_16x16x32_f16 v[174:177], v[162:165], v[194:197], v[174:177]
	v_mfma_f32_16x16x32_f16 v[178:181], v[154:157], v[202:205], v[178:181]
	v_mfma_f32_16x16x32_f16 v[182:185], v[162:165], v[202:205], v[182:185]
	v_mfma_f32_16x16x32_f16 v[186:189], v[154:157], v[210:213], v[186:189]
	v_mfma_f32_16x16x32_f16 v[190:193], v[162:165], v[210:213], v[190:193]
	v_mfma_f32_16x16x32_f16 v[126:129], v[158:161], v[222:225], v[126:129]
	v_mfma_f32_16x16x32_f16 v[50:53], v[166:169], v[222:225], v[50:53]
	v_mfma_f32_16x16x32_f16 v[170:173], v[158:161], v[198:201], v[170:173]
	v_mfma_f32_16x16x32_f16 v[174:177], v[166:169], v[198:201], v[174:177]
	v_mfma_f32_16x16x32_f16 v[178:181], v[158:161], v[206:209], v[178:181]
	v_mfma_f32_16x16x32_f16 v[182:185], v[166:169], v[206:209], v[182:185]
	v_mfma_f32_16x16x32_f16 v[186:189], v[158:161], v[214:217], v[186:189]
	v_mfma_f32_16x16x32_f16 v[190:193], v[166:169], v[214:217], v[190:193]
	s_setprio 0
	s_barrier
	s_mov_b32 m0, s14
	v_lshl_add_u64 v[154:155], v[22:23], 0, s[0:1]
	global_load_lds_dwordx4 v[154:155], off
	v_lshl_add_u64 v[154:155], v[24:25], 0, s[0:1]
	s_mov_b32 m0, s11
	s_nop 0
	global_load_lds_dwordx4 v[154:155], off
	s_waitcnt vmcnt(6)
	s_barrier
	s_setprio 1
	v_mfma_f32_16x16x32_f16 v[82:85], v[234:237], v[194:197], v[82:85]
	v_mfma_f32_16x16x32_f16 v[130:133], v[226:229], v[202:205], v[130:133]
	v_mfma_f32_16x16x32_f16 v[142:145], v[234:237], v[202:205], v[142:145]
	v_mfma_f32_16x16x32_f16 v[146:149], v[226:229], v[210:213], v[146:149]
	v_mfma_f32_16x16x32_f16 v[150:153], v[234:237], v[210:213], v[150:153]
	v_mfma_f32_16x16x32_f16 v[118:121], v[226:229], v[218:221], v[118:121]
	v_mfma_f32_16x16x32_f16 v[122:125], v[234:237], v[218:221], v[122:125]
	v_mfma_f32_16x16x32_f16 v[54:57], v[226:229], v[194:197], v[54:57]
	v_mfma_f32_16x16x32_f16 v[82:85], v[238:241], v[198:201], v[82:85]
	v_mfma_f32_16x16x32_f16 v[130:133], v[230:233], v[206:209], v[130:133]
	v_mfma_f32_16x16x32_f16 v[142:145], v[238:241], v[206:209], v[142:145]
	v_mfma_f32_16x16x32_f16 v[146:149], v[230:233], v[214:217], v[146:149]
	v_mfma_f32_16x16x32_f16 v[150:153], v[238:241], v[214:217], v[150:153]
	v_mfma_f32_16x16x32_f16 v[118:121], v[230:233], v[222:225], v[118:121]
	v_mfma_f32_16x16x32_f16 v[122:125], v[238:241], v[222:225], v[122:125]
	v_mfma_f32_16x16x32_f16 v[54:57], v[230:233], v[198:201], v[54:57]
	s_setprio 0
	s_barrier
	ds_read_b128 v[154:157], v10
	ds_read_b128 v[158:161], v11
	ds_read_b128 v[162:165], v12
	ds_read_b128 v[166:169], v13
	s_mov_b32 m0, s20
	v_lshl_add_u64 v[226:227], v[18:19], 0, s[0:1]
	ds_read_b128 v[194:197], v1 offset:32768
	ds_read_b128 v[198:201], v1 offset:33792
	ds_read_b128 v[202:205], v1 offset:34816
	ds_read_b128 v[206:209], v1 offset:35840
	ds_read_b128 v[210:213], v1 offset:36864
	ds_read_b128 v[214:217], v1 offset:37888
	ds_read_b128 v[218:221], v1 offset:38912
	ds_read_b128 v[222:225], v1 offset:39936
	global_load_lds_dwordx4 v[226:227], off
	v_lshl_add_u64 v[226:227], v[20:21], 0, s[0:1]
	s_mov_b32 m0, s18
	s_nop 0
	global_load_lds_dwordx4 v[226:227], off
	s_waitcnt lgkmcnt(8)
	s_barrier
	s_waitcnt lgkmcnt(0)
	s_setprio 1
	s_waitcnt lgkmcnt(0)
	v_mfma_f32_16x16x32_f16 v[86:89], v[154:157], v[194:197], v[86:89]
	v_mfma_f32_16x16x32_f16 v[90:93], v[162:165], v[194:197], v[90:93]
	v_mfma_f32_16x16x32_f16 v[94:97], v[154:157], v[202:205], v[94:97]
	v_mfma_f32_16x16x32_f16 v[98:101], v[162:165], v[202:205], v[98:101]
	v_mfma_f32_16x16x32_f16 v[102:105], v[154:157], v[210:213], v[102:105]
	v_mfma_f32_16x16x32_f16 v[106:109], v[162:165], v[210:213], v[106:109]
	v_mfma_f32_16x16x32_f16 v[110:113], v[154:157], v[218:221], v[110:113]
	v_mfma_f32_16x16x32_f16 v[86:89], v[158:161], v[198:201], v[86:89]
	v_mfma_f32_16x16x32_f16 v[90:93], v[166:169], v[198:201], v[90:93]
	v_mfma_f32_16x16x32_f16 v[94:97], v[158:161], v[206:209], v[94:97]
	v_mfma_f32_16x16x32_f16 v[98:101], v[166:169], v[206:209], v[98:101]
	v_mfma_f32_16x16x32_f16 v[102:105], v[158:161], v[214:217], v[102:105]
	v_mfma_f32_16x16x32_f16 v[106:109], v[166:169], v[214:217], v[106:109]
	v_mfma_f32_16x16x32_f16 v[110:113], v[158:161], v[222:225], v[110:113]
	v_mfma_f32_16x16x32_f16 v[114:117], v[162:165], v[218:221], v[114:117]
	v_mfma_f32_16x16x32_f16 v[114:117], v[166:169], v[222:225], v[114:117]
	s_setprio 0
	s_barrier
	s_mov_b64 s[0:1], 0x280
	v_readfirstlane_b32 s10, v48
	v_lshl_add_u64 v[242:243], v[30:31], 0, s[0:1]
	s_mov_b32 m0, s10
	v_readfirstlane_b32 s2, v49
	ds_read_b128 v[226:229], v14
	ds_read_b128 v[230:233], v15
	ds_read_b128 v[234:237], v16
	ds_read_b128 v[238:241], v17
	global_load_lds_dwordx4 v[242:243], off
	v_lshl_add_u64 v[242:243], v[32:33], 0, s[0:1]
	s_mov_b32 m0, s2
	s_nop 0
	global_load_lds_dwordx4 v[242:243], off
	s_barrier
	s_waitcnt lgkmcnt(0)
	s_setprio 1
	s_waitcnt lgkmcnt(0)
	v_mfma_f32_16x16x32_f16 v[134:137], v[226:229], v[194:197], v[134:137]
	v_mfma_f32_16x16x32_f16 v[58:61], v[234:237], v[194:197], v[58:61]
	v_mfma_f32_16x16x32_f16 v[138:141], v[226:229], v[202:205], v[138:141]
	v_mfma_f32_16x16x32_f16 v[62:65], v[234:237], v[202:205], v[62:65]
	v_mfma_f32_16x16x32_f16 v[66:69], v[226:229], v[210:213], v[66:69]
	v_mfma_f32_16x16x32_f16 v[70:73], v[234:237], v[210:213], v[70:73]
	v_mfma_f32_16x16x32_f16 v[74:77], v[226:229], v[218:221], v[74:77]
	v_mfma_f32_16x16x32_f16 v[78:81], v[234:237], v[218:221], v[78:81]
	v_mfma_f32_16x16x32_f16 v[134:137], v[230:233], v[198:201], v[134:137]
	v_mfma_f32_16x16x32_f16 v[58:61], v[238:241], v[198:201], v[58:61]
	v_mfma_f32_16x16x32_f16 v[138:141], v[230:233], v[206:209], v[138:141]
	v_mfma_f32_16x16x32_f16 v[62:65], v[238:241], v[206:209], v[62:65]
	v_mfma_f32_16x16x32_f16 v[66:69], v[230:233], v[214:217], v[66:69]
	v_mfma_f32_16x16x32_f16 v[70:73], v[238:241], v[214:217], v[70:73]
	v_mfma_f32_16x16x32_f16 v[74:77], v[230:233], v[222:225], v[74:77]
	v_mfma_f32_16x16x32_f16 v[78:81], v[238:241], v[222:225], v[78:81]
	s_setprio 0
	v_readfirstlane_b32 s11, v46
	v_lshl_add_u64 v[48:49], v[26:27], 0, s[0:1]
	s_mov_b32 m0, s11
	v_readfirstlane_b32 s3, v47
	s_barrier
	ds_read_b128 v[194:197], v1 offset:49152
	ds_read_b128 v[198:201], v1 offset:50176
	ds_read_b128 v[202:205], v1 offset:51200
	ds_read_b128 v[206:209], v1 offset:52224
	ds_read_b128 v[210:213], v1 offset:53248
	ds_read_b128 v[214:217], v1 offset:54272
	ds_read_b128 v[218:221], v1 offset:55296
	ds_read_b128 v[222:225], v1 offset:56320
	global_load_lds_dwordx4 v[48:49], off
	v_lshl_add_u64 v[48:49], v[28:29], 0, s[0:1]
	s_mov_b32 m0, s3
	s_nop 0
	global_load_lds_dwordx4 v[48:49], off
	s_barrier
	s_waitcnt lgkmcnt(0)
	s_setprio 1
	s_waitcnt lgkmcnt(0)
	v_mfma_f32_16x16x32_f16 v[126:129], v[154:157], v[218:221], v[126:129]
	v_mfma_f32_16x16x32_f16 v[50:53], v[162:165], v[218:221], v[50:53]
	v_mfma_f32_16x16x32_f16 v[46:49], v[154:157], v[194:197], v[170:173]
	v_mfma_f32_16x16x32_f16 v[170:173], v[162:165], v[194:197], v[174:177]
	v_mfma_f32_16x16x32_f16 v[174:177], v[154:157], v[202:205], v[178:181]
	v_mfma_f32_16x16x32_f16 v[178:181], v[162:165], v[202:205], v[182:185]
	v_mfma_f32_16x16x32_f16 v[182:185], v[154:157], v[210:213], v[186:189]
	v_mfma_f32_16x16x32_f16 v[186:189], v[162:165], v[210:213], v[190:193]
	v_mfma_f32_16x16x32_f16 v[126:129], v[158:161], v[222:225], v[126:129]
	v_mfma_f32_16x16x32_f16 v[50:53], v[166:169], v[222:225], v[50:53]
	v_mfma_f32_16x16x32_f16 v[46:49], v[158:161], v[198:201], v[46:49]
	v_mfma_f32_16x16x32_f16 v[170:173], v[166:169], v[198:201], v[170:173]
	v_mfma_f32_16x16x32_f16 v[174:177], v[158:161], v[206:209], v[174:177]
	v_mfma_f32_16x16x32_f16 v[178:181], v[166:169], v[206:209], v[178:181]
	v_mfma_f32_16x16x32_f16 v[182:185], v[158:161], v[214:217], v[182:185]
	v_mfma_f32_16x16x32_f16 v[186:189], v[166:169], v[214:217], v[186:189]
	s_setprio 0
	s_barrier
	v_readfirstlane_b32 s5, v37
	v_lshl_add_u64 v[154:155], v[22:23], 0, s[0:1]
	s_mov_b32 m0, s5
	v_readfirstlane_b32 s4, v39
	global_load_lds_dwordx4 v[154:155], off
	v_lshl_add_u64 v[154:155], v[24:25], 0, s[0:1]
	s_mov_b32 m0, s4
	s_nop 0
	global_load_lds_dwordx4 v[154:155], off
	s_waitcnt vmcnt(6)
	s_barrier
	s_setprio 1
	v_mfma_f32_16x16x32_f16 v[82:85], v[234:237], v[194:197], v[82:85]
	v_mfma_f32_16x16x32_f16 v[130:133], v[226:229], v[202:205], v[130:133]
	v_mfma_f32_16x16x32_f16 v[142:145], v[234:237], v[202:205], v[142:145]
	v_mfma_f32_16x16x32_f16 v[146:149], v[226:229], v[210:213], v[146:149]
	v_mfma_f32_16x16x32_f16 v[150:153], v[234:237], v[210:213], v[150:153]
	v_mfma_f32_16x16x32_f16 v[118:121], v[226:229], v[218:221], v[118:121]
	v_mfma_f32_16x16x32_f16 v[122:125], v[234:237], v[218:221], v[122:125]
	v_mfma_f32_16x16x32_f16 v[54:57], v[226:229], v[194:197], v[54:57]
	v_mfma_f32_16x16x32_f16 v[82:85], v[238:241], v[198:201], v[82:85]
	v_mfma_f32_16x16x32_f16 v[130:133], v[230:233], v[206:209], v[130:133]
	v_mfma_f32_16x16x32_f16 v[142:145], v[238:241], v[206:209], v[142:145]
	v_mfma_f32_16x16x32_f16 v[146:149], v[230:233], v[214:217], v[146:149]
	v_mfma_f32_16x16x32_f16 v[150:153], v[238:241], v[214:217], v[150:153]
	v_mfma_f32_16x16x32_f16 v[118:121], v[230:233], v[222:225], v[118:121]
	v_mfma_f32_16x16x32_f16 v[122:125], v[238:241], v[222:225], v[122:125]
	v_mfma_f32_16x16x32_f16 v[54:57], v[230:233], v[198:201], v[54:57]
	s_setprio 0
	s_barrier
	ds_read_b128 v[154:157], v2
	ds_read_b128 v[158:161], v3
	ds_read_b128 v[162:165], v4
	ds_read_b128 v[166:169], v5
	v_readfirstlane_b32 s14, v38
	v_lshl_add_u64 v[190:191], v[18:19], 0, s[0:1]
	s_mov_b32 m0, s14
	v_readfirstlane_b32 s7, v40
	global_load_lds_dwordx4 v[190:191], off
	v_lshl_add_u64 v[38:39], v[20:21], 0, s[0:1]
	s_mov_b32 m0, s7
	s_nop 0
	global_load_lds_dwordx4 v[38:39], off
	ds_read_b128 v[190:193], v1
	ds_read_b128 v[194:197], v1 offset:1024
	ds_read_b128 v[198:201], v1 offset:2048
	ds_read_b128 v[202:205], v1 offset:3072
	ds_read_b128 v[206:209], v1 offset:4096
	ds_read_b128 v[210:213], v1 offset:5120
	ds_read_b128 v[214:217], v1 offset:6144
	ds_read_b128 v[218:221], v1 offset:7168
	s_waitcnt lgkmcnt(8)
	s_barrier
	s_waitcnt lgkmcnt(0)
	s_setprio 1
	s_waitcnt lgkmcnt(0)
	v_mfma_f32_16x16x32_f16 v[86:89], v[154:157], v[190:193], v[86:89]
	v_mfma_f32_16x16x32_f16 v[90:93], v[162:165], v[190:193], v[90:93]
	v_mfma_f32_16x16x32_f16 v[94:97], v[154:157], v[198:201], v[94:97]
	v_mfma_f32_16x16x32_f16 v[98:101], v[162:165], v[198:201], v[98:101]
	v_mfma_f32_16x16x32_f16 v[102:105], v[154:157], v[206:209], v[102:105]
	v_mfma_f32_16x16x32_f16 v[106:109], v[162:165], v[206:209], v[106:109]
	v_mfma_f32_16x16x32_f16 v[110:113], v[154:157], v[214:217], v[110:113]
	v_mfma_f32_16x16x32_f16 v[86:89], v[158:161], v[194:197], v[86:89]
	v_mfma_f32_16x16x32_f16 v[90:93], v[166:169], v[194:197], v[90:93]
	v_mfma_f32_16x16x32_f16 v[94:97], v[158:161], v[202:205], v[94:97]
	v_mfma_f32_16x16x32_f16 v[98:101], v[166:169], v[202:205], v[98:101]
	v_mfma_f32_16x16x32_f16 v[102:105], v[158:161], v[210:213], v[102:105]
	v_mfma_f32_16x16x32_f16 v[106:109], v[166:169], v[210:213], v[106:109]
	v_mfma_f32_16x16x32_f16 v[110:113], v[158:161], v[218:221], v[110:113]
	v_mfma_f32_16x16x32_f16 v[114:117], v[162:165], v[214:217], v[114:117]
	v_mfma_f32_16x16x32_f16 v[114:117], v[166:169], v[218:221], v[114:117]
	s_setprio 0
	s_barrier
	s_mov_b64 s[0:1], 0x300
	v_readfirstlane_b32 s15, v36
	v_lshl_add_u64 v[38:39], v[30:31], 0, s[0:1]
	s_mov_b32 m0, s15
	v_readfirstlane_b32 s15, v41
	ds_read_b128 v[222:225], v6
	ds_read_b128 v[226:229], v7
	ds_read_b128 v[230:233], v8
	ds_read_b128 v[234:237], v9
	global_load_lds_dwordx4 v[38:39], off
	v_lshl_add_u64 v[36:37], v[32:33], 0, s[0:1]
	s_mov_b32 m0, s15
	s_nop 0
	global_load_lds_dwordx4 v[36:37], off
	s_barrier
	s_waitcnt lgkmcnt(0)
	s_setprio 1
	s_waitcnt lgkmcnt(0)
	v_mfma_f32_16x16x32_f16 v[36:39], v[222:225], v[190:193], v[134:137]
	v_mfma_f32_16x16x32_f16 v[58:61], v[230:233], v[190:193], v[58:61]
	v_mfma_f32_16x16x32_f16 v[134:137], v[222:225], v[198:201], v[138:141]
	v_mfma_f32_16x16x32_f16 v[62:65], v[230:233], v[198:201], v[62:65]
	v_mfma_f32_16x16x32_f16 v[66:69], v[222:225], v[206:209], v[66:69]
	v_mfma_f32_16x16x32_f16 v[70:73], v[230:233], v[206:209], v[70:73]
	v_mfma_f32_16x16x32_f16 v[74:77], v[222:225], v[214:217], v[74:77]
	v_mfma_f32_16x16x32_f16 v[78:81], v[230:233], v[214:217], v[78:81]
	v_mfma_f32_16x16x32_f16 v[36:39], v[226:229], v[194:197], v[36:39]
	v_mfma_f32_16x16x32_f16 v[58:61], v[234:237], v[194:197], v[58:61]
	v_mfma_f32_16x16x32_f16 v[134:137], v[226:229], v[202:205], v[134:137]
	v_mfma_f32_16x16x32_f16 v[62:65], v[234:237], v[202:205], v[62:65]
	v_mfma_f32_16x16x32_f16 v[66:69], v[226:229], v[210:213], v[66:69]
	v_mfma_f32_16x16x32_f16 v[70:73], v[234:237], v[210:213], v[70:73]
	v_mfma_f32_16x16x32_f16 v[74:77], v[226:229], v[218:221], v[74:77]
	v_mfma_f32_16x16x32_f16 v[78:81], v[234:237], v[218:221], v[78:81]
	s_setprio 0
	v_readfirstlane_b32 s15, v35
	v_lshl_add_u64 v[40:41], v[26:27], 0, s[0:1]
	s_mov_b32 m0, s15
	v_readfirstlane_b32 s15, v42
	s_barrier
	ds_read_b128 v[138:141], v1 offset:16384
	ds_read_b128 v[190:193], v1 offset:17408
	ds_read_b128 v[194:197], v1 offset:18432
	ds_read_b128 v[198:201], v1 offset:19456
	ds_read_b128 v[202:205], v1 offset:20480
	ds_read_b128 v[206:209], v1 offset:21504
	ds_read_b128 v[210:213], v1 offset:22528
	ds_read_b128 v[214:217], v1 offset:23552
	global_load_lds_dwordx4 v[40:41], off
	v_lshl_add_u64 v[40:41], v[28:29], 0, s[0:1]
	s_mov_b32 m0, s15
	s_nop 0
	global_load_lds_dwordx4 v[40:41], off
	s_barrier
	s_waitcnt lgkmcnt(0)
	s_setprio 1
	s_waitcnt lgkmcnt(0)
	v_mfma_f32_16x16x32_f16 v[126:129], v[154:157], v[210:213], v[126:129]
	v_mfma_f32_16x16x32_f16 v[50:53], v[162:165], v[210:213], v[50:53]
	v_mfma_f32_16x16x32_f16 v[46:49], v[154:157], v[138:141], v[46:49]
	v_mfma_f32_16x16x32_f16 v[170:173], v[162:165], v[138:141], v[170:173]
	v_mfma_f32_16x16x32_f16 v[174:177], v[154:157], v[194:197], v[174:177]
	v_mfma_f32_16x16x32_f16 v[178:181], v[162:165], v[194:197], v[178:181]
	v_mfma_f32_16x16x32_f16 v[182:185], v[154:157], v[202:205], v[182:185]
	v_mfma_f32_16x16x32_f16 v[186:189], v[162:165], v[202:205], v[186:189]
	v_mfma_f32_16x16x32_f16 v[126:129], v[158:161], v[214:217], v[126:129]
	v_mfma_f32_16x16x32_f16 v[50:53], v[166:169], v[214:217], v[50:53]
	v_mfma_f32_16x16x32_f16 v[46:49], v[158:161], v[190:193], v[46:49]
	v_mfma_f32_16x16x32_f16 v[170:173], v[166:169], v[190:193], v[170:173]
	v_mfma_f32_16x16x32_f16 v[174:177], v[158:161], v[198:201], v[174:177]
	v_mfma_f32_16x16x32_f16 v[178:181], v[166:169], v[198:201], v[178:181]
	v_mfma_f32_16x16x32_f16 v[182:185], v[158:161], v[206:209], v[182:185]
	v_mfma_f32_16x16x32_f16 v[186:189], v[166:169], v[206:209], v[186:189]
	s_setprio 0
	s_barrier
	v_readfirstlane_b32 s15, v34
	v_lshl_add_u64 v[40:41], v[22:23], 0, s[0:1]
	s_mov_b32 m0, s15
	v_readfirstlane_b32 s15, v43
	global_load_lds_dwordx4 v[40:41], off
	v_lshl_add_u64 v[34:35], v[24:25], 0, s[0:1]
	s_mov_b32 m0, s15
	s_nop 0
	global_load_lds_dwordx4 v[34:35], off
	s_waitcnt vmcnt(6)
	s_barrier
	s_setprio 1
	v_mfma_f32_16x16x32_f16 v[40:43], v[222:225], v[138:141], v[54:57]
	v_mfma_f32_16x16x32_f16 v[54:57], v[230:233], v[138:141], v[82:85]
	v_mfma_f32_16x16x32_f16 v[82:85], v[222:225], v[194:197], v[130:133]
	v_mfma_f32_16x16x32_f16 v[130:133], v[230:233], v[194:197], v[142:145]
	v_mfma_f32_16x16x32_f16 v[138:141], v[222:225], v[202:205], v[146:149]
	v_mfma_f32_16x16x32_f16 v[142:145], v[230:233], v[202:205], v[150:153]
	v_mfma_f32_16x16x32_f16 v[118:121], v[222:225], v[210:213], v[118:121]
	v_mfma_f32_16x16x32_f16 v[122:125], v[230:233], v[210:213], v[122:125]
	v_mfma_f32_16x16x32_f16 v[82:85], v[226:229], v[198:201], v[82:85]
	v_mfma_f32_16x16x32_f16 v[130:133], v[234:237], v[198:201], v[130:133]
	v_mfma_f32_16x16x32_f16 v[138:141], v[226:229], v[206:209], v[138:141]
	v_mfma_f32_16x16x32_f16 v[142:145], v[234:237], v[206:209], v[142:145]
	v_mfma_f32_16x16x32_f16 v[118:121], v[226:229], v[214:217], v[118:121]
	v_mfma_f32_16x16x32_f16 v[122:125], v[234:237], v[214:217], v[122:125]
	v_mfma_f32_16x16x32_f16 v[40:43], v[226:229], v[190:193], v[40:43]
	v_mfma_f32_16x16x32_f16 v[54:57], v[234:237], v[190:193], v[54:57]
	s_setprio 0
	s_barrier
	ds_read_b128 v[146:149], v10
	ds_read_b128 v[150:153], v11
	ds_read_b128 v[154:157], v12
	ds_read_b128 v[158:161], v13
	v_readfirstlane_b32 s15, v44
	v_lshl_add_u64 v[34:35], v[18:19], 0, s[0:1]
	s_mov_b32 m0, s15
	ds_read_b128 v[162:165], v1 offset:32768
	ds_read_b128 v[166:169], v1 offset:33792
	ds_read_b128 v[190:193], v1 offset:34816
	ds_read_b128 v[194:197], v1 offset:35840
	ds_read_b128 v[198:201], v1 offset:36864
	ds_read_b128 v[202:205], v1 offset:37888
	ds_read_b128 v[206:209], v1 offset:38912
	ds_read_b128 v[210:213], v1 offset:39936
	global_load_lds_dwordx4 v[34:35], off
	v_lshl_add_u64 v[34:35], v[20:21], 0, s[0:1]
	v_readfirstlane_b32 s0, v45
	s_mov_b32 m0, s0
	s_nop 0
	global_load_lds_dwordx4 v[34:35], off
	s_waitcnt lgkmcnt(8)
	s_barrier
	s_waitcnt lgkmcnt(0)
	s_setprio 1
	s_waitcnt lgkmcnt(0)
	v_mfma_f32_16x16x32_f16 v[86:89], v[146:149], v[162:165], v[86:89]
	v_mfma_f32_16x16x32_f16 v[90:93], v[154:157], v[162:165], v[90:93]
	v_mfma_f32_16x16x32_f16 v[94:97], v[146:149], v[190:193], v[94:97]
	v_mfma_f32_16x16x32_f16 v[98:101], v[154:157], v[190:193], v[98:101]
	v_mfma_f32_16x16x32_f16 v[102:105], v[146:149], v[198:201], v[102:105]
	v_mfma_f32_16x16x32_f16 v[106:109], v[154:157], v[198:201], v[106:109]
	v_mfma_f32_16x16x32_f16 v[110:113], v[146:149], v[206:209], v[110:113]
	v_mfma_f32_16x16x32_f16 v[86:89], v[150:153], v[166:169], v[86:89]
	v_mfma_f32_16x16x32_f16 v[90:93], v[158:161], v[166:169], v[90:93]
	v_mfma_f32_16x16x32_f16 v[94:97], v[150:153], v[194:197], v[94:97]
	v_mfma_f32_16x16x32_f16 v[98:101], v[158:161], v[194:197], v[98:101]
	v_mfma_f32_16x16x32_f16 v[102:105], v[150:153], v[202:205], v[102:105]
	v_mfma_f32_16x16x32_f16 v[106:109], v[158:161], v[202:205], v[106:109]
	v_mfma_f32_16x16x32_f16 v[110:113], v[150:153], v[210:213], v[110:113]
	v_mfma_f32_16x16x32_f16 v[114:117], v[154:157], v[206:209], v[114:117]
	v_mfma_f32_16x16x32_f16 v[114:117], v[158:161], v[210:213], v[114:117]
	s_setprio 0
	s_barrier
	s_mov_b64 s[0:1], 0x380
	s_mov_b32 m0, s10
	v_lshl_add_u64 v[30:31], v[30:31], 0, s[0:1]
	ds_read_b128 v[214:217], v14
	ds_read_b128 v[218:221], v15
	ds_read_b128 v[222:225], v16
	ds_read_b128 v[226:229], v17
	global_load_lds_dwordx4 v[30:31], off
	v_lshl_add_u64 v[30:31], v[32:33], 0, s[0:1]
	s_mov_b32 m0, s2
	s_nop 0
	global_load_lds_dwordx4 v[30:31], off
	s_barrier
	s_waitcnt lgkmcnt(0)
	s_setprio 1
	s_waitcnt lgkmcnt(0)
	v_mfma_f32_16x16x32_f16 v[30:33], v[214:217], v[162:165], v[36:39]
	v_mfma_f32_16x16x32_f16 v[34:37], v[222:225], v[162:165], v[58:61]
	v_mfma_f32_16x16x32_f16 v[58:61], v[214:217], v[190:193], v[134:137]
	v_mfma_f32_16x16x32_f16 v[62:65], v[222:225], v[190:193], v[62:65]
	v_mfma_f32_16x16x32_f16 v[66:69], v[214:217], v[198:201], v[66:69]
	v_mfma_f32_16x16x32_f16 v[70:73], v[222:225], v[198:201], v[70:73]
	v_mfma_f32_16x16x32_f16 v[74:77], v[214:217], v[206:209], v[74:77]
	v_mfma_f32_16x16x32_f16 v[78:81], v[222:225], v[206:209], v[78:81]
	v_mfma_f32_16x16x32_f16 v[34:37], v[226:229], v[166:169], v[34:37]
	v_mfma_f32_16x16x32_f16 v[58:61], v[218:221], v[194:197], v[58:61]
	v_mfma_f32_16x16x32_f16 v[62:65], v[226:229], v[194:197], v[62:65]
	v_mfma_f32_16x16x32_f16 v[66:69], v[218:221], v[202:205], v[66:69]
	v_mfma_f32_16x16x32_f16 v[70:73], v[226:229], v[202:205], v[70:73]
	v_mfma_f32_16x16x32_f16 v[74:77], v[218:221], v[210:213], v[74:77]
	v_mfma_f32_16x16x32_f16 v[78:81], v[226:229], v[210:213], v[78:81]
	v_mfma_f32_16x16x32_f16 v[30:33], v[218:221], v[166:169], v[30:33]
	s_setprio 0
	s_mov_b32 m0, s11
	v_lshl_add_u64 v[26:27], v[26:27], 0, s[0:1]
	s_barrier
	ds_read_b128 v[134:137], v1 offset:49152
	ds_read_b128 v[162:165], v1 offset:50176
	ds_read_b128 v[166:169], v1 offset:51200
	ds_read_b128 v[190:193], v1 offset:52224
	ds_read_b128 v[194:197], v1 offset:53248
	ds_read_b128 v[198:201], v1 offset:54272
	ds_read_b128 v[202:205], v1 offset:55296
	ds_read_b128 v[206:209], v1 offset:56320
	global_load_lds_dwordx4 v[26:27], off
	v_lshl_add_u64 v[26:27], v[28:29], 0, s[0:1]
	s_mov_b32 m0, s3
	s_nop 0
	global_load_lds_dwordx4 v[26:27], off
	s_barrier
	s_waitcnt lgkmcnt(0)
	s_setprio 1
	s_waitcnt lgkmcnt(0)
	v_mfma_f32_16x16x32_f16 v[26:29], v[146:149], v[134:137], v[46:49]
	v_mfma_f32_16x16x32_f16 v[126:129], v[146:149], v[202:205], v[126:129]
	v_mfma_f32_16x16x32_f16 v[48:51], v[154:157], v[202:205], v[50:53]
	v_mfma_f32_16x16x32_f16 v[44:47], v[154:157], v[134:137], v[170:173]
	v_mfma_f32_16x16x32_f16 v[170:173], v[146:149], v[166:169], v[174:177]
	v_mfma_f32_16x16x32_f16 v[174:177], v[154:157], v[166:169], v[178:181]
	v_mfma_f32_16x16x32_f16 v[178:181], v[146:149], v[194:197], v[182:185]
	v_mfma_f32_16x16x32_f16 v[182:185], v[154:157], v[194:197], v[186:189]
	v_mfma_f32_16x16x32_f16 v[126:129], v[150:153], v[206:209], v[126:129]
	v_mfma_f32_16x16x32_f16 v[48:51], v[158:161], v[206:209], v[48:51]
	v_mfma_f32_16x16x32_f16 v[26:29], v[150:153], v[162:165], v[26:29]
	v_mfma_f32_16x16x32_f16 v[44:47], v[158:161], v[162:165], v[44:47]
	v_mfma_f32_16x16x32_f16 v[170:173], v[150:153], v[190:193], v[170:173]
	v_mfma_f32_16x16x32_f16 v[174:177], v[158:161], v[190:193], v[174:177]
	v_mfma_f32_16x16x32_f16 v[178:181], v[150:153], v[198:201], v[178:181]
	v_mfma_f32_16x16x32_f16 v[182:185], v[158:161], v[198:201], v[182:185]
	s_setprio 0
	s_barrier
	s_mov_b32 m0, s5
	v_lshl_add_u64 v[22:23], v[22:23], 0, s[0:1]
	global_load_lds_dwordx4 v[22:23], off
	v_lshl_add_u64 v[22:23], v[24:25], 0, s[0:1]
	s_mov_b32 m0, s4
	s_nop 0
	global_load_lds_dwordx4 v[22:23], off
	s_waitcnt vmcnt(6)
	s_barrier
	s_setprio 1
	v_mfma_f32_16x16x32_f16 v[22:25], v[214:217], v[134:137], v[40:43]
	v_mfma_f32_16x16x32_f16 v[38:41], v[222:225], v[134:137], v[54:57]
	v_mfma_f32_16x16x32_f16 v[52:55], v[214:217], v[166:169], v[82:85]
	v_mfma_f32_16x16x32_f16 v[82:85], v[222:225], v[166:169], v[130:133]
	v_mfma_f32_16x16x32_f16 v[130:133], v[214:217], v[194:197], v[138:141]
	v_mfma_f32_16x16x32_f16 v[134:137], v[222:225], v[194:197], v[142:145]
	v_mfma_f32_16x16x32_f16 v[118:121], v[214:217], v[202:205], v[118:121]
	v_mfma_f32_16x16x32_f16 v[122:125], v[222:225], v[202:205], v[122:125]
	v_mfma_f32_16x16x32_f16 v[52:55], v[218:221], v[190:193], v[52:55]
	v_mfma_f32_16x16x32_f16 v[82:85], v[226:229], v[190:193], v[82:85]
	v_mfma_f32_16x16x32_f16 v[130:133], v[218:221], v[198:201], v[130:133]
	v_mfma_f32_16x16x32_f16 v[134:137], v[226:229], v[198:201], v[134:137]
	v_mfma_f32_16x16x32_f16 v[118:121], v[218:221], v[206:209], v[118:121]
	v_mfma_f32_16x16x32_f16 v[122:125], v[226:229], v[206:209], v[122:125]
	v_mfma_f32_16x16x32_f16 v[22:25], v[218:221], v[162:165], v[22:25]
	v_mfma_f32_16x16x32_f16 v[38:41], v[226:229], v[162:165], v[38:41]
	s_setprio 0
	s_mov_b32 m0, s14
	v_lshl_add_u64 v[18:19], v[18:19], 0, s[0:1]
	s_barrier
	ds_read_b128 v[138:141], v2
	ds_read_b128 v[142:145], v3
	ds_read_b128 v[146:149], v4
	ds_read_b128 v[2:5], v5
	global_load_lds_dwordx4 v[18:19], off
	v_lshl_add_u64 v[18:19], v[20:21], 0, s[0:1]
	s_mov_b32 m0, s7
	s_nop 0
	global_load_lds_dwordx4 v[18:19], off
	ds_read_b128 v[18:21], v1
	ds_read_b128 v[150:153], v1 offset:1024
	ds_read_b128 v[154:157], v1 offset:2048
	ds_read_b128 v[158:161], v1 offset:3072
	ds_read_b128 v[162:165], v1 offset:4096
	ds_read_b128 v[166:169], v1 offset:5120
	ds_read_b128 v[186:189], v1 offset:6144
	ds_read_b128 v[190:193], v1 offset:7168
	s_barrier
	s_waitcnt lgkmcnt(0)
	s_setprio 1
	s_waitcnt lgkmcnt(0)
	v_mfma_f32_16x16x32_f16 v[86:89], v[138:141], v[18:21], v[86:89]
	v_mfma_f32_16x16x32_f16 v[90:93], v[146:149], v[18:21], v[90:93]
	v_mfma_f32_16x16x32_f16 v[94:97], v[138:141], v[154:157], v[94:97]
	v_mfma_f32_16x16x32_f16 v[98:101], v[146:149], v[154:157], v[98:101]
	v_mfma_f32_16x16x32_f16 v[102:105], v[138:141], v[162:165], v[102:105]
	v_mfma_f32_16x16x32_f16 v[106:109], v[146:149], v[162:165], v[106:109]
	v_mfma_f32_16x16x32_f16 v[110:113], v[138:141], v[186:189], v[110:113]
	v_mfma_f32_16x16x32_f16 v[86:89], v[142:145], v[150:153], v[86:89]
	v_mfma_f32_16x16x32_f16 v[90:93], v[2:5], v[150:153], v[90:93]
	v_mfma_f32_16x16x32_f16 v[94:97], v[142:145], v[158:161], v[94:97]
	v_mfma_f32_16x16x32_f16 v[98:101], v[2:5], v[158:161], v[98:101]
	v_mfma_f32_16x16x32_f16 v[102:105], v[142:145], v[166:169], v[102:105]
	v_mfma_f32_16x16x32_f16 v[106:109], v[2:5], v[166:169], v[106:109]
	v_mfma_f32_16x16x32_f16 v[110:113], v[142:145], v[190:193], v[110:113]
	v_mfma_f32_16x16x32_f16 v[114:117], v[146:149], v[186:189], v[114:117]
	v_mfma_f32_16x16x32_f16 v[114:117], v[2:5], v[190:193], v[114:117]
	s_setprio 0
	s_barrier
	ds_read_b128 v[194:197], v6
	ds_read_b128 v[198:201], v7
	ds_read_b128 v[202:205], v8
	ds_read_b128 v[6:9], v9
	s_barrier
	s_waitcnt lgkmcnt(0)
	s_setprio 1
	s_waitcnt lgkmcnt(0)
	v_mfma_f32_16x16x32_f16 v[30:33], v[194:197], v[18:21], v[30:33]
	v_mfma_f32_16x16x32_f16 v[18:21], v[202:205], v[18:21], v[34:37]
	v_mfma_f32_16x16x32_f16 v[34:37], v[194:197], v[154:157], v[58:61]
	v_mfma_f32_16x16x32_f16 v[56:59], v[202:205], v[154:157], v[62:65]
	v_mfma_f32_16x16x32_f16 v[60:63], v[194:197], v[162:165], v[66:69]
	v_mfma_f32_16x16x32_f16 v[64:67], v[202:205], v[162:165], v[70:73]
	v_mfma_f32_16x16x32_f16 v[68:71], v[194:197], v[186:189], v[74:77]
	v_mfma_f32_16x16x32_f16 v[72:75], v[202:205], v[186:189], v[78:81]
	v_mfma_f32_16x16x32_f16 v[34:37], v[198:201], v[158:161], v[34:37]
	v_mfma_f32_16x16x32_f16 v[56:59], v[6:9], v[158:161], v[56:59]
	v_mfma_f32_16x16x32_f16 v[60:63], v[198:201], v[166:169], v[60:63]
	v_mfma_f32_16x16x32_f16 v[64:67], v[6:9], v[166:169], v[64:67]
	v_mfma_f32_16x16x32_f16 v[68:71], v[198:201], v[190:193], v[68:71]
	v_mfma_f32_16x16x32_f16 v[72:75], v[6:9], v[190:193], v[72:75]
	v_mfma_f32_16x16x32_f16 v[30:33], v[198:201], v[150:153], v[30:33]
	v_mfma_f32_16x16x32_f16 v[18:21], v[6:9], v[150:153], v[18:21]
	s_setprio 0
	s_barrier
	ds_read_b128 v[76:79], v1 offset:16384
	ds_read_b128 v[150:153], v1 offset:17408
	ds_read_b128 v[154:157], v1 offset:18432
	ds_read_b128 v[158:161], v1 offset:19456
	ds_read_b128 v[162:165], v1 offset:20480
	ds_read_b128 v[166:169], v1 offset:21504
	ds_read_b128 v[186:189], v1 offset:22528
	ds_read_b128 v[190:193], v1 offset:23552
	s_waitcnt vmcnt(4)
	s_barrier
	s_waitcnt lgkmcnt(0)
	s_setprio 1
	s_waitcnt lgkmcnt(0)
	v_mfma_f32_16x16x32_f16 v[42:45], v[146:149], v[76:79], v[44:47]
	v_mfma_f32_16x16x32_f16 v[174:177], v[146:149], v[154:157], v[174:177]
	v_mfma_f32_16x16x32_f16 v[182:185], v[146:149], v[162:165], v[182:185]
	v_mfma_f32_16x16x32_f16 v[46:49], v[146:149], v[186:189], v[48:51]
	v_mfma_f32_16x16x32_f16 v[26:29], v[138:141], v[76:79], v[26:29]
	v_mfma_f32_16x16x32_f16 v[42:45], v[2:5], v[150:153], v[42:45]
	v_mfma_f32_16x16x32_f16 v[170:173], v[138:141], v[154:157], v[170:173]
	v_mfma_f32_16x16x32_f16 v[174:177], v[2:5], v[158:161], v[174:177]
	v_mfma_f32_16x16x32_f16 v[178:181], v[138:141], v[162:165], v[178:181]
	v_mfma_f32_16x16x32_f16 v[182:185], v[2:5], v[166:169], v[182:185]
	v_mfma_f32_16x16x32_f16 v[126:129], v[138:141], v[186:189], v[126:129]
	v_mfma_f32_16x16x32_f16 v[2:5], v[2:5], v[190:193], v[46:49]
	v_mfma_f32_16x16x32_f16 v[26:29], v[142:145], v[150:153], v[26:29]
	v_mfma_f32_16x16x32_f16 v[170:173], v[142:145], v[158:161], v[170:173]
	v_mfma_f32_16x16x32_f16 v[178:181], v[142:145], v[166:169], v[178:181]
	v_mfma_f32_16x16x32_f16 v[206:209], v[142:145], v[190:193], v[126:129]
	s_setprio 0
	s_setprio 1
	v_mfma_f32_16x16x32_f16 v[46:49], v[194:197], v[154:157], v[52:55]
	v_mfma_f32_16x16x32_f16 v[50:53], v[202:205], v[154:157], v[82:85]
	v_mfma_f32_16x16x32_f16 v[210:213], v[6:9], v[158:161], v[50:53]
	v_mfma_f32_16x16x32_f16 v[50:53], v[194:197], v[162:165], v[130:133]
	v_mfma_f32_16x16x32_f16 v[214:217], v[198:201], v[166:169], v[50:53]
	v_mfma_f32_16x16x32_f16 v[50:53], v[202:205], v[162:165], v[134:137]
	v_mfma_f32_16x16x32_f16 v[166:169], v[6:9], v[166:169], v[50:53]
	v_mfma_f32_16x16x32_f16 v[50:53], v[194:197], v[186:189], v[118:121]
	v_mfma_f32_16x16x32_f16 v[22:25], v[194:197], v[76:79], v[22:25]
	v_mfma_f32_16x16x32_f16 v[38:41], v[202:205], v[76:79], v[38:41]
	v_mfma_f32_16x16x32_f16 v[194:197], v[198:201], v[190:193], v[50:53]
	v_mfma_f32_16x16x32_f16 v[50:53], v[202:205], v[186:189], v[122:125]
	v_mfma_f32_16x16x32_f16 v[22:25], v[198:201], v[150:153], v[22:25]
	v_mfma_f32_16x16x32_f16 v[38:41], v[6:9], v[150:153], v[38:41]
	v_mfma_f32_16x16x32_f16 v[46:49], v[198:201], v[158:161], v[46:49]
	v_mfma_f32_16x16x32_f16 v[186:189], v[6:9], v[190:193], v[50:53]
	s_setprio 0
	s_barrier
	ds_read_b128 v[6:9], v10
	ds_read_b128 v[82:85], v11
	ds_read_b128 v[190:193], v12
	ds_read_b128 v[10:13], v13
	ds_read_b128 v[50:53], v1 offset:32768
	ds_read_b128 v[76:79], v1 offset:33792
	ds_read_b128 v[118:121], v1 offset:34816
	ds_read_b128 v[126:129], v1 offset:35840
	ds_read_b128 v[198:201], v1 offset:36864
	ds_read_b128 v[202:205], v1 offset:37888
	ds_read_b128 v[218:221], v1 offset:38912
	ds_read_b128 v[222:225], v1 offset:39936
	s_waitcnt vmcnt(2)
	s_barrier
	s_waitcnt lgkmcnt(0)
	s_setprio 1
	s_waitcnt lgkmcnt(0)
	v_mfma_f32_16x16x32_f16 v[86:89], v[6:9], v[50:53], v[86:89]
	v_mfma_f32_16x16x32_f16 v[162:165], v[82:85], v[76:79], v[86:89]
	v_mfma_f32_16x16x32_f16 v[86:89], v[190:193], v[50:53], v[90:93]
	v_mfma_f32_16x16x32_f16 v[154:157], v[10:13], v[76:79], v[86:89]
	v_mfma_f32_16x16x32_f16 v[86:89], v[6:9], v[118:121], v[94:97]
	v_mfma_f32_16x16x32_f16 v[146:149], v[82:85], v[126:129], v[86:89]
	v_mfma_f32_16x16x32_f16 v[86:89], v[190:193], v[118:121], v[98:101]
	v_mfma_f32_16x16x32_f16 v[138:141], v[10:13], v[126:129], v[86:89]
	v_mfma_f32_16x16x32_f16 v[86:89], v[6:9], v[198:201], v[102:105]
	v_mfma_f32_16x16x32_f16 v[130:133], v[82:85], v[202:205], v[86:89]
	v_mfma_f32_16x16x32_f16 v[86:89], v[190:193], v[198:201], v[106:109]
	v_mfma_f32_16x16x32_f16 v[122:125], v[10:13], v[202:205], v[86:89]
	v_mfma_f32_16x16x32_f16 v[86:89], v[6:9], v[218:221], v[110:113]
	v_mfma_f32_16x16x32_f16 v[110:113], v[82:85], v[222:225], v[86:89]
	v_mfma_f32_16x16x32_f16 v[86:89], v[190:193], v[218:221], v[114:117]
	v_mfma_f32_16x16x32_f16 v[102:105], v[10:13], v[222:225], v[86:89]
	s_setprio 0
	s_barrier
	ds_read_b128 v[114:117], v14
	ds_read_b128 v[226:229], v15
	ds_read_b128 v[230:233], v16
	ds_read_b128 v[234:237], v17
	s_waitcnt vmcnt(0)
	s_barrier
	s_waitcnt lgkmcnt(0)
	s_setprio 1
	s_waitcnt lgkmcnt(0)
	v_mfma_f32_16x16x32_f16 v[14:17], v[114:117], v[50:53], v[30:33]
	v_mfma_f32_16x16x32_f16 v[158:161], v[226:229], v[76:79], v[14:17]
	v_mfma_f32_16x16x32_f16 v[14:17], v[230:233], v[50:53], v[18:21]
	v_mfma_f32_16x16x32_f16 v[150:153], v[234:237], v[76:79], v[14:17]
	v_mfma_f32_16x16x32_f16 v[14:17], v[114:117], v[118:121], v[34:37]
	v_mfma_f32_16x16x32_f16 v[142:145], v[226:229], v[126:129], v[14:17]
	v_mfma_f32_16x16x32_f16 v[14:17], v[230:233], v[118:121], v[56:59]
	v_mfma_f32_16x16x32_f16 v[134:137], v[234:237], v[126:129], v[14:17]
	v_mfma_f32_16x16x32_f16 v[14:17], v[114:117], v[198:201], v[60:63]
	v_mfma_f32_16x16x32_f16 v[126:129], v[226:229], v[202:205], v[14:17]
	v_mfma_f32_16x16x32_f16 v[14:17], v[230:233], v[198:201], v[64:67]
	v_mfma_f32_16x16x32_f16 v[118:121], v[234:237], v[202:205], v[14:17]
	v_mfma_f32_16x16x32_f16 v[14:17], v[114:117], v[218:221], v[68:71]
	v_mfma_f32_16x16x32_f16 v[106:109], v[226:229], v[222:225], v[14:17]
	v_mfma_f32_16x16x32_f16 v[14:17], v[230:233], v[218:221], v[72:75]
	v_mfma_f32_16x16x32_f16 v[98:101], v[234:237], v[222:225], v[14:17]
	s_setprio 0
	s_barrier
	ds_read_b128 v[18:21], v1 offset:49152
	ds_read_b128 v[30:33], v1 offset:50176
	ds_read_b128 v[34:37], v1 offset:51200
	ds_read_b128 v[54:57], v1 offset:52224
	ds_read_b128 v[58:61], v1 offset:53248
	ds_read_b128 v[198:201], v1 offset:54272
	ds_read_b128 v[202:205], v1 offset:55296
	ds_read_b128 v[218:221], v1 offset:56320
	s_barrier
	s_waitcnt lgkmcnt(0)
	s_setprio 1
	s_waitcnt lgkmcnt(0)
	v_mfma_f32_16x16x32_f16 v[14:17], v[6:9], v[18:21], v[26:29]
	v_mfma_f32_16x16x32_f16 v[94:97], v[82:85], v[30:33], v[14:17]
	v_mfma_f32_16x16x32_f16 v[14:17], v[190:193], v[18:21], v[42:45]
	v_mfma_f32_16x16x32_f16 v[86:89], v[10:13], v[30:33], v[14:17]
	v_mfma_f32_16x16x32_f16 v[14:17], v[6:9], v[34:37], v[170:173]
	v_mfma_f32_16x16x32_f16 v[78:81], v[82:85], v[54:57], v[14:17]
	v_mfma_f32_16x16x32_f16 v[14:17], v[190:193], v[34:37], v[174:177]
	v_mfma_f32_16x16x32_f16 v[70:73], v[10:13], v[54:57], v[14:17]
	v_mfma_f32_16x16x32_f16 v[14:17], v[6:9], v[58:61], v[178:181]
	v_mfma_f32_16x16x32_f16 v[62:65], v[82:85], v[198:201], v[14:17]
	v_mfma_f32_16x16x32_f16 v[14:17], v[190:193], v[58:61], v[182:185]
	v_mfma_f32_16x16x32_f16 v[6:9], v[6:9], v[202:205], v[206:209]
	v_mfma_f32_16x16x32_f16 v[2:5], v[190:193], v[202:205], v[2:5]
	v_mfma_f32_16x16x32_f16 v[50:53], v[10:13], v[198:201], v[14:17]
	v_mfma_f32_16x16x32_f16 v[14:17], v[82:85], v[218:221], v[6:9]
	v_mfma_f32_16x16x32_f16 v[10:13], v[10:13], v[218:221], v[2:5]
	s_setprio 0
	s_setprio 1
	v_mfma_f32_16x16x32_f16 v[2:5], v[114:117], v[18:21], v[22:25]
	v_mfma_f32_16x16x32_f16 v[6:9], v[230:233], v[18:21], v[38:41]
	v_mfma_f32_16x16x32_f16 v[90:93], v[226:229], v[30:33], v[2:5]
	v_mfma_f32_16x16x32_f16 v[2:5], v[114:117], v[34:37], v[46:49]
	v_mfma_f32_16x16x32_f16 v[82:85], v[234:237], v[30:33], v[6:9]
	v_mfma_f32_16x16x32_f16 v[6:9], v[230:233], v[34:37], v[210:213]
	v_mfma_f32_16x16x32_f16 v[74:77], v[226:229], v[54:57], v[2:5]
	v_mfma_f32_16x16x32_f16 v[2:5], v[114:117], v[58:61], v[214:217]
	v_mfma_f32_16x16x32_f16 v[66:69], v[234:237], v[54:57], v[6:9]
	v_mfma_f32_16x16x32_f16 v[6:9], v[230:233], v[58:61], v[166:169]
	v_mfma_f32_16x16x32_f16 v[58:61], v[226:229], v[198:201], v[2:5]
	v_mfma_f32_16x16x32_f16 v[2:5], v[114:117], v[202:205], v[194:197]
	v_mfma_f32_16x16x32_f16 v[34:37], v[234:237], v[198:201], v[6:9]
	v_mfma_f32_16x16x32_f16 v[6:9], v[226:229], v[218:221], v[2:5]
	v_mfma_f32_16x16x32_f16 v[2:5], v[230:233], v[202:205], v[186:189]
	v_mfma_f32_16x16x32_f16 v[2:5], v[234:237], v[218:221], v[2:5]
	s_setprio 0
	s_barrier
	s_add_i32 s0, 0, 0x20800
	v_bfe_u32 v166, v0, 4, 2
	v_bfe_u32 v1, v0, 6, 2
	v_lshlrev_b32_e32 v18, 5, v166
	v_lshl_or_b32 v18, v1, 7, v18
	v_add_u32_e32 v19, s0, v18
	s_add_i32 s1, 0, 0x20c00
	v_add_u32_e32 v20, s1, v18
	ds_read_b128 v[54:57], v19
	ds_read_b128 v[46:49], v20
	v_or_b32_e32 v19, 16, v18
	v_add_u32_e32 v20, s0, v19
	v_add_u32_e32 v19, s1, v19
	ds_read_b128 v[42:45], v20
	ds_read_b128 v[38:41], v19
	v_or_b32_e32 v19, 0x200, v18
	v_add_u32_e32 v20, s0, v19
	v_add_u32_e32 v19, s1, v19
	v_or_b32_e32 v18, 0x210, v18
	ds_read_b128 v[30:33], v20
	ds_read_b128 v[26:29], v19
	v_add_u32_e32 v19, s0, v18
	v_and_b32_e32 v114, 15, v0
	v_ashrrev_i32_e32 v0, 2, v0
	s_movk_i32 s0, 0xffc0
	v_and_or_b32 v169, v0, s0, v114
	s_add_i32 s0, 0, 0x20000
	v_add_u32_e32 v18, s1, v18
	v_lshl_add_u32 v168, v169, 3, s0
	ds_read_b128 v[22:25], v19
	ds_read_b128 v[18:21], v18
	s_waitcnt vmcnt(0)
	ds_read2st64_b64 v[114:117], v168 offset1:2
	v_lshlrev_b32_e32 v0, 5, v1
	v_lshlrev_b32_e32 v1, 3, v166
	v_or3_b32 v166, v0, v1, s13
	v_add_u32_e32 v167, s12, v169
	s_waitcnt lgkmcnt(0)
	v_fma_f32 v154, -v114, v42, v154
	v_fma_f32 v154, v115, v154, v38
	v_fma_f32 v1, -v114, v54, v162
	v_fma_f32 v162, -v114, v55, v163
	v_fma_f32 v163, -v114, v56, v164
	v_fma_f32 v164, -v114, v57, v165
	v_max_f32_e32 v165, 0, v154
	v_fma_f32 v154, -v114, v43, v155
	v_fma_f32 v154, v115, v154, v39
	v_max_f32_e32 v170, 0, v154
	v_fma_f32 v154, -v114, v44, v156
	v_fma_f32 v154, v115, v154, v40
	v_max_f32_e32 v156, 0, v154
	v_fma_f32 v154, -v114, v45, v157
	v_fma_f32 v1, v115, v1, v46
	v_fma_f32 v162, v115, v162, v47
	v_fma_f32 v163, v115, v163, v48
	v_fma_f32 v164, v115, v164, v49
	v_fma_f32 v154, v115, v154, v41
	v_mul_lo_u32 v0, v167, s6
	v_max_f32_e32 v1, 0, v1
	v_max_f32_e32 v162, 0, v162
	v_max_f32_e32 v163, 0, v163
	v_max_f32_e32 v164, 0, v164
	v_max_f32_e32 v157, 0, v154
	s_and_b32 s9, s9, 0xffff
	s_mov_b32 s11, 0x20000
	s_mov_b32 s10, 0x7ffffff0
	v_cvt_pk_f16_f32 v155, v163, v164
	v_cvt_pk_f16_f32 v154, v1, v162
	v_cvt_pk_f16_f32 v157, v156, v157
	v_cvt_pk_f16_f32 v156, v165, v170
	v_add_lshl_u32 v0, v166, v0, 1
	buffer_store_dwordx4 v[154:157], v0, s[8:11], 0 offen sc1
	v_fma_f32 v1, -v114, v30, v158
	v_fma_f32 v150, -v114, v22, v150
	v_fma_f32 v154, -v114, v31, v159
	v_fma_f32 v155, -v114, v32, v160
	v_fma_f32 v156, -v114, v33, v161
	v_fma_f32 v151, -v114, v23, v151
	v_fma_f32 v152, -v114, v24, v152
	v_fma_f32 v114, -v114, v25, v153
	v_fma_f32 v1, v115, v1, v26
	v_fma_f32 v154, v115, v154, v27
	v_fma_f32 v155, v115, v155, v28
	v_fma_f32 v156, v115, v156, v29
	v_fma_f32 v150, v115, v150, v18
	v_fma_f32 v151, v115, v151, v19
	v_fma_f32 v152, v115, v152, v20
	v_fma_f32 v114, v115, v114, v21
	v_max_f32_e32 v1, 0, v1
	v_max_f32_e32 v154, 0, v154
	v_max_f32_e32 v155, 0, v155
	v_max_f32_e32 v156, 0, v156
	v_max_f32_e32 v150, 0, v150
	v_max_f32_e32 v151, 0, v151
	v_max_f32_e32 v152, 0, v152
	v_max_f32_e32 v114, 0, v114
	v_cvt_pk_f16_f32 v153, v152, v114
	v_cvt_pk_f16_f32 v152, v150, v151
	v_cvt_pk_f16_f32 v151, v155, v156
	v_cvt_pk_f16_f32 v150, v1, v154
	buffer_store_dwordx4 v[150:153], v0, s[8:11], 0 offen offset:256 sc1
	v_or_b32_e32 v0, 16, v169
	v_add_u32_e32 v114, s12, v0
	v_lshl_add_u32 v0, v0, 3, s0
	ds_read_b64 v[0:1], v0
	v_or_b32_e32 v155, 32, v169
	v_or_b32_e32 v156, 48, v169
	v_mul_lo_u32 v154, v114, s6
	v_lshl_add_u32 v114, v155, 3, s0
	s_waitcnt lgkmcnt(0)
	v_fma_f32 v146, -v0, v54, v146
	v_fma_f32 v147, -v0, v55, v147
	v_fma_f32 v148, -v0, v56, v148
	v_fma_f32 v149, -v0, v57, v149
	v_fma_f32 v138, -v0, v42, v138
	v_fma_f32 v139, -v0, v43, v139
	v_fma_f32 v140, -v0, v44, v140
	v_fma_f32 v141, -v0, v45, v141
	v_fma_f32 v146, v1, v146, v46
	v_fma_f32 v147, v1, v147, v47
	v_fma_f32 v148, v1, v148, v48
	v_fma_f32 v149, v1, v149, v49
	v_fma_f32 v138, v1, v138, v38
	v_fma_f32 v139, v1, v139, v39
	v_fma_f32 v140, v1, v140, v40
	v_fma_f32 v141, v1, v141, v41
	v_lshl_add_u32 v115, v156, 3, s0
	v_max_f32_e32 v146, 0, v146
	v_max_f32_e32 v147, 0, v147
	v_max_f32_e32 v148, 0, v148
	v_max_f32_e32 v149, 0, v149
	v_max_f32_e32 v138, 0, v138
	v_max_f32_e32 v139, 0, v139
	v_max_f32_e32 v140, 0, v140
	v_max_f32_e32 v141, 0, v141
	ds_read_b64 v[152:153], v114
	ds_read_b64 v[114:115], v115
	ds_read_b64 v[150:151], v168 offset:1408
	v_cvt_pk_f16_f32 v141, v140, v141
	v_cvt_pk_f16_f32 v140, v138, v139
	v_cvt_pk_f16_f32 v139, v148, v149
	v_cvt_pk_f16_f32 v138, v146, v147
	v_add_lshl_u32 v146, v166, v154, 1
	buffer_store_dwordx4 v[138:141], v146, s[8:11], 0 offen sc1
	v_fma_f32 v134, -v0, v22, v134
	v_fma_f32 v135, -v0, v23, v135
	v_fma_f32 v138, -v0, v30, v142
	v_fma_f32 v139, -v0, v31, v143
	v_fma_f32 v140, -v0, v32, v144
	v_fma_f32 v141, -v0, v33, v145
	v_fma_f32 v136, -v0, v24, v136
	v_fma_f32 v0, -v0, v25, v137
	v_fma_f32 v136, v1, v136, v20
	v_fma_f32 v0, v1, v0, v21
	v_fma_f32 v138, v1, v138, v26
	v_fma_f32 v139, v1, v139, v27
	v_fma_f32 v140, v1, v140, v28
	v_fma_f32 v141, v1, v141, v29
	v_fma_f32 v134, v1, v134, v18
	v_fma_f32 v135, v1, v135, v19
	v_max_f32_e32 v136, 0, v136
	v_max_f32_e32 v0, 0, v0
	s_waitcnt lgkmcnt(2)
	v_fma_f32 v1, -v152, v54, v130
	v_fma_f32 v130, -v152, v55, v131
	v_fma_f32 v131, -v152, v56, v132
	v_fma_f32 v132, -v152, v57, v133
	v_fma_f32 v122, -v152, v42, v122
	v_fma_f32 v123, -v152, v43, v123
	v_fma_f32 v124, -v152, v44, v124
	v_fma_f32 v125, -v152, v45, v125
	v_cvt_pk_f16_f32 v137, v136, v0
	v_add_u32_e32 v0, s12, v155
	v_fma_f32 v1, v153, v1, v46
	v_fma_f32 v130, v153, v130, v47
	v_fma_f32 v131, v153, v131, v48
	v_fma_f32 v132, v153, v132, v49
	v_fma_f32 v122, v153, v122, v38
	v_fma_f32 v123, v153, v123, v39
	v_fma_f32 v124, v153, v124, v40
	v_fma_f32 v125, v153, v125, v41
	v_max_f32_e32 v138, 0, v138
	v_max_f32_e32 v139, 0, v139
	v_max_f32_e32 v140, 0, v140
	v_max_f32_e32 v141, 0, v141
	v_max_f32_e32 v134, 0, v134
	v_max_f32_e32 v135, 0, v135
	v_mul_lo_u32 v0, v0, s6
	v_max_f32_e32 v1, 0, v1
	v_max_f32_e32 v130, 0, v130
	v_max_f32_e32 v131, 0, v131
	v_max_f32_e32 v132, 0, v132
	v_max_f32_e32 v122, 0, v122
	v_max_f32_e32 v123, 0, v123
	v_max_f32_e32 v124, 0, v124
	v_max_f32_e32 v125, 0, v125
	v_cvt_pk_f16_f32 v136, v134, v135
	v_cvt_pk_f16_f32 v135, v140, v141
	v_cvt_pk_f16_f32 v134, v138, v139
	v_cvt_pk_f16_f32 v125, v124, v125
	v_cvt_pk_f16_f32 v124, v122, v123
	v_cvt_pk_f16_f32 v123, v131, v132
	v_cvt_pk_f16_f32 v122, v1, v130
	v_add_lshl_u32 v0, v166, v0, 1
	buffer_store_dwordx4 v[134:137], v146, s[8:11], 0 offen offset:256 sc1
	buffer_store_dwordx4 v[122:125], v0, s[8:11], 0 offen sc1
	v_fma_f32 v1, -v152, v30, v126
	v_fma_f32 v118, -v152, v22, v118
	v_fma_f32 v122, -v152, v31, v127
	v_fma_f32 v123, -v152, v32, v128
	v_fma_f32 v124, -v152, v33, v129
	v_fma_f32 v119, -v152, v23, v119
	v_fma_f32 v120, -v152, v24, v120
	v_fma_f32 v121, -v152, v25, v121
	v_fma_f32 v1, v153, v1, v26
	v_fma_f32 v122, v153, v122, v27
	v_fma_f32 v123, v153, v123, v28
	v_fma_f32 v124, v153, v124, v29
	v_fma_f32 v118, v153, v118, v18
	v_fma_f32 v119, v153, v119, v19
	v_fma_f32 v120, v153, v120, v20
	v_fma_f32 v121, v153, v121, v21
	v_max_f32_e32 v1, 0, v1
	v_max_f32_e32 v122, 0, v122
	v_max_f32_e32 v123, 0, v123
	v_max_f32_e32 v124, 0, v124
	v_max_f32_e32 v118, 0, v118
	v_max_f32_e32 v119, 0, v119
	v_max_f32_e32 v120, 0, v120
	v_max_f32_e32 v121, 0, v121
	v_cvt_pk_f16_f32 v121, v120, v121
	v_cvt_pk_f16_f32 v120, v118, v119
	v_cvt_pk_f16_f32 v119, v123, v124
	v_cvt_pk_f16_f32 v118, v1, v122
	s_waitcnt lgkmcnt(1)
	v_fma_f32 v1, -v114, v54, v110
	v_fma_f32 v110, -v114, v55, v111
	v_fma_f32 v111, -v114, v56, v112
	v_fma_f32 v112, -v114, v57, v113
	v_fma_f32 v102, -v114, v42, v102
	v_fma_f32 v103, -v114, v43, v103
	v_fma_f32 v104, -v114, v44, v104
	v_fma_f32 v105, -v114, v45, v105
	buffer_store_dwordx4 v[118:121], v0, s[8:11], 0 offen offset:256 sc1
	s_and_saveexec_b64 s[24:25], vcc
	s_cbranch_execz .LBB8_8
	s_barrier
.LBB8_8:
	s_or_b64 exec, exec, s[24:25]
	v_add_u32_e32 v0, s12, v156
	v_fma_f32 v1, v115, v1, v46
	v_fma_f32 v110, v115, v110, v47
	v_fma_f32 v111, v115, v111, v48
	v_fma_f32 v112, v115, v112, v49
	v_fma_f32 v102, v115, v102, v38
	v_fma_f32 v103, v115, v103, v39
	v_fma_f32 v104, v115, v104, v40
	v_fma_f32 v105, v115, v105, v41
	v_mul_lo_u32 v0, v0, s6
	v_max_f32_e32 v1, 0, v1
	v_max_f32_e32 v110, 0, v110
	v_max_f32_e32 v111, 0, v111
	v_max_f32_e32 v112, 0, v112
	v_max_f32_e32 v102, 0, v102
	v_max_f32_e32 v103, 0, v103
	v_max_f32_e32 v104, 0, v104
	v_max_f32_e32 v105, 0, v105
	v_cvt_pk_f16_f32 v105, v104, v105
	v_cvt_pk_f16_f32 v104, v102, v103
	v_cvt_pk_f16_f32 v103, v111, v112
	v_cvt_pk_f16_f32 v102, v1, v110
	v_add_lshl_u32 v0, v166, v0, 1
	buffer_store_dwordx4 v[102:105], v0, s[8:11], 0 offen sc1
	v_fma_f32 v1, -v114, v30, v106
	v_fma_f32 v98, -v114, v22, v98
	v_fma_f32 v102, -v114, v31, v107
	v_fma_f32 v103, -v114, v32, v108
	v_fma_f32 v104, -v114, v33, v109
	v_fma_f32 v99, -v114, v23, v99
	v_fma_f32 v100, -v114, v24, v100
	v_fma_f32 v101, -v114, v25, v101
	v_fma_f32 v1, v115, v1, v26
	v_fma_f32 v102, v115, v102, v27
	v_fma_f32 v103, v115, v103, v28
	v_fma_f32 v104, v115, v104, v29
	v_fma_f32 v98, v115, v98, v18
	v_fma_f32 v99, v115, v99, v19
	v_fma_f32 v100, v115, v100, v20
	v_fma_f32 v101, v115, v101, v21
	v_max_f32_e32 v1, 0, v1
	v_max_f32_e32 v102, 0, v102
	v_max_f32_e32 v103, 0, v103
	v_max_f32_e32 v104, 0, v104
	v_max_f32_e32 v98, 0, v98
	v_max_f32_e32 v99, 0, v99
	v_max_f32_e32 v100, 0, v100
	v_max_f32_e32 v101, 0, v101
	v_cvt_pk_f16_f32 v101, v100, v101
	v_cvt_pk_f16_f32 v100, v98, v99
	v_cvt_pk_f16_f32 v99, v103, v104
	v_cvt_pk_f16_f32 v98, v1, v102
	v_fma_f32 v1, -v116, v54, v94
	v_fma_f32 v94, -v116, v55, v95
	v_fma_f32 v95, -v116, v56, v96
	v_fma_f32 v96, -v116, v57, v97
	v_fma_f32 v86, -v116, v42, v86
	v_fma_f32 v87, -v116, v43, v87
	v_fma_f32 v88, -v116, v44, v88
	v_fma_f32 v89, -v116, v45, v89
	buffer_store_dwordx4 v[98:101], v0, s[8:11], 0 offen offset:256 sc1
	v_add_u32_e32 v0, 0x80, v167
	v_fma_f32 v1, v117, v1, v46
	v_fma_f32 v94, v117, v94, v47
	v_fma_f32 v95, v117, v95, v48
	v_fma_f32 v96, v117, v96, v49
	v_fma_f32 v86, v117, v86, v38
	v_fma_f32 v87, v117, v87, v39
	v_fma_f32 v88, v117, v88, v40
	v_fma_f32 v89, v117, v89, v41
	v_mul_lo_u32 v0, v0, s6
	v_max_f32_e32 v1, 0, v1
	v_max_f32_e32 v94, 0, v94
	v_max_f32_e32 v95, 0, v95
	v_max_f32_e32 v96, 0, v96
	v_max_f32_e32 v86, 0, v86
	v_max_f32_e32 v87, 0, v87
	v_max_f32_e32 v88, 0, v88
	v_max_f32_e32 v89, 0, v89
	v_cvt_pk_f16_f32 v89, v88, v89
	v_cvt_pk_f16_f32 v88, v86, v87
	v_cvt_pk_f16_f32 v87, v95, v96
	v_cvt_pk_f16_f32 v86, v1, v94
	v_add_lshl_u32 v0, v166, v0, 1
	buffer_store_dwordx4 v[86:89], v0, s[8:11], 0 offen sc1
	v_fma_f32 v1, -v116, v30, v90
	v_fma_f32 v82, -v116, v22, v82
	v_fma_f32 v86, -v116, v31, v91
	v_fma_f32 v86, v117, v86, v27
	v_max_f32_e32 v90, 0, v86
	v_fma_f32 v86, -v116, v32, v92
	v_fma_f32 v87, -v116, v33, v93
	v_fma_f32 v83, -v116, v23, v83
	v_fma_f32 v84, -v116, v24, v84
	v_fma_f32 v85, -v116, v25, v85
	v_fma_f32 v86, v117, v86, v28
	v_fma_f32 v87, v117, v87, v29
	v_fma_f32 v82, v117, v82, v18
	v_fma_f32 v83, v117, v83, v19
	v_fma_f32 v84, v117, v84, v20
	v_fma_f32 v85, v117, v85, v21
	v_max_f32_e32 v86, 0, v86
	v_max_f32_e32 v87, 0, v87
	v_max_f32_e32 v82, 0, v82
	v_max_f32_e32 v83, 0, v83
	v_max_f32_e32 v84, 0, v84
	v_max_f32_e32 v85, 0, v85
	v_cvt_pk_f16_f32 v85, v84, v85
	v_cvt_pk_f16_f32 v84, v82, v83
	v_cvt_pk_f16_f32 v83, v86, v87
	ds_read2_b64 v[86:89], v168 offset0:144 offset1:160
	v_fma_f32 v1, v117, v1, v26
	v_max_f32_e32 v1, 0, v1
	v_cvt_pk_f16_f32 v82, v1, v90
	buffer_store_dwordx4 v[82:85], v0, s[8:11], 0 offen offset:256 sc1
	s_waitcnt lgkmcnt(0)
	v_fma_f32 v1, -v86, v54, v78
	v_fma_f32 v78, -v86, v55, v79
	v_fma_f32 v79, -v86, v56, v80
	v_fma_f32 v80, -v86, v57, v81
	v_fma_f32 v70, -v86, v42, v70
	v_fma_f32 v71, -v86, v43, v71
	v_fma_f32 v72, -v86, v44, v72
	v_fma_f32 v73, -v86, v45, v73
	v_add_u32_e32 v0, 0x90, v167
	v_fma_f32 v1, v87, v1, v46
	v_fma_f32 v78, v87, v78, v47
	v_fma_f32 v79, v87, v79, v48
	v_fma_f32 v80, v87, v80, v49
	v_fma_f32 v70, v87, v70, v38
	v_fma_f32 v71, v87, v71, v39
	v_fma_f32 v72, v87, v72, v40
	v_fma_f32 v73, v87, v73, v41
	v_mul_lo_u32 v0, v0, s6
	v_max_f32_e32 v1, 0, v1
	v_max_f32_e32 v78, 0, v78
	v_max_f32_e32 v79, 0, v79
	v_max_f32_e32 v80, 0, v80
	v_max_f32_e32 v70, 0, v70
	v_max_f32_e32 v71, 0, v71
	v_max_f32_e32 v72, 0, v72
	v_max_f32_e32 v73, 0, v73
	v_cvt_pk_f16_f32 v73, v72, v73
	v_cvt_pk_f16_f32 v72, v70, v71
	v_cvt_pk_f16_f32 v71, v79, v80
	v_cvt_pk_f16_f32 v70, v1, v78
	v_add_lshl_u32 v0, v166, v0, 1
	buffer_store_dwordx4 v[70:73], v0, s[8:11], 0 offen sc1
	v_fma_f32 v1, -v86, v30, v74
	v_fma_f32 v66, -v86, v22, v66
	v_fma_f32 v70, -v86, v31, v75
	v_fma_f32 v71, -v86, v32, v76
	v_fma_f32 v72, -v86, v33, v77
	v_fma_f32 v67, -v86, v23, v67
	v_fma_f32 v68, -v86, v24, v68
	v_fma_f32 v69, -v86, v25, v69
	v_fma_f32 v1, v87, v1, v26
	v_fma_f32 v70, v87, v70, v27
	v_fma_f32 v71, v87, v71, v28
	v_fma_f32 v72, v87, v72, v29
	v_fma_f32 v66, v87, v66, v18
	v_fma_f32 v67, v87, v67, v19
	v_fma_f32 v68, v87, v68, v20
	v_fma_f32 v69, v87, v69, v21
	v_max_f32_e32 v1, 0, v1
	v_max_f32_e32 v70, 0, v70
	v_max_f32_e32 v71, 0, v71
	v_max_f32_e32 v72, 0, v72
	v_max_f32_e32 v66, 0, v66
	v_max_f32_e32 v67, 0, v67
	v_max_f32_e32 v68, 0, v68
	v_max_f32_e32 v69, 0, v69
	v_cvt_pk_f16_f32 v69, v68, v69
	v_cvt_pk_f16_f32 v68, v66, v67
	v_cvt_pk_f16_f32 v67, v71, v72
	v_cvt_pk_f16_f32 v66, v1, v70
	v_fma_f32 v1, -v88, v54, v62
	v_fma_f32 v62, -v88, v55, v63
	v_fma_f32 v63, -v88, v56, v64
	v_fma_f32 v64, -v88, v57, v65
	v_fma_f32 v50, -v88, v42, v50
	v_fma_f32 v51, -v88, v43, v51
	v_fma_f32 v52, -v88, v44, v52
	v_fma_f32 v53, -v88, v45, v53
	buffer_store_dwordx4 v[66:69], v0, s[8:11], 0 offen offset:256 sc1
	v_add_u32_e32 v0, 0xa0, v167
	v_fma_f32 v1, v89, v1, v46
	v_fma_f32 v62, v89, v62, v47
	v_fma_f32 v63, v89, v63, v48
	v_fma_f32 v64, v89, v64, v49
	v_fma_f32 v50, v89, v50, v38
	v_fma_f32 v51, v89, v51, v39
	v_fma_f32 v52, v89, v52, v40
	v_fma_f32 v53, v89, v53, v41
	v_mul_lo_u32 v0, v0, s6
	v_max_f32_e32 v1, 0, v1
	v_max_f32_e32 v62, 0, v62
	v_max_f32_e32 v63, 0, v63
	v_max_f32_e32 v64, 0, v64
	v_max_f32_e32 v50, 0, v50
	v_max_f32_e32 v51, 0, v51
	v_max_f32_e32 v52, 0, v52
	v_max_f32_e32 v53, 0, v53
	v_cvt_pk_f16_f32 v53, v52, v53
	v_cvt_pk_f16_f32 v52, v50, v51
	v_cvt_pk_f16_f32 v51, v63, v64
	v_cvt_pk_f16_f32 v50, v1, v62
	v_add_lshl_u32 v0, v166, v0, 1
	buffer_store_dwordx4 v[50:53], v0, s[8:11], 0 offen sc1
	v_fma_f32 v1, -v88, v30, v58
	v_fma_f32 v34, -v88, v22, v34
	v_fma_f32 v50, -v88, v31, v59
	v_fma_f32 v35, -v88, v23, v35
	v_fma_f32 v36, -v88, v24, v36
	v_fma_f32 v37, -v88, v25, v37
	v_fma_f32 v1, v89, v1, v26
	v_fma_f32 v50, v89, v50, v27
	v_fma_f32 v34, v89, v34, v18
	v_fma_f32 v35, v89, v35, v19
	v_fma_f32 v36, v89, v36, v20
	v_fma_f32 v37, v89, v37, v21
	v_max_f32_e32 v1, 0, v1
	v_max_f32_e32 v50, 0, v50
	v_fma_f32 v51, -v88, v32, v60
	v_fma_f32 v52, -v88, v33, v61
	v_max_f32_e32 v34, 0, v34
	v_max_f32_e32 v35, 0, v35
	v_max_f32_e32 v36, 0, v36
	v_max_f32_e32 v37, 0, v37
	v_fma_f32 v51, v89, v51, v28
	v_fma_f32 v52, v89, v52, v29
	v_cvt_pk_f16_f32 v37, v36, v37
	v_cvt_pk_f16_f32 v36, v34, v35
	v_cvt_pk_f16_f32 v34, v1, v50
	v_fma_f32 v1, -v150, v54, v14
	v_fma_f32 v14, -v150, v55, v15
	v_fma_f32 v10, -v150, v42, v10
	v_fma_f32 v11, -v150, v43, v11
	v_fma_f32 v12, -v150, v44, v12
	v_fma_f32 v13, -v150, v45, v13
	v_max_f32_e32 v51, 0, v51
	v_max_f32_e32 v52, 0, v52
	v_fma_f32 v1, v151, v1, v46
	v_fma_f32 v14, v151, v14, v47
	v_fma_f32 v10, v151, v10, v38
	v_fma_f32 v11, v151, v11, v39
	v_fma_f32 v12, v151, v12, v40
	v_fmac_f32_e32 v41, v151, v13
	v_cvt_pk_f16_f32 v35, v51, v52
	v_max_f32_e32 v1, 0, v1
	v_max_f32_e32 v14, 0, v14
	v_max_f32_e32 v10, 0, v10
	v_max_f32_e32 v11, 0, v11
	v_max_f32_e32 v12, 0, v12
	v_max_f32_e32 v13, 0, v41
	buffer_store_dwordx4 v[34:37], v0, s[8:11], 0 offen offset:256 sc1
	v_add_u32_e32 v0, 0xb0, v167
	v_cvt_pk_f16_f32 v13, v12, v13
	v_cvt_pk_f16_f32 v12, v10, v11
	v_cvt_pk_f16_f32 v10, v1, v14
	v_fma_f32 v1, -v150, v31, v7
	v_fma_f32 v3, -v150, v23, v3
	v_mul_lo_u32 v0, v0, s6
	v_fma_f32 v1, v151, v1, v27
	v_fma_f32 v3, v151, v3, v19
	v_fma_f32 v15, -v150, v56, v16
	v_fma_f32 v16, -v150, v57, v17
	v_add_lshl_u32 v14, v166, v0, 1
	v_fma_f32 v0, -v150, v30, v6
	v_max_f32_e32 v6, 0, v1
	v_fma_f32 v1, -v150, v32, v8
	v_fma_f32 v7, -v150, v33, v9
	v_fma_f32 v2, -v150, v22, v2
	v_max_f32_e32 v8, 0, v3
	v_fma_f32 v3, -v150, v24, v4
	v_fma_f32 v4, -v150, v25, v5
	v_fma_f32 v15, v151, v15, v48
	v_fmac_f32_e32 v49, v151, v16
	v_fma_f32 v0, v151, v0, v26
	v_fma_f32 v1, v151, v1, v28
	v_fmac_f32_e32 v29, v151, v7
	v_fma_f32 v2, v151, v2, v18
	v_fma_f32 v3, v151, v3, v20
	v_fmac_f32_e32 v21, v151, v4
	v_max_f32_e32 v15, 0, v15
	v_max_f32_e32 v16, 0, v49
	v_max_f32_e32 v0, 0, v0
	v_max_f32_e32 v1, 0, v1
	v_max_f32_e32 v7, 0, v29
	v_max_f32_e32 v2, 0, v2
	v_max_f32_e32 v3, 0, v3
	v_max_f32_e32 v4, 0, v21
	v_cvt_pk_f16_f32 v11, v15, v16
	v_cvt_pk_f16_f32 v3, v3, v4
	v_cvt_pk_f16_f32 v2, v2, v8
	v_cvt_pk_f16_f32 v1, v1, v7
	v_cvt_pk_f16_f32 v0, v0, v6
	buffer_store_dwordx4 v[10:13], v14, s[8:11], 0 offen sc1
	buffer_store_dwordx4 v[0:3], v14, s[8:11], 0 offen offset:256 sc1
	s_endpgm
